# 134 plain v_pk_add_f32 (LayerNorm statistics, split-K style sums) split into scalar v_add_f32 pairs, same code size
# baseline (speedup 1.0000x reference)
.LBB0_339:
	v_and_b32_e32 v181, 63, v98
	v_bfe_u32 v182, v98, 4, 2
	s_lshl_b32 s5, s8, 5
	s_barrier
	s_lshl_b32 s6, s10, 8
	v_add_u32_e32 v180, s49, v0
	s_or_b32 s5, s6, s5
	v_lshl_add_u32 v178, s0, 8, v180
	v_lshl_add_u32 v170, v182, 3, s5
	v_add_u32_e32 v176, 16, v178
	v_ashrrev_i32_e32 v171, 31, v170
	v_ashrrev_i32_e32 v179, 31, v178
	v_ashrrev_i32_e32 v177, 31, v176
	s_mov_b32 s10, 0x41800000
	v_lshl_add_u64 v[30:31], v[170:171], 2, s[30:31]
	v_lshlrev_b64 v[2:3], 13, v[178:179]
	v_lshlrev_b64 v[18:19], 13, v[176:177]
	v_add_u32_e32 v174, 32, v178
	s_mov_b32 s7, 1.0
	s_mov_b32 s34, 0x3fd744fd
	s_mov_b32 s11, 0x41880000
	s_mov_b32 s5, s10
	v_lshl_add_u64 v[14:15], v[30:31], 0, v[2:3]
	v_lshl_add_u64 v[32:33], v[30:31], 0, v[18:19]
	v_ashrrev_i32_e32 v175, 31, v174
	global_load_dwordx4 v[2:5], v[14:15], off offset:16
	global_load_dwordx4 v[6:9], v[14:15], off
	global_load_dwordx4 v[10:13], v[14:15], off offset:528
	s_nop 0
	global_load_dwordx4 v[14:17], v[14:15], off offset:512
	s_nop 0
	global_load_dwordx4 v[18:21], v[32:33], off offset:16
	global_load_dwordx4 v[22:25], v[32:33], off
	global_load_dwordx4 v[26:29], v[32:33], off offset:528
	global_load_dwordx4 v[184:187], v[32:33], off offset:512
	v_lshlrev_b64 v[32:33], 13, v[174:175]
	v_add_u32_e32 v172, 48, v178
	v_lshl_add_u64 v[32:33], v[30:31], 0, v[32:33]
	v_ashrrev_i32_e32 v173, 31, v172
	global_load_dwordx4 v[188:191], v[32:33], off offset:16
	global_load_dwordx4 v[192:195], v[32:33], off
	global_load_dwordx4 v[196:199], v[32:33], off offset:528
	global_load_dwordx4 v[204:207], v[32:33], off offset:512
	v_lshlrev_b64 v[32:33], 13, v[172:173]
	v_lshl_add_u64 v[32:33], v[30:31], 0, v[32:33]
	global_load_dwordx4 v[208:211], v[32:33], off offset:16
	global_load_dwordx4 v[212:215], v[32:33], off
	global_load_dwordx4 v[216:219], v[32:33], off offset:528
	global_load_dwordx4 v[220:223], v[32:33], off offset:512
	s_lshl_b32 s7, s8, 3
	v_cmp_eq_u32_e32 vcc, 0, v182
	s_add_i32 s7, s7, 0
	s_waitcnt vmcnt(15)
	v_pk_fma_f32 v[100:101], v[4:5], s[34:35], v[40:41] op_sel_hi:[1,0,1]
	s_waitcnt vmcnt(14)
	v_pk_fma_f32 v[102:103], v[6:7], s[34:35], v[34:35] op_sel_hi:[1,0,1]
	s_waitcnt vmcnt(13)
	v_pk_fma_f32 v[34:35], s[34:35], v[10:11], v[86:87] op_sel_hi:[0,1,1]
	v_pk_fma_f32 v[104:105], v[8:9], s[34:35], v[36:37] op_sel_hi:[1,0,1]
	v_pk_fma_f32 v[98:99], v[2:3], s[34:35], v[38:39] op_sel_hi:[1,0,1]
	s_waitcnt vmcnt(12)
	v_pk_fma_f32 v[40:41], s[34:35], v[16:17], v[84:85] op_sel_hi:[0,1,1]
	v_pk_fma_f32 v[38:39], s[34:35], v[14:15], v[82:83] op_sel_hi:[0,1,1]
	v_pk_fma_f32 v[36:37], s[34:35], v[12:13], v[88:89] op_sel_hi:[0,1,1]
	s_waitcnt vmcnt(5)
	v_pk_fma_f32 v[10:11], s[34:35], v[196:197], v[154:155] op_sel_hi:[0,1,1]
	v_add_u32_e32 v154, 0x80, v178
	v_ashrrev_i32_e32 v155, 31, v154
	v_pk_fma_f32 v[88:89], s[34:35], v[24:25], v[72:73] op_sel_hi:[0,1,1]
	v_pk_fma_f32 v[86:87], s[34:35], v[22:23], v[70:71] op_sel_hi:[0,1,1]
	v_pk_fma_f32 v[84:85], s[34:35], v[20:21], v[68:69] op_sel_hi:[0,1,1]
	v_pk_fma_f32 v[82:83], s[34:35], v[18:19], v[66:67] op_sel_hi:[0,1,1]
	v_pk_fma_f32 v[24:25], s[34:35], v[186:187], v[168:169] op_sel_hi:[0,1,1]
	v_pk_fma_f32 v[22:23], s[34:35], v[184:185], v[166:167] op_sel_hi:[0,1,1]
	v_pk_fma_f32 v[20:21], s[34:35], v[28:29], v[164:165] op_sel_hi:[0,1,1]
	v_pk_fma_f32 v[18:19], s[34:35], v[26:27], v[162:163] op_sel_hi:[0,1,1]
	v_pk_fma_f32 v[80:81], s[34:35], v[194:195], v[80:81] op_sel_hi:[0,1,1]
	v_pk_fma_f32 v[78:79], s[34:35], v[192:193], v[78:79] op_sel_hi:[0,1,1]
	v_pk_fma_f32 v[76:77], s[34:35], v[190:191], v[76:77] op_sel_hi:[0,1,1]
	v_pk_fma_f32 v[74:75], s[34:35], v[188:189], v[74:75] op_sel_hi:[0,1,1]
	s_waitcnt vmcnt(4)
	v_pk_fma_f32 v[16:17], s[34:35], v[206:207], v[160:161] op_sel_hi:[0,1,1]
	v_pk_fma_f32 v[14:15], s[34:35], v[204:205], v[158:159] op_sel_hi:[0,1,1]
	v_pk_fma_f32 v[12:13], s[34:35], v[198:199], v[156:157] op_sel_hi:[0,1,1]
	s_waitcnt vmcnt(2)
	v_pk_fma_f32 v[72:73], s[34:35], v[214:215], v[120:121] op_sel_hi:[0,1,1]
	v_pk_fma_f32 v[70:71], s[34:35], v[212:213], v[118:119] op_sel_hi:[0,1,1]
	v_pk_fma_f32 v[68:69], s[34:35], v[210:211], v[116:117] op_sel_hi:[0,1,1]
	v_pk_fma_f32 v[66:67], s[34:35], v[208:209], v[114:115] op_sel_hi:[0,1,1]
	s_waitcnt vmcnt(0)
	v_pk_fma_f32 v[8:9], s[34:35], v[222:223], v[128:129] op_sel_hi:[0,1,1]
	v_pk_fma_f32 v[6:7], s[34:35], v[220:221], v[126:127] op_sel_hi:[0,1,1]
	v_pk_fma_f32 v[4:5], s[34:35], v[218:219], v[124:125] op_sel_hi:[0,1,1]
	v_pk_fma_f32 v[2:3], s[34:35], v[216:217], v[122:123] op_sel_hi:[0,1,1]
	v_lshlrev_b64 v[26:27], 13, v[154:155]
	v_add_u32_e32 v160, 0x90, v178
	v_lshl_add_u64 v[32:33], v[30:31], 0, v[26:27]
	v_ashrrev_i32_e32 v161, 31, v160
	global_load_dwordx4 v[26:29], v[32:33], off offset:16
	global_load_dwordx4 v[114:117], v[32:33], off
	global_load_dwordx4 v[118:121], v[32:33], off offset:528
	global_load_dwordx4 v[162:165], v[32:33], off offset:512
	v_lshlrev_b64 v[32:33], 13, v[160:161]
	v_add_u32_e32 v158, 0xa0, v178
	v_lshl_add_u64 v[32:33], v[30:31], 0, v[32:33]
	v_ashrrev_i32_e32 v159, 31, v158
	global_load_dwordx4 v[166:169], v[32:33], off offset:16
	global_load_dwordx4 v[184:187], v[32:33], off
	global_load_dwordx4 v[188:191], v[32:33], off offset:528
	global_load_dwordx4 v[192:195], v[32:33], off offset:512
	v_lshlrev_b64 v[32:33], 13, v[158:159]
	v_add_u32_e32 v156, 0xb0, v178
	v_lshl_add_u64 v[32:33], v[30:31], 0, v[32:33]
	v_ashrrev_i32_e32 v157, 31, v156
	global_load_dwordx4 v[196:199], v[32:33], off offset:16
	global_load_dwordx4 v[204:207], v[32:33], off
	global_load_dwordx4 v[208:211], v[32:33], off offset:528
	global_load_dwordx4 v[212:215], v[32:33], off offset:512
	v_lshlrev_b64 v[32:33], 13, v[156:157]
	v_lshl_add_u64 v[122:123], v[30:31], 0, v[32:33]
	global_load_dwordx4 v[30:33], v[122:123], off offset:16
	global_load_dwordx4 v[216:219], v[122:123], off
	global_load_dwordx4 v[220:223], v[122:123], off offset:528
	global_load_dwordx4 v[224:227], v[122:123], off offset:512
	s_waitcnt vmcnt(15)
	v_pk_fma_f32 v[124:125], s[34:35], v[28:29], v[44:45] op_sel_hi:[0,1,1]
	s_waitcnt vmcnt(14)
	v_pk_fma_f32 v[126:127], s[34:35], v[114:115], v[46:47] op_sel_hi:[0,1,1]
	v_pk_fma_f32 v[128:129], s[34:35], v[116:117], v[48:49] op_sel_hi:[0,1,1]
	v_pk_fma_f32 v[122:123], s[34:35], v[26:27], v[42:43] op_sel_hi:[0,1,1]
	s_waitcnt vmcnt(12)
	v_pk_fma_f32 v[64:65], s[34:35], v[164:165], v[64:65] op_sel_hi:[0,1,1]
	s_waitcnt vmcnt(11)
	v_pk_fma_f32 v[114:115], s[34:35], v[166:167], v[50:51] op_sel_hi:[0,1,1]
	v_pk_fma_f32 v[116:117], s[34:35], v[168:169], v[52:53] op_sel_hi:[0,1,1]
	s_waitcnt vmcnt(9)
	v_pk_fma_f32 v[50:51], s[34:35], v[188:189], v[106:107] op_sel_hi:[0,1,1]
	v_pk_fma_f32 v[52:53], s[34:35], v[190:191], v[108:109] op_sel_hi:[0,1,1]
	v_pk_fma_f32 v[62:63], s[34:35], v[162:163], v[62:63] op_sel_hi:[0,1,1]
	s_waitcnt vmcnt(7)
	v_pk_fma_f32 v[106:107], s[34:35], v[196:197], v[90:91] op_sel_hi:[0,1,1]
	v_pk_fma_f32 v[108:109], s[34:35], v[198:199], v[92:93] op_sel_hi:[0,1,1]
	v_pk_fma_f32 v[60:61], s[34:35], v[120:121], v[60:61] op_sel_hi:[0,1,1]
	s_waitcnt vmcnt(3)
	v_pk_fma_f32 v[90:91], s[34:35], v[30:31], v[130:131] op_sel_hi:[0,1,1]
	v_add_f32_e32 v130, v102, v103
	v_add_f32_e32 v131, v104, v105
	v_pk_fma_f32 v[92:93], s[34:35], v[32:33], v[132:133] op_sel_hi:[0,1,1]
	v_add_f32_e32 v130, v130, v131
	v_mul_f32_e32 v131, v103, v103
	v_mul_f32_e32 v132, v105, v105
	v_fmac_f32_e32 v131, v102, v102
	v_fmac_f32_e32 v132, v104, v104
	v_add_f32_e32 v131, v131, v132
	v_add_f32_e32 v132, v98, v99
	v_add_f32_e32 v133, v100, v101
	v_add_f32_e32 v130, 0, v130
	v_add_f32_e32 v132, v132, v133
	v_add_f32_e32 v130, v132, v130
	v_mul_f32_e32 v132, v99, v99
	v_mul_f32_e32 v133, v101, v101
	v_fmac_f32_e32 v132, v98, v98
	v_fmac_f32_e32 v133, v100, v100
	v_add_f32_e32 v132, v132, v133
	v_add_f32_e32 v131, v131, v132
	v_add_f32_e32 v132, v38, v39
	v_add_f32_e32 v133, v40, v41
	v_add_f32_e32 v132, v132, v133
	v_add_f32_e32 v130, v132, v130
	v_mul_f32_e32 v132, v39, v39
	v_mul_f32_e32 v133, v41, v41
	v_fmac_f32_e32 v132, v38, v38
	v_fmac_f32_e32 v133, v40, v40
	v_add_f32_e32 v132, v132, v133
	v_add_f32_e32 v131, v132, v131
	v_add_f32_e32 v132, v34, v35
	v_add_f32_e32 v133, v36, v37
	v_add_f32_e32 v132, v132, v133
	v_add_f32_e32 v130, v132, v130
	v_mul_f32_e32 v132, v35, v35
	v_mul_f32_e32 v133, v37, v37
	v_fmac_f32_e32 v132, v34, v34
	v_fmac_f32_e32 v133, v36, v36
	v_add_f32_e32 v132, v132, v133
	v_add_f32_e32 v132, v132, v131
	ds_swizzle_b32 v131, v130 offset:swizzle(SWAP,16)
	v_pk_fma_f32 v[58:59], s[34:35], v[118:119], v[58:59] op_sel_hi:[0,1,1]
	v_pk_fma_f32 v[120:121], s[34:35], v[186:187], v[56:57] op_sel_hi:[0,1,1]
	v_pk_fma_f32 v[118:119], s[34:35], v[184:185], v[54:55] op_sel_hi:[0,1,1]
	v_pk_fma_f32 v[56:57], s[34:35], v[194:195], v[112:113] op_sel_hi:[0,1,1]
	s_waitcnt lgkmcnt(0)
	v_add_f32_e32 v131, v130, v131
	ds_swizzle_b32 v130, v132 offset:swizzle(SWAP,16)
	v_pk_fma_f32 v[54:55], s[34:35], v[192:193], v[110:111] op_sel_hi:[0,1,1]
	v_pk_fma_f32 v[112:113], s[34:35], v[206:207], v[96:97] op_sel_hi:[0,1,1]
	v_pk_fma_f32 v[110:111], s[34:35], v[204:205], v[94:95] op_sel_hi:[0,1,1]
	v_pk_fma_f32 v[48:49], s[34:35], v[214:215], v[152:153] op_sel_hi:[0,1,1]
	v_pk_fma_f32 v[46:47], s[34:35], v[212:213], v[150:151] op_sel_hi:[0,1,1]
	v_pk_fma_f32 v[44:45], s[34:35], v[210:211], v[148:149] op_sel_hi:[0,1,1]
	v_pk_fma_f32 v[42:43], s[34:35], v[208:209], v[146:147] op_sel_hi:[0,1,1]
	s_waitcnt vmcnt(2)
	v_pk_fma_f32 v[96:97], s[34:35], v[218:219], v[136:137] op_sel_hi:[0,1,1]
	v_pk_fma_f32 v[94:95], s[34:35], v[216:217], v[134:135] op_sel_hi:[0,1,1]
	s_waitcnt vmcnt(0)
	v_pk_fma_f32 v[32:33], s[34:35], v[226:227], v[144:145] op_sel_hi:[0,1,1]
	v_pk_fma_f32 v[30:31], s[34:35], v[224:225], v[142:143] op_sel_hi:[0,1,1]
	v_pk_fma_f32 v[28:29], s[34:35], v[222:223], v[140:141] op_sel_hi:[0,1,1]
	v_pk_fma_f32 v[26:27], s[34:35], v[220:221], v[138:139] op_sel_hi:[0,1,1]
	s_waitcnt lgkmcnt(0)
	v_add_f32_e32 v130, v132, v130
	v_mov_b32_e32 v133, v131
	v_mov_b32_e32 v132, v130
	s_nop 0
	v_permlane32_swap_b32_e32 v131, v133
	v_permlane32_swap_b32_e32 v130, v132
	s_and_saveexec_b64 s[30:31], vcc
	s_mov_b32 s60, 2.0
	s_mov_b64 s[12:13], s[22:23]
	v_readlane_b32 s22, v254, 29
	s_mov_b32 s61, 0x40400000
	s_mov_b64 s[52:53], 0x400
	s_mov_b32 s56, s16
	s_mov_b32 s36, s17
	v_readlane_b32 s17, v254, 33
	s_mov_b32 s37, s41
	v_readlane_b32 s23, v254, 30
	s_cbranch_execz .LBB0_341
	v_add_f32_e32 v130, v130, v132
	v_add_f32_e32 v131, v131, v133
	s_lshl_b32 s8, s44, 11
	v_mul_f32_e32 v132, 0x3c800000, v131
	v_fma_f32 v130, -v131, v132, v130
	s_add_i32 s8, s7, s8
	v_max_f32_e32 v133, 0, v130
	v_lshl_add_u32 v130, v0, 5, s8
	ds_write_b64 v130, v[132:133]
.LBB0_341:
	s_or_b64 exec, exec, s[30:31]
	v_add_f32_e32 v130, v86, v87
	v_add_f32_e32 v131, v88, v89
	v_add_f32_e32 v130, v130, v131
	v_mul_f32_e32 v131, v87, v87
	v_mul_f32_e32 v132, v89, v89
	v_fmac_f32_e32 v131, v86, v86
	v_fmac_f32_e32 v132, v88, v88
	v_add_f32_e32 v131, v131, v132
	v_add_f32_e32 v132, v82, v83
	v_add_f32_e32 v133, v84, v85
	v_add_f32_e32 v130, 0, v130
	v_add_f32_e32 v132, v132, v133
	v_add_f32_e32 v130, v132, v130
	v_mul_f32_e32 v132, v83, v83
	v_mul_f32_e32 v133, v85, v85
	v_fmac_f32_e32 v132, v82, v82
	v_fmac_f32_e32 v133, v84, v84
	v_add_f32_e32 v132, v132, v133
	v_add_f32_e32 v131, v131, v132
	v_add_f32_e32 v132, v22, v23
	v_add_f32_e32 v133, v24, v25
	v_add_f32_e32 v132, v132, v133
	v_add_f32_e32 v130, v132, v130
	v_mul_f32_e32 v132, v23, v23
	v_mul_f32_e32 v133, v25, v25
	v_fmac_f32_e32 v132, v22, v22
	v_fmac_f32_e32 v133, v24, v24
	v_add_f32_e32 v132, v132, v133
	v_add_f32_e32 v131, v132, v131
	v_add_f32_e32 v132, v18, v19
	v_add_f32_e32 v133, v20, v21
	v_add_f32_e32 v132, v132, v133
	v_add_f32_e32 v130, v132, v130
	v_mul_f32_e32 v132, v19, v19
	v_mul_f32_e32 v133, v21, v21
	v_fmac_f32_e32 v132, v18, v18
	v_fmac_f32_e32 v133, v20, v20
	v_add_f32_e32 v132, v132, v133
	v_add_f32_e32 v132, v132, v131
	ds_swizzle_b32 v131, v130 offset:swizzle(SWAP,16)
	ds_swizzle_b32 v133, v132 offset:swizzle(SWAP,16)
	s_waitcnt lgkmcnt(1)
	v_add_f32_e32 v131, v130, v131
	s_waitcnt lgkmcnt(0)
	v_add_f32_e32 v130, v132, v133
	v_mov_b32_e32 v133, v131
	v_mov_b32_e32 v132, v130
	s_nop 0
	v_permlane32_swap_b32_e32 v131, v133
	v_permlane32_swap_b32_e32 v130, v132
	s_and_saveexec_b64 s[30:31], vcc
	s_cbranch_execz .LBB0_343
	v_add_f32_e32 v130, v130, v132
	v_add_f32_e32 v131, v131, v133
	s_lshl_b32 s8, s44, 11
	v_mul_f32_e32 v132, 0x3c800000, v131
	v_fma_f32 v130, -v131, v132, v130
	s_add_i32 s8, s7, s8
	v_max_f32_e32 v133, 0, v130
	v_lshl_add_u32 v130, v0, 5, s8
	ds_write_b64 v130, v[132:133] offset:512
.LBB0_343:
	s_or_b64 exec, exec, s[30:31]
	v_add_f32_e32 v130, v78, v79
	v_add_f32_e32 v131, v80, v81
	v_add_f32_e32 v130, v130, v131
	v_mul_f32_e32 v131, v79, v79
	v_mul_f32_e32 v132, v81, v81
	v_fmac_f32_e32 v131, v78, v78
	v_fmac_f32_e32 v132, v80, v80
	v_add_f32_e32 v131, v131, v132
	v_add_f32_e32 v132, v74, v75
	v_add_f32_e32 v133, v76, v77
	v_add_f32_e32 v130, 0, v130
	v_add_f32_e32 v132, v132, v133
	v_add_f32_e32 v130, v132, v130
	v_mul_f32_e32 v132, v75, v75
	v_mul_f32_e32 v133, v77, v77
	v_fmac_f32_e32 v132, v74, v74
	v_fmac_f32_e32 v133, v76, v76
	v_add_f32_e32 v132, v132, v133
	v_add_f32_e32 v131, v131, v132
	v_add_f32_e32 v132, v14, v15
	v_add_f32_e32 v133, v16, v17
	v_add_f32_e32 v132, v132, v133
	v_add_f32_e32 v130, v132, v130
	v_mul_f32_e32 v132, v15, v15
	v_mul_f32_e32 v133, v17, v17
	v_fmac_f32_e32 v132, v14, v14
	v_fmac_f32_e32 v133, v16, v16
	v_add_f32_e32 v132, v132, v133
	v_add_f32_e32 v131, v132, v131
	v_add_f32_e32 v132, v10, v11
	v_add_f32_e32 v133, v12, v13
	v_add_f32_e32 v132, v132, v133
	v_add_f32_e32 v130, v132, v130
	v_mul_f32_e32 v132, v11, v11
	v_mul_f32_e32 v133, v13, v13
	v_fmac_f32_e32 v132, v10, v10
	v_fmac_f32_e32 v133, v12, v12
	v_add_f32_e32 v132, v132, v133
	v_add_f32_e32 v132, v132, v131
	ds_swizzle_b32 v131, v130 offset:swizzle(SWAP,16)
	ds_swizzle_b32 v133, v132 offset:swizzle(SWAP,16)
	s_waitcnt lgkmcnt(1)
	v_add_f32_e32 v131, v130, v131
	s_waitcnt lgkmcnt(0)
	v_add_f32_e32 v130, v132, v133
	v_mov_b32_e32 v133, v131
	v_mov_b32_e32 v132, v130
	s_nop 0
	v_permlane32_swap_b32_e32 v131, v133
	v_permlane32_swap_b32_e32 v130, v132
	s_and_saveexec_b64 s[30:31], vcc
	s_cbranch_execz .LBB0_345
	v_add_f32_e32 v130, v130, v132
	v_add_f32_e32 v131, v131, v133
	s_lshl_b32 s8, s44, 11
	v_mul_f32_e32 v132, 0x3c800000, v131
	v_fma_f32 v130, -v131, v132, v130
	s_add_i32 s8, s7, s8
	v_max_f32_e32 v133, 0, v130
	v_lshl_add_u32 v130, v0, 5, s8
	ds_write_b64 v130, v[132:133] offset:1024
.LBB0_345:
	s_or_b64 exec, exec, s[30:31]
	v_add_f32_e32 v130, v70, v71
	v_add_f32_e32 v131, v72, v73
	v_add_f32_e32 v130, v130, v131
	v_mul_f32_e32 v131, v71, v71
	v_mul_f32_e32 v132, v73, v73
	v_fmac_f32_e32 v131, v70, v70
	v_fmac_f32_e32 v132, v72, v72
	v_add_f32_e32 v131, v131, v132
	v_add_f32_e32 v132, v66, v67
	v_add_f32_e32 v133, v68, v69
	v_add_f32_e32 v130, 0, v130
	v_add_f32_e32 v132, v132, v133
	v_add_f32_e32 v130, v132, v130
	v_mul_f32_e32 v132, v67, v67
	v_mul_f32_e32 v133, v69, v69
	v_fmac_f32_e32 v132, v66, v66
	v_fmac_f32_e32 v133, v68, v68
	v_add_f32_e32 v132, v132, v133
	v_add_f32_e32 v131, v131, v132
	v_add_f32_e32 v132, v6, v7
	v_add_f32_e32 v133, v8, v9
	v_add_f32_e32 v132, v132, v133
	v_add_f32_e32 v130, v132, v130
	v_mul_f32_e32 v132, v7, v7
	v_mul_f32_e32 v133, v9, v9
	v_fmac_f32_e32 v132, v6, v6
	v_fmac_f32_e32 v133, v8, v8
	v_add_f32_e32 v132, v132, v133
	v_add_f32_e32 v131, v132, v131
	v_add_f32_e32 v132, v2, v3
	v_add_f32_e32 v133, v4, v5
	v_add_f32_e32 v132, v132, v133
	v_add_f32_e32 v130, v132, v130
	v_mul_f32_e32 v132, v3, v3
	v_mul_f32_e32 v133, v5, v5
	v_fmac_f32_e32 v132, v2, v2
	v_fmac_f32_e32 v133, v4, v4
	v_add_f32_e32 v132, v132, v133
	v_add_f32_e32 v132, v132, v131
	ds_swizzle_b32 v131, v130 offset:swizzle(SWAP,16)
	ds_swizzle_b32 v133, v132 offset:swizzle(SWAP,16)
	s_waitcnt lgkmcnt(1)
	v_add_f32_e32 v131, v130, v131
	s_waitcnt lgkmcnt(0)
	v_add_f32_e32 v130, v132, v133
	v_mov_b32_e32 v133, v131
	v_mov_b32_e32 v132, v130
	s_nop 0
	v_permlane32_swap_b32_e32 v131, v133
	v_permlane32_swap_b32_e32 v130, v132
	s_and_saveexec_b64 s[30:31], vcc
	s_cbranch_execz .LBB0_347
	v_add_f32_e32 v130, v130, v132
	v_add_f32_e32 v131, v131, v133
	s_lshl_b32 s8, s44, 11
	v_mul_f32_e32 v132, 0x3c800000, v131
	v_fma_f32 v130, -v131, v132, v130
	s_add_i32 s8, s7, s8
	v_max_f32_e32 v133, 0, v130
	v_lshl_add_u32 v130, v0, 5, s8
	ds_write_b64 v130, v[132:133] offset:1536
.LBB0_347:
	s_or_b64 exec, exec, s[30:31]
	v_add_f32_e32 v130, v126, v127
	v_add_f32_e32 v131, v128, v129
	v_add_f32_e32 v130, v130, v131
	v_mul_f32_e32 v131, v127, v127
	v_mul_f32_e32 v132, v129, v129
	v_fmac_f32_e32 v131, v126, v126
	v_fmac_f32_e32 v132, v128, v128
	v_add_f32_e32 v131, v131, v132
	v_add_f32_e32 v132, v122, v123
	v_add_f32_e32 v133, v124, v125
	v_add_f32_e32 v130, 0, v130
	v_add_f32_e32 v132, v132, v133
	v_add_f32_e32 v130, v132, v130
	v_mul_f32_e32 v132, v123, v123
	v_mul_f32_e32 v133, v125, v125
	v_fmac_f32_e32 v132, v122, v122
	v_fmac_f32_e32 v133, v124, v124
	v_add_f32_e32 v132, v132, v133
	v_add_f32_e32 v131, v131, v132
	v_add_f32_e32 v132, v62, v63
	v_add_f32_e32 v133, v64, v65
	v_add_f32_e32 v132, v132, v133
	v_add_f32_e32 v130, v132, v130
	v_mul_f32_e32 v132, v63, v63
	v_mul_f32_e32 v133, v65, v65
	v_fmac_f32_e32 v132, v62, v62
	v_fmac_f32_e32 v133, v64, v64
	v_add_f32_e32 v132, v132, v133
	v_add_f32_e32 v131, v132, v131
	v_add_f32_e32 v132, v58, v59
	v_add_f32_e32 v133, v60, v61
	v_add_f32_e32 v132, v132, v133
	v_add_f32_e32 v130, v132, v130
	v_mul_f32_e32 v132, v59, v59
	v_mul_f32_e32 v133, v61, v61
	v_fmac_f32_e32 v132, v58, v58
	v_fmac_f32_e32 v133, v60, v60
	v_add_f32_e32 v132, v132, v133
	v_add_f32_e32 v132, v132, v131
	ds_swizzle_b32 v131, v130 offset:swizzle(SWAP,16)
	ds_swizzle_b32 v133, v132 offset:swizzle(SWAP,16)
	s_waitcnt lgkmcnt(1)
	v_add_f32_e32 v131, v130, v131
	s_waitcnt lgkmcnt(0)
	v_add_f32_e32 v130, v132, v133
	v_mov_b32_e32 v133, v131
	v_mov_b32_e32 v132, v130
	s_nop 0
	v_permlane32_swap_b32_e32 v131, v133
	v_permlane32_swap_b32_e32 v130, v132
	s_and_saveexec_b64 s[30:31], vcc
	s_cbranch_execz .LBB0_349
	v_add_f32_e32 v130, v130, v132
	v_add_f32_e32 v131, v131, v133
	s_lshl_b32 s8, s44, 11
	v_mul_f32_e32 v132, 0x3c800000, v131
	v_fma_f32 v130, -v131, v132, v130
	s_add_i32 s8, s7, s8
	v_max_f32_e32 v133, 0, v130
	v_lshl_add_u32 v130, v0, 5, s8
	ds_write_b64 v130, v[132:133] offset:4096
.LBB0_349:
	s_or_b64 exec, exec, s[30:31]
	v_add_f32_e32 v130, v118, v119
	v_add_f32_e32 v131, v120, v121
	v_add_f32_e32 v130, v130, v131
	v_mul_f32_e32 v131, v119, v119
	v_mul_f32_e32 v132, v121, v121
	v_fmac_f32_e32 v131, v118, v118
	v_fmac_f32_e32 v132, v120, v120
	v_add_f32_e32 v131, v131, v132
	v_add_f32_e32 v132, v114, v115
	v_add_f32_e32 v133, v116, v117
	v_add_f32_e32 v130, 0, v130
	v_add_f32_e32 v132, v132, v133
	v_add_f32_e32 v130, v132, v130
	v_mul_f32_e32 v132, v115, v115
	v_mul_f32_e32 v133, v117, v117
	v_fmac_f32_e32 v132, v114, v114
	v_fmac_f32_e32 v133, v116, v116
	v_add_f32_e32 v132, v132, v133
	v_add_f32_e32 v131, v131, v132
	v_add_f32_e32 v132, v54, v55
	v_add_f32_e32 v133, v56, v57
	v_add_f32_e32 v132, v132, v133
	v_add_f32_e32 v130, v132, v130
	v_mul_f32_e32 v132, v55, v55
	v_mul_f32_e32 v133, v57, v57
	v_fmac_f32_e32 v132, v54, v54
	v_fmac_f32_e32 v133, v56, v56
	v_add_f32_e32 v132, v132, v133
	v_add_f32_e32 v131, v132, v131
	v_add_f32_e32 v132, v50, v51
	v_add_f32_e32 v133, v52, v53
	v_add_f32_e32 v132, v132, v133
	v_add_f32_e32 v130, v132, v130
	v_mul_f32_e32 v132, v51, v51
	v_mul_f32_e32 v133, v53, v53
	v_fmac_f32_e32 v132, v50, v50
	v_fmac_f32_e32 v133, v52, v52
	v_add_f32_e32 v132, v132, v133
	v_add_f32_e32 v132, v132, v131
	ds_swizzle_b32 v131, v130 offset:swizzle(SWAP,16)
	ds_swizzle_b32 v133, v132 offset:swizzle(SWAP,16)
	s_waitcnt lgkmcnt(1)
	v_add_f32_e32 v131, v130, v131
	s_waitcnt lgkmcnt(0)
	v_add_f32_e32 v130, v132, v133
	v_mov_b32_e32 v133, v131
	v_mov_b32_e32 v132, v130
	s_nop 0
	v_permlane32_swap_b32_e32 v131, v133
	v_permlane32_swap_b32_e32 v130, v132
	s_and_saveexec_b64 s[30:31], vcc
	s_cbranch_execz .LBB0_351
	v_add_f32_e32 v130, v130, v132
	v_add_f32_e32 v131, v131, v133
	s_lshl_b32 s8, s44, 11
	v_mul_f32_e32 v132, 0x3c800000, v131
	v_fma_f32 v130, -v131, v132, v130
	s_add_i32 s8, s7, s8
	v_max_f32_e32 v133, 0, v130
	v_lshl_add_u32 v130, v0, 5, s8
	ds_write_b64 v130, v[132:133] offset:4608
.LBB0_351:
	s_or_b64 exec, exec, s[30:31]
	v_add_f32_e32 v130, v110, v111
	v_add_f32_e32 v131, v112, v113
	v_add_f32_e32 v130, v130, v131
	v_mul_f32_e32 v131, v111, v111
	v_mul_f32_e32 v132, v113, v113
	v_fmac_f32_e32 v131, v110, v110
	v_fmac_f32_e32 v132, v112, v112
	v_add_f32_e32 v131, v131, v132
	v_add_f32_e32 v132, v106, v107
	v_add_f32_e32 v133, v108, v109
	v_add_f32_e32 v130, 0, v130
	v_add_f32_e32 v132, v132, v133
	v_add_f32_e32 v130, v132, v130
	v_mul_f32_e32 v132, v107, v107
	v_mul_f32_e32 v133, v109, v109
	v_fmac_f32_e32 v132, v106, v106
	v_fmac_f32_e32 v133, v108, v108
	v_add_f32_e32 v132, v132, v133
	v_add_f32_e32 v131, v131, v132
	v_add_f32_e32 v132, v46, v47
	v_add_f32_e32 v133, v48, v49
	v_add_f32_e32 v132, v132, v133
	v_add_f32_e32 v130, v132, v130
	v_mul_f32_e32 v132, v47, v47
	v_mul_f32_e32 v133, v49, v49
	v_fmac_f32_e32 v132, v46, v46
	v_fmac_f32_e32 v133, v48, v48
	v_add_f32_e32 v132, v132, v133
	v_add_f32_e32 v131, v132, v131
	v_add_f32_e32 v132, v42, v43
	v_add_f32_e32 v133, v44, v45
	v_add_f32_e32 v132, v132, v133
	v_add_f32_e32 v130, v132, v130
	v_mul_f32_e32 v132, v43, v43
	v_mul_f32_e32 v133, v45, v45
	v_fmac_f32_e32 v132, v42, v42
	v_fmac_f32_e32 v133, v44, v44
	v_add_f32_e32 v132, v132, v133
	v_add_f32_e32 v132, v132, v131
	ds_swizzle_b32 v131, v130 offset:swizzle(SWAP,16)
	ds_swizzle_b32 v133, v132 offset:swizzle(SWAP,16)
	s_waitcnt lgkmcnt(1)
	v_add_f32_e32 v131, v130, v131
	s_waitcnt lgkmcnt(0)
	v_add_f32_e32 v130, v132, v133
	v_mov_b32_e32 v133, v131
	v_mov_b32_e32 v132, v130
	s_nop 0
	v_permlane32_swap_b32_e32 v131, v133
	v_permlane32_swap_b32_e32 v130, v132
	s_and_saveexec_b64 s[30:31], vcc
	s_cbranch_execz .LBB0_353
	v_add_f32_e32 v130, v130, v132
	v_add_f32_e32 v131, v131, v133
	s_lshl_b32 s8, s44, 11
	v_mul_f32_e32 v132, 0x3c800000, v131
	v_fma_f32 v130, -v131, v132, v130
	s_add_i32 s8, s7, s8
	v_max_f32_e32 v133, 0, v130
	v_lshl_add_u32 v130, v0, 5, s8
	ds_write_b64 v130, v[132:133] offset:5120
.LBB0_353:
	s_or_b64 exec, exec, s[30:31]
	v_add_f32_e32 v130, v94, v95
	v_add_f32_e32 v131, v96, v97
	v_add_f32_e32 v130, v130, v131
	v_mul_f32_e32 v131, v95, v95
	v_mul_f32_e32 v132, v97, v97
	v_fmac_f32_e32 v131, v94, v94
	v_fmac_f32_e32 v132, v96, v96
	v_add_f32_e32 v131, v131, v132
	v_add_f32_e32 v132, v90, v91
	v_add_f32_e32 v133, v92, v93
	v_add_f32_e32 v130, 0, v130
	v_add_f32_e32 v132, v132, v133
	v_add_f32_e32 v130, v132, v130
	v_mul_f32_e32 v132, v91, v91
	v_mul_f32_e32 v133, v93, v93
	v_fmac_f32_e32 v132, v90, v90
	v_fmac_f32_e32 v133, v92, v92
	v_add_f32_e32 v132, v132, v133
	v_add_f32_e32 v131, v131, v132
	v_add_f32_e32 v132, v30, v31
	v_add_f32_e32 v133, v32, v33
	v_add_f32_e32 v132, v132, v133
	v_add_f32_e32 v130, v132, v130
	v_mul_f32_e32 v132, v31, v31
	v_mul_f32_e32 v133, v33, v33
	v_fmac_f32_e32 v132, v30, v30
	v_fmac_f32_e32 v133, v32, v32
	v_add_f32_e32 v132, v132, v133
	v_add_f32_e32 v131, v132, v131
	v_add_f32_e32 v132, v26, v27
	v_add_f32_e32 v133, v28, v29
	v_add_f32_e32 v132, v132, v133
	v_add_f32_e32 v130, v132, v130
	v_mul_f32_e32 v132, v27, v27
	v_mul_f32_e32 v133, v29, v29
	v_fmac_f32_e32 v132, v26, v26
	v_fmac_f32_e32 v133, v28, v28
	v_add_f32_e32 v132, v132, v133
	v_add_f32_e32 v132, v132, v131
	ds_swizzle_b32 v131, v130 offset:swizzle(SWAP,16)
	ds_swizzle_b32 v133, v132 offset:swizzle(SWAP,16)
	s_waitcnt lgkmcnt(1)
	v_add_f32_e32 v131, v130, v131
	s_waitcnt lgkmcnt(0)
	v_add_f32_e32 v130, v132, v133
	v_mov_b32_e32 v133, v131
	v_mov_b32_e32 v132, v130
	s_nop 0
	v_permlane32_swap_b32_e32 v131, v133
	v_permlane32_swap_b32_e32 v130, v132
	s_and_saveexec_b64 s[30:31], vcc
	s_cbranch_execz .LBB0_355
	v_add_f32_e32 v130, v130, v132
	v_add_f32_e32 v131, v131, v133
	s_lshl_b32 s8, s44, 11
	v_mul_f32_e32 v132, 0x3c800000, v131
	v_fma_f32 v130, -v131, v132, v130
	s_add_i32 s7, s7, s8
	v_max_f32_e32 v133, 0, v130
	v_lshl_add_u32 v0, v0, 5, s7
	ds_write_b64 v0, v[132:133] offset:5632
.LBB0_355:
	s_or_b64 exec, exec, s[30:31]
	v_or_b32_e32 v0, s1, v181
	v_cmp_eq_u32_e32 vcc, 0, v0
	s_and_saveexec_b64 s[30:31], vcc
	ds_write_b32 v1, v1 offset:10240
	s_or_b64 exec, exec, s[30:31]
	s_waitcnt lgkmcnt(0)
	s_barrier
	v_cmp_gt_i32_e32 vcc, 32, v181
	s_and_saveexec_b64 s[30:31], vcc
	s_cbranch_execz .LBB0_368
	s_lshl_b32 s1, s1, 5
	v_and_or_b32 v130, v181, 31, s1
	v_lshl_add_u32 v0, v130, 5, 0
	ds_read_b128 v[132:135], v0
	ds_read_b128 v[136:139], v0 offset:16
	s_ashr_i32 s1, s0, 31
	s_lshl_b64 s[0:1], s[0:1], 14
	s_add_u32 s0, s39, s0
	s_waitcnt lgkmcnt(1)
	v_add_f32_e32 v131, v132, v134
	s_waitcnt lgkmcnt(0)
	v_add_f32_e32 v131, v131, v136
	v_add_f32_e32 v131, v131, v138
	v_fmamk_f32 v132, v131, 0xbe800000, v132
	v_fmac_f32_e32 v134, 0xbe800000, v131
	v_fmamk_f32 v136, v131, 0xbe800000, v136
	v_fmac_f32_e32 v138, 0xbe800000, v131
	v_mul_f32_e32 v143, v132, v132
	v_mul_f32_e32 v145, v134, v134
	v_mul_f32_e32 v147, v136, v136
	v_mul_f32_e32 v149, v138, v138
	v_mov_b32_e32 v142, v133
	v_mov_b32_e32 v144, v135
	v_mov_b32_e32 v146, v137
	v_mov_b32_e32 v148, v139
	v_add_f32_e32 v132, v142, v144
	v_add_f32_e32 v133, v143, v145
	v_add_f32_e32 v134, v146, v148
	v_add_f32_e32 v135, v147, v149
	v_mul_f32_e32 v140, 0x3e800000, v131
	v_add_f32_e32 v132, v132, v134
	v_add_f32_e32 v133, v133, v135
	s_addc_u32 s1, s17, s1
	v_ashrrev_i32_e32 v131, 31, v130
	v_fmac_f32_e32 v132, 0x42800000, v133
	v_lshl_add_u64 v[136:137], v[130:131], 3, s[0:1]
	s_ashr_i32 s7, s6, 31
	s_movk_i32 s0, 0xffe0
	v_lshl_add_u64 v[134:135], s[6:7], 3, v[136:137]
	v_and_or_b32 v141, v132, s0, 1
	s_mov_b64 s[0:1], 0x1000
	global_store_dwordx2 v[134:135], v[140:141], off sc1
	v_lshl_add_u64 v[140:141], v[136:137], 0, s[0:1]
	s_mov_b64 s[0:1], 0x1800
	s_memrealtime s[34:35]
	v_lshl_add_u64 v[142:143], v[136:137], 0, s[0:1]
	s_mov_b64 s[0:1], 0x2000
	v_lshl_add_u64 v[146:147], v[136:137], 0, s[0:1]
	s_mov_b64 s[0:1], 0x2800
	v_lshl_add_u64 v[148:149], v[136:137], 0, s[0:1]
	s_mov_b64 s[0:1], 0x3000
	v_lshl_add_u64 v[150:151], v[136:137], 0, s[0:1]
	s_mov_b64 s[0:1], 0x3800
	v_lshl_add_u64 v[152:153], v[136:137], 0, s[0:1]
	s_mov_b64 s[6:7], 0
	s_branch .LBB0_361

.LBB0_417:
	v_readlane_b32 s5, v254, 16
	s_cmp_gt_u32 s5, 1
	s_cselect_b64 s[6:7], -1, 0
	s_and_b64 s[6:7], s[6:7], s[24:25]
	s_and_b64 s[6:7], s[6:7], exec
	s_mov_b32 s5, 0x4c100000
	s_cselect_b32 s5, s5, 0x32e00000
	s_add_u32 s12, s14, s5
	s_addc_u32 s13, s15, 0
	v_and_b32_e32 v219, 63, v130
	v_bfe_u32 v220, v130, 4, 2
	s_lshl_b32 s5, s8, 5
	s_lshl_b32 s6, s10, 8
	s_barrier
	s_or_b32 s5, s6, s5
	v_add_u32_e32 v218, s45, v0
	v_lshl_add_u32 v198, v220, 3, s5
	v_lshl_add_u32 v216, s0, 8, v218
	v_ashrrev_i32_e32 v199, 31, v198
	v_ashrrev_i32_e32 v217, 31, v216
	v_lshl_add_u64 v[134:135], v[198:199], 1, s[12:13]
	v_lshlrev_b64 v[2:3], 12, v[216:217]
	v_add_u32_e32 v214, 16, v216
	s_mov_b32 s7, 1.0
	s_mov_b32 s26, 0x3fd744fd
	s_mov_b32 s5, s28
	v_lshl_add_u64 v[2:3], v[134:135], 0, v[2:3]
	v_ashrrev_i32_e32 v215, 31, v214
	global_load_dwordx4 v[130:133], v[2:3], off
	global_load_dwordx4 v[194:197], v[2:3], off offset:256
	v_lshlrev_b64 v[2:3], 12, v[214:215]
	v_add_u32_e32 v212, 32, v216
	v_lshl_add_u64 v[2:3], v[134:135], 0, v[2:3]
	v_ashrrev_i32_e32 v213, 31, v212
	global_load_dwordx4 v[190:193], v[2:3], off
	global_load_dwordx4 v[186:189], v[2:3], off offset:256
	v_lshlrev_b64 v[2:3], 12, v[212:213]
	v_add_u32_e32 v210, 48, v216
	v_lshl_add_u64 v[2:3], v[134:135], 0, v[2:3]
	v_ashrrev_i32_e32 v211, 31, v210
	global_load_dwordx4 v[182:185], v[2:3], off
	global_load_dwordx4 v[178:181], v[2:3], off offset:256
	v_lshlrev_b64 v[2:3], 12, v[210:211]
	v_add_u32_e32 v208, 0x80, v216
	v_lshl_add_u64 v[2:3], v[134:135], 0, v[2:3]
	v_ashrrev_i32_e32 v209, 31, v208
	global_load_dwordx4 v[30:33], v[2:3], off
	global_load_dwordx4 v[26:29], v[2:3], off offset:256
	v_lshlrev_b64 v[2:3], 12, v[208:209]
	v_add_u32_e32 v206, 0x90, v216
	v_lshl_add_u64 v[2:3], v[134:135], 0, v[2:3]
	v_ashrrev_i32_e32 v207, 31, v206
	global_load_dwordx4 v[22:25], v[2:3], off
	global_load_dwordx4 v[18:21], v[2:3], off offset:256
	v_lshlrev_b64 v[2:3], 12, v[206:207]
	v_add_u32_e32 v204, 0xa0, v216
	v_lshl_add_u64 v[2:3], v[134:135], 0, v[2:3]
	v_ashrrev_i32_e32 v205, 31, v204
	global_load_dwordx4 v[14:17], v[2:3], off
	global_load_dwordx4 v[10:13], v[2:3], off offset:256
	v_lshlrev_b64 v[2:3], 12, v[204:205]
	v_add_u32_e32 v200, 0xb0, v216
	v_lshl_add_u64 v[2:3], v[134:135], 0, v[2:3]
	v_ashrrev_i32_e32 v201, 31, v200
	global_load_dwordx4 v[6:9], v[2:3], off
	s_nop 0
	global_load_dwordx4 v[2:5], v[2:3], off offset:256
	v_lshlrev_b64 v[136:137], 12, v[200:201]
	v_lshl_add_u64 v[134:135], v[134:135], 0, v[136:137]
	global_load_dwordx4 v[174:177], v[134:135], off
	global_load_dwordx4 v[170:173], v[134:135], off offset:256
	s_lshl_b32 s7, s8, 3
	v_cmp_eq_u32_e32 vcc, 0, v220
	s_add_i32 s7, s7, 0
	s_waitcnt vmcnt(15)
	v_lshlrev_b32_e32 v134, 16, v130
	v_and_b32_e32 v135, 0xffff0000, v130
	v_lshlrev_b32_e32 v130, 16, v131
	v_and_b32_e32 v131, 0xffff0000, v131
	v_lshlrev_b32_e32 v222, 16, v132
	v_and_b32_e32 v223, 0xffff0000, v132
	v_pk_fma_f32 v[136:137], s[26:27], v[130:131], v[116:117] op_sel_hi:[0,1,1]
	v_pk_fma_f32 v[134:135], s[26:27], v[134:135], v[114:115] op_sel_hi:[0,1,1]
	s_waitcnt vmcnt(14)
	v_lshlrev_b32_e32 v114, 16, v196
	v_and_b32_e32 v115, 0xffff0000, v196
	v_lshlrev_b32_e32 v116, 16, v197
	v_and_b32_e32 v117, 0xffff0000, v197
	v_lshlrev_b32_e32 v132, 16, v133
	v_and_b32_e32 v133, 0xffff0000, v133
	v_pk_fma_f32 v[130:131], s[26:27], v[222:223], v[118:119] op_sel_hi:[0,1,1]
	v_lshlrev_b32_e32 v118, 16, v194
	v_and_b32_e32 v119, 0xffff0000, v194
	v_pk_fma_f32 v[64:65], s[26:27], v[116:117], v[64:65] op_sel_hi:[0,1,1]
	v_pk_fma_f32 v[62:63], s[26:27], v[114:115], v[62:63] op_sel_hi:[0,1,1]
	s_waitcnt vmcnt(13)
	v_lshlrev_b32_e32 v114, 16, v192
	v_and_b32_e32 v115, 0xffff0000, v192
	v_lshlrev_b32_e32 v116, 16, v193
	v_and_b32_e32 v117, 0xffff0000, v193
	v_pk_fma_f32 v[132:133], s[26:27], v[132:133], v[120:121] op_sel_hi:[0,1,1]
	v_lshlrev_b32_e32 v120, 16, v195
	v_and_b32_e32 v121, 0xffff0000, v195
	v_pk_fma_f32 v[58:59], s[26:27], v[118:119], v[58:59] op_sel_hi:[0,1,1]
	v_lshlrev_b32_e32 v118, 16, v190
	v_and_b32_e32 v119, 0xffff0000, v190
	v_pk_fma_f32 v[116:117], s[26:27], v[116:117], v[52:53] op_sel_hi:[0,1,1]
	v_pk_fma_f32 v[114:115], s[26:27], v[114:115], v[50:51] op_sel_hi:[0,1,1]
	s_waitcnt vmcnt(12)
	v_lshlrev_b32_e32 v50, 16, v188
	v_and_b32_e32 v51, 0xffff0000, v188
	v_lshlrev_b32_e32 v52, 16, v189
	v_and_b32_e32 v53, 0xffff0000, v189
	v_pk_fma_f32 v[60:61], s[26:27], v[120:121], v[60:61] op_sel_hi:[0,1,1]
	v_lshlrev_b32_e32 v120, 16, v191
	v_and_b32_e32 v121, 0xffff0000, v191
	v_pk_fma_f32 v[118:119], s[26:27], v[118:119], v[54:55] op_sel_hi:[0,1,1]
	v_lshlrev_b32_e32 v54, 16, v186
	v_and_b32_e32 v55, 0xffff0000, v186
	v_pk_fma_f32 v[52:53], s[26:27], v[52:53], v[108:109] op_sel_hi:[0,1,1]
	v_pk_fma_f32 v[50:51], s[26:27], v[50:51], v[106:107] op_sel_hi:[0,1,1]
	s_waitcnt vmcnt(11)
	v_lshlrev_b32_e32 v106, 16, v184
	v_and_b32_e32 v107, 0xffff0000, v184
	v_lshlrev_b32_e32 v108, 16, v185
	v_and_b32_e32 v109, 0xffff0000, v185
	v_pk_fma_f32 v[120:121], s[26:27], v[120:121], v[56:57] op_sel_hi:[0,1,1]
	v_lshlrev_b32_e32 v56, 16, v187
	v_and_b32_e32 v57, 0xffff0000, v187
	v_pk_fma_f32 v[54:55], s[26:27], v[54:55], v[110:111] op_sel_hi:[0,1,1]
	v_lshlrev_b32_e32 v110, 16, v182
	v_and_b32_e32 v111, 0xffff0000, v182
	v_pk_fma_f32 v[108:109], s[26:27], v[108:109], v[44:45] op_sel_hi:[0,1,1]
	v_pk_fma_f32 v[106:107], s[26:27], v[106:107], v[42:43] op_sel_hi:[0,1,1]
	s_waitcnt vmcnt(10)
	v_lshlrev_b32_e32 v42, 16, v180
	v_and_b32_e32 v43, 0xffff0000, v180
	v_lshlrev_b32_e32 v44, 16, v181
	v_and_b32_e32 v45, 0xffff0000, v181
	v_pk_fma_f32 v[56:57], s[26:27], v[56:57], v[112:113] op_sel_hi:[0,1,1]
	v_lshlrev_b32_e32 v112, 16, v183
	v_and_b32_e32 v113, 0xffff0000, v183
	v_pk_fma_f32 v[110:111], s[26:27], v[110:111], v[46:47] op_sel_hi:[0,1,1]
	v_lshlrev_b32_e32 v46, 16, v178
	v_and_b32_e32 v47, 0xffff0000, v178
	v_pk_fma_f32 v[44:45], s[26:27], v[44:45], v[100:101] op_sel_hi:[0,1,1]
	v_pk_fma_f32 v[42:43], s[26:27], v[42:43], v[98:99] op_sel_hi:[0,1,1]
	s_waitcnt vmcnt(9)
	v_lshlrev_b32_e32 v98, 16, v32
	v_and_b32_e32 v99, 0xffff0000, v32
	v_lshlrev_b32_e32 v32, 16, v33
	v_and_b32_e32 v33, 0xffff0000, v33
	v_lshlrev_b32_e32 v100, 16, v30
	v_and_b32_e32 v101, 0xffff0000, v30
	v_pk_fma_f32 v[112:113], s[26:27], v[112:113], v[48:49] op_sel_hi:[0,1,1]
	v_lshlrev_b32_e32 v48, 16, v179
	v_and_b32_e32 v49, 0xffff0000, v179
	v_pk_fma_f32 v[46:47], s[26:27], v[46:47], v[102:103] op_sel_hi:[0,1,1]
	v_lshlrev_b32_e32 v30, 16, v31
	v_and_b32_e32 v31, 0xffff0000, v31
	v_pk_fma_f32 v[102:103], s[26:27], v[100:101], v[38:39] op_sel_hi:[0,1,1]
	v_pk_fma_f32 v[100:101], s[26:27], v[32:33], v[36:37] op_sel_hi:[0,1,1]
	s_waitcnt vmcnt(8)
	v_lshlrev_b32_e32 v32, 16, v26
	v_and_b32_e32 v33, 0xffff0000, v26
	v_lshlrev_b32_e32 v26, 16, v27
	v_and_b32_e32 v27, 0xffff0000, v27
	v_pk_fma_f32 v[48:49], s[26:27], v[48:49], v[104:105] op_sel_hi:[0,1,1]
	v_pk_fma_f32 v[104:105], s[26:27], v[30:31], v[40:41] op_sel_hi:[0,1,1]
	v_lshlrev_b32_e32 v30, 16, v28
	v_and_b32_e32 v31, 0xffff0000, v28
	v_lshlrev_b32_e32 v28, 16, v29
	v_and_b32_e32 v29, 0xffff0000, v29
	v_pk_fma_f32 v[40:41], s[26:27], v[26:27], v[164:165] op_sel_hi:[0,1,1]
	s_waitcnt vmcnt(7)
	v_lshlrev_b32_e32 v26, 16, v24
	v_and_b32_e32 v27, 0xffff0000, v24
	v_lshlrev_b32_e32 v24, 16, v25
	v_and_b32_e32 v25, 0xffff0000, v25
	v_pk_fma_f32 v[36:37], s[26:27], v[28:29], v[96:97] op_sel_hi:[0,1,1]
	v_lshlrev_b32_e32 v28, 16, v22
	v_and_b32_e32 v29, 0xffff0000, v22
	v_lshlrev_b32_e32 v22, 16, v23
	v_and_b32_e32 v23, 0xffff0000, v23
	v_pk_fma_f32 v[92:93], s[26:27], v[24:25], v[92:93] op_sel_hi:[0,1,1]
	s_waitcnt vmcnt(6)
	v_lshlrev_b32_e32 v24, 16, v18
	v_and_b32_e32 v25, 0xffff0000, v18
	v_lshlrev_b32_e32 v18, 16, v19
	v_and_b32_e32 v19, 0xffff0000, v19
	v_pk_fma_f32 v[38:39], s[26:27], v[32:33], v[162:163] op_sel_hi:[0,1,1]
	v_pk_fma_f32 v[96:97], s[26:27], v[22:23], v[156:157] op_sel_hi:[0,1,1]
	v_lshlrev_b32_e32 v22, 16, v20
	v_and_b32_e32 v23, 0xffff0000, v20
	v_lshlrev_b32_e32 v20, 16, v21
	v_and_b32_e32 v21, 0xffff0000, v21
	v_pk_fma_f32 v[32:33], s[26:27], v[18:19], v[168:169] op_sel_hi:[0,1,1]
	s_waitcnt vmcnt(5)
	v_lshlrev_b32_e32 v18, 16, v16
	v_and_b32_e32 v19, 0xffff0000, v16
	v_lshlrev_b32_e32 v16, 16, v17
	v_and_b32_e32 v17, 0xffff0000, v17
	v_pk_fma_f32 v[98:99], s[26:27], v[98:99], v[34:35] op_sel_hi:[0,1,1]
	v_pk_fma_f32 v[34:35], s[26:27], v[30:31], v[94:95] op_sel_hi:[0,1,1]
	v_pk_fma_f32 v[94:95], s[26:27], v[28:29], v[154:155] op_sel_hi:[0,1,1]
	v_pk_fma_f32 v[28:29], s[26:27], v[20:21], v[160:161] op_sel_hi:[0,1,1]
	v_lshlrev_b32_e32 v20, 16, v14
	v_and_b32_e32 v21, 0xffff0000, v14
	v_lshlrev_b32_e32 v14, 16, v15
	v_and_b32_e32 v15, 0xffff0000, v15
	v_pk_fma_f32 v[84:85], s[26:27], v[16:17], v[84:85] op_sel_hi:[0,1,1]
	s_waitcnt vmcnt(4)
	v_lshlrev_b32_e32 v16, 16, v10
	v_and_b32_e32 v17, 0xffff0000, v10
	v_lshlrev_b32_e32 v10, 16, v11
	v_and_b32_e32 v11, 0xffff0000, v11
	v_pk_fma_f32 v[30:31], s[26:27], v[24:25], v[166:167] op_sel_hi:[0,1,1]
	v_pk_fma_f32 v[88:89], s[26:27], v[14:15], v[88:89] op_sel_hi:[0,1,1]
	v_lshlrev_b32_e32 v14, 16, v12
	v_and_b32_e32 v15, 0xffff0000, v12
	v_lshlrev_b32_e32 v12, 16, v13
	v_and_b32_e32 v13, 0xffff0000, v13
	v_pk_fma_f32 v[24:25], s[26:27], v[10:11], v[152:153] op_sel_hi:[0,1,1]
	s_waitcnt vmcnt(3)
	v_lshlrev_b32_e32 v10, 16, v8
	v_and_b32_e32 v11, 0xffff0000, v8
	v_lshlrev_b32_e32 v8, 16, v9
	v_and_b32_e32 v9, 0xffff0000, v9
	v_pk_fma_f32 v[86:87], s[26:27], v[20:21], v[86:87] op_sel_hi:[0,1,1]
	v_pk_fma_f32 v[20:21], s[26:27], v[12:13], v[148:149] op_sel_hi:[0,1,1]
	v_lshlrev_b32_e32 v12, 16, v6
	v_and_b32_e32 v13, 0xffff0000, v6
	v_lshlrev_b32_e32 v6, 16, v7
	v_and_b32_e32 v7, 0xffff0000, v7
	v_pk_fma_f32 v[76:77], s[26:27], v[8:9], v[76:77] op_sel_hi:[0,1,1]
	s_waitcnt vmcnt(2)
	v_lshlrev_b32_e32 v8, 16, v2
	v_and_b32_e32 v9, 0xffff0000, v2
	v_lshlrev_b32_e32 v2, 16, v3
	v_and_b32_e32 v3, 0xffff0000, v3
	v_pk_fma_f32 v[90:91], s[26:27], v[26:27], v[90:91] op_sel_hi:[0,1,1]
	v_pk_fma_f32 v[26:27], s[26:27], v[22:23], v[158:159] op_sel_hi:[0,1,1]
	v_pk_fma_f32 v[22:23], s[26:27], v[16:17], v[150:151] op_sel_hi:[0,1,1]
	v_pk_fma_f32 v[80:81], s[26:27], v[6:7], v[80:81] op_sel_hi:[0,1,1]
	v_lshlrev_b32_e32 v6, 16, v4
	v_and_b32_e32 v7, 0xffff0000, v4
	v_lshlrev_b32_e32 v4, 16, v5
	v_and_b32_e32 v5, 0xffff0000, v5
	v_pk_fma_f32 v[16:17], s[26:27], v[2:3], v[144:145] op_sel_hi:[0,1,1]
	s_waitcnt vmcnt(1)
	v_lshlrev_b32_e32 v2, 16, v176
	v_and_b32_e32 v3, 0xffff0000, v176
	v_pk_fma_f32 v[78:79], s[26:27], v[12:13], v[78:79] op_sel_hi:[0,1,1]
	v_pk_fma_f32 v[12:13], s[26:27], v[4:5], v[140:141] op_sel_hi:[0,1,1]
	v_lshlrev_b32_e32 v4, 16, v177
	v_and_b32_e32 v5, 0xffff0000, v177
	v_pk_fma_f32 v[66:67], s[26:27], v[2:3], v[66:67] op_sel_hi:[0,1,1]
	s_waitcnt vmcnt(0)
	v_lshlrev_b32_e32 v2, 16, v172
	v_and_b32_e32 v3, 0xffff0000, v172
	v_pk_fma_f32 v[68:69], s[26:27], v[4:5], v[68:69] op_sel_hi:[0,1,1]
	v_lshlrev_b32_e32 v4, 16, v173
	v_and_b32_e32 v5, 0xffff0000, v173
	v_pk_fma_f32 v[2:3], s[26:27], v[2:3], v[122:123] op_sel_hi:[0,1,1]
	v_add_f32_e32 v122, v134, v135
	v_add_f32_e32 v123, v136, v137
	v_pk_fma_f32 v[4:5], s[26:27], v[4:5], v[124:125] op_sel_hi:[0,1,1]
	v_add_f32_e32 v122, v122, v123
	v_mul_f32_e32 v123, v135, v135
	v_mul_f32_e32 v124, v137, v137
	v_fmac_f32_e32 v123, v134, v134
	v_fmac_f32_e32 v124, v136, v136
	v_add_f32_e32 v123, v123, v124
	v_add_f32_e32 v124, v130, v131
	v_add_f32_e32 v125, v132, v133
	v_add_f32_e32 v122, 0, v122
	v_add_f32_e32 v124, v124, v125
	v_add_f32_e32 v122, v124, v122
	v_mul_f32_e32 v124, v131, v131
	v_mul_f32_e32 v125, v133, v133
	v_fmac_f32_e32 v124, v130, v130
	v_fmac_f32_e32 v125, v132, v132
	v_add_f32_e32 v124, v124, v125
	v_add_f32_e32 v123, v123, v124
	v_add_f32_e32 v124, v58, v59
	v_add_f32_e32 v125, v60, v61
	v_add_f32_e32 v124, v124, v125
	v_add_f32_e32 v122, v124, v122
	v_mul_f32_e32 v124, v59, v59
	v_mul_f32_e32 v125, v61, v61
	v_fmac_f32_e32 v124, v58, v58
	v_fmac_f32_e32 v125, v60, v60
	v_add_f32_e32 v124, v124, v125
	v_add_f32_e32 v123, v124, v123
	v_add_f32_e32 v124, v62, v63
	v_add_f32_e32 v125, v64, v65
	v_add_f32_e32 v124, v124, v125
	v_add_f32_e32 v122, v124, v122
	v_mul_f32_e32 v124, v63, v63
	v_mul_f32_e32 v125, v65, v65
	v_fmac_f32_e32 v124, v62, v62
	v_fmac_f32_e32 v125, v64, v64
	v_add_f32_e32 v124, v124, v125
	v_add_f32_e32 v124, v124, v123
	ds_swizzle_b32 v123, v122 offset:swizzle(SWAP,16)
	v_pk_fma_f32 v[82:83], s[26:27], v[18:19], v[82:83] op_sel_hi:[0,1,1]
	v_pk_fma_f32 v[18:19], s[26:27], v[14:15], v[146:147] op_sel_hi:[0,1,1]
	v_pk_fma_f32 v[74:75], s[26:27], v[10:11], v[74:75] op_sel_hi:[0,1,1]
	v_pk_fma_f32 v[14:15], s[26:27], v[8:9], v[142:143] op_sel_hi:[0,1,1]
	s_waitcnt lgkmcnt(0)
	v_add_f32_e32 v123, v122, v123
	ds_swizzle_b32 v122, v124 offset:swizzle(SWAP,16)
	v_pk_fma_f32 v[10:11], s[26:27], v[6:7], v[138:139] op_sel_hi:[0,1,1]
	v_lshlrev_b32_e32 v6, 16, v174
	v_and_b32_e32 v7, 0xffff0000, v174
	v_lshlrev_b32_e32 v8, 16, v175
	v_and_b32_e32 v9, 0xffff0000, v175
	v_pk_fma_f32 v[72:73], s[26:27], v[8:9], v[72:73] op_sel_hi:[0,1,1]
	v_pk_fma_f32 v[70:71], s[26:27], v[6:7], v[70:71] op_sel_hi:[0,1,1]
	v_lshlrev_b32_e32 v6, 16, v170
	v_and_b32_e32 v7, 0xffff0000, v170
	v_lshlrev_b32_e32 v8, 16, v171
	v_and_b32_e32 v9, 0xffff0000, v171
	v_pk_fma_f32 v[8:9], s[26:27], v[8:9], v[128:129] op_sel_hi:[0,1,1]
	v_pk_fma_f32 v[6:7], s[26:27], v[6:7], v[126:127] op_sel_hi:[0,1,1]
	s_waitcnt lgkmcnt(0)
	v_add_f32_e32 v122, v124, v122
	v_mov_b32_e32 v125, v123
	v_mov_b32_e32 v124, v122
	s_nop 0
	v_permlane32_swap_b32_e32 v123, v125
	v_permlane32_swap_b32_e32 v122, v124
	s_and_saveexec_b64 s[26:27], vcc
	s_mov_b64 s[52:53], 0x400
	s_mov_b32 s56, s16
	s_mov_b32 s36, s17
	s_mov_b64 s[12:13], s[22:23]
	s_mov_b32 s17, s41
	s_mov_b32 s37, s42
	s_mov_b32 s31, s43
	s_mov_b64 s[22:23], s[78:79]
	s_cbranch_execz .LBB0_419
	v_add_f32_e32 v122, v122, v124
	v_add_f32_e32 v123, v123, v125
	s_lshl_b32 s8, s30, 11
	v_mul_f32_e32 v124, 0x3c800000, v123
	v_fma_f32 v122, -v123, v124, v122
	s_add_i32 s8, s7, s8
	v_max_f32_e32 v125, 0, v122
	v_lshl_add_u32 v122, v0, 5, s8
	ds_write_b64 v122, v[124:125]
.LBB0_419:
	s_or_b64 exec, exec, s[26:27]
	v_add_f32_e32 v122, v118, v119
	v_add_f32_e32 v123, v120, v121
	v_add_f32_e32 v122, v122, v123
	v_mul_f32_e32 v123, v119, v119
	v_mul_f32_e32 v124, v121, v121
	v_fmac_f32_e32 v123, v118, v118
	v_fmac_f32_e32 v124, v120, v120
	v_add_f32_e32 v123, v123, v124
	v_add_f32_e32 v124, v114, v115
	v_add_f32_e32 v125, v116, v117
	v_add_f32_e32 v122, 0, v122
	v_add_f32_e32 v124, v124, v125
	v_add_f32_e32 v122, v124, v122
	v_mul_f32_e32 v124, v115, v115
	v_mul_f32_e32 v125, v117, v117
	v_fmac_f32_e32 v124, v114, v114
	v_fmac_f32_e32 v125, v116, v116
	v_add_f32_e32 v124, v124, v125
	v_add_f32_e32 v123, v123, v124
	v_add_f32_e32 v124, v54, v55
	v_add_f32_e32 v125, v56, v57
	v_add_f32_e32 v124, v124, v125
	v_add_f32_e32 v122, v124, v122
	v_mul_f32_e32 v124, v55, v55
	v_mul_f32_e32 v125, v57, v57
	v_fmac_f32_e32 v124, v54, v54
	v_fmac_f32_e32 v125, v56, v56
	v_add_f32_e32 v124, v124, v125
	v_add_f32_e32 v123, v124, v123
	v_add_f32_e32 v124, v50, v51
	v_add_f32_e32 v125, v52, v53
	v_add_f32_e32 v124, v124, v125
	v_add_f32_e32 v122, v124, v122
	v_mul_f32_e32 v124, v51, v51
	v_mul_f32_e32 v125, v53, v53
	v_fmac_f32_e32 v124, v50, v50
	v_fmac_f32_e32 v125, v52, v52
	v_add_f32_e32 v124, v124, v125
	v_add_f32_e32 v124, v124, v123
	ds_swizzle_b32 v123, v122 offset:swizzle(SWAP,16)
	ds_swizzle_b32 v125, v124 offset:swizzle(SWAP,16)
	s_waitcnt lgkmcnt(1)
	v_add_f32_e32 v123, v122, v123
	s_waitcnt lgkmcnt(0)
	v_add_f32_e32 v122, v124, v125
	v_mov_b32_e32 v125, v123
	v_mov_b32_e32 v124, v122
	s_nop 0
	v_permlane32_swap_b32_e32 v123, v125
	v_permlane32_swap_b32_e32 v122, v124
	s_and_saveexec_b64 s[26:27], vcc
	s_cbranch_execz .LBB0_421
	v_add_f32_e32 v122, v122, v124
	v_add_f32_e32 v123, v123, v125
	s_lshl_b32 s8, s30, 11
	v_mul_f32_e32 v124, 0x3c800000, v123
	v_fma_f32 v122, -v123, v124, v122
	s_add_i32 s8, s7, s8
	v_max_f32_e32 v125, 0, v122
	v_lshl_add_u32 v122, v0, 5, s8
	ds_write_b64 v122, v[124:125] offset:512
.LBB0_421:
	s_or_b64 exec, exec, s[26:27]
	v_add_f32_e32 v122, v110, v111
	v_add_f32_e32 v123, v112, v113
	v_add_f32_e32 v122, v122, v123
	v_mul_f32_e32 v123, v111, v111
	v_mul_f32_e32 v124, v113, v113
	v_fmac_f32_e32 v123, v110, v110
	v_fmac_f32_e32 v124, v112, v112
	v_add_f32_e32 v123, v123, v124
	v_add_f32_e32 v124, v106, v107
	v_add_f32_e32 v125, v108, v109
	v_add_f32_e32 v122, 0, v122
	v_add_f32_e32 v124, v124, v125
	v_add_f32_e32 v122, v124, v122
	v_mul_f32_e32 v124, v107, v107
	v_mul_f32_e32 v125, v109, v109
	v_fmac_f32_e32 v124, v106, v106
	v_fmac_f32_e32 v125, v108, v108
	v_add_f32_e32 v124, v124, v125
	v_add_f32_e32 v123, v123, v124
	v_add_f32_e32 v124, v46, v47
	v_add_f32_e32 v125, v48, v49
	v_add_f32_e32 v124, v124, v125
	v_add_f32_e32 v122, v124, v122
	v_mul_f32_e32 v124, v47, v47
	v_mul_f32_e32 v125, v49, v49
	v_fmac_f32_e32 v124, v46, v46
	v_fmac_f32_e32 v125, v48, v48
	v_add_f32_e32 v124, v124, v125
	v_add_f32_e32 v123, v124, v123
	v_add_f32_e32 v124, v42, v43
	v_add_f32_e32 v125, v44, v45
	v_add_f32_e32 v124, v124, v125
	v_add_f32_e32 v122, v124, v122
	v_mul_f32_e32 v124, v43, v43
	v_mul_f32_e32 v125, v45, v45
	v_fmac_f32_e32 v124, v42, v42
	v_fmac_f32_e32 v125, v44, v44
	v_add_f32_e32 v124, v124, v125
	v_add_f32_e32 v124, v124, v123
	ds_swizzle_b32 v123, v122 offset:swizzle(SWAP,16)
	ds_swizzle_b32 v125, v124 offset:swizzle(SWAP,16)
	s_waitcnt lgkmcnt(1)
	v_add_f32_e32 v123, v122, v123
	s_waitcnt lgkmcnt(0)
	v_add_f32_e32 v122, v124, v125
	v_mov_b32_e32 v125, v123
	v_mov_b32_e32 v124, v122
	s_nop 0
	v_permlane32_swap_b32_e32 v123, v125
	v_permlane32_swap_b32_e32 v122, v124
	s_and_saveexec_b64 s[26:27], vcc
	s_cbranch_execz .LBB0_423
	v_add_f32_e32 v122, v122, v124
	v_add_f32_e32 v123, v123, v125
	s_lshl_b32 s8, s30, 11
	v_mul_f32_e32 v124, 0x3c800000, v123
	v_fma_f32 v122, -v123, v124, v122
	s_add_i32 s8, s7, s8
	v_max_f32_e32 v125, 0, v122
	v_lshl_add_u32 v122, v0, 5, s8
	ds_write_b64 v122, v[124:125] offset:1024
.LBB0_423:
	s_or_b64 exec, exec, s[26:27]
	v_add_f32_e32 v122, v102, v103
	v_add_f32_e32 v123, v104, v105
	v_add_f32_e32 v122, v122, v123
	v_mul_f32_e32 v123, v103, v103
	v_mul_f32_e32 v124, v105, v105
	v_fmac_f32_e32 v123, v102, v102
	v_fmac_f32_e32 v124, v104, v104
	v_add_f32_e32 v123, v123, v124
	v_add_f32_e32 v124, v98, v99
	v_add_f32_e32 v125, v100, v101
	v_add_f32_e32 v122, 0, v122
	v_add_f32_e32 v124, v124, v125
	v_add_f32_e32 v122, v124, v122
	v_mul_f32_e32 v124, v99, v99
	v_mul_f32_e32 v125, v101, v101
	v_fmac_f32_e32 v124, v98, v98
	v_fmac_f32_e32 v125, v100, v100
	v_add_f32_e32 v124, v124, v125
	v_add_f32_e32 v123, v123, v124
	v_add_f32_e32 v124, v38, v39
	v_add_f32_e32 v125, v40, v41
	v_add_f32_e32 v124, v124, v125
	v_add_f32_e32 v122, v124, v122
	v_mul_f32_e32 v124, v39, v39
	v_mul_f32_e32 v125, v41, v41
	v_fmac_f32_e32 v124, v38, v38
	v_fmac_f32_e32 v125, v40, v40
	v_add_f32_e32 v124, v124, v125
	v_add_f32_e32 v123, v124, v123
	v_add_f32_e32 v124, v34, v35
	v_add_f32_e32 v125, v36, v37
	v_add_f32_e32 v124, v124, v125
	v_add_f32_e32 v122, v124, v122
	v_mul_f32_e32 v124, v35, v35
	v_mul_f32_e32 v125, v37, v37
	v_fmac_f32_e32 v124, v34, v34
	v_fmac_f32_e32 v125, v36, v36
	v_add_f32_e32 v124, v124, v125
	v_add_f32_e32 v124, v124, v123
	ds_swizzle_b32 v123, v122 offset:swizzle(SWAP,16)
	ds_swizzle_b32 v125, v124 offset:swizzle(SWAP,16)
	s_waitcnt lgkmcnt(1)
	v_add_f32_e32 v123, v122, v123
	s_waitcnt lgkmcnt(0)
	v_add_f32_e32 v122, v124, v125
	v_mov_b32_e32 v125, v123
	v_mov_b32_e32 v124, v122
	s_nop 0
	v_permlane32_swap_b32_e32 v123, v125
	v_permlane32_swap_b32_e32 v122, v124
	s_and_saveexec_b64 s[26:27], vcc
	s_cbranch_execz .LBB0_425
	v_add_f32_e32 v122, v122, v124
	v_add_f32_e32 v123, v123, v125
	s_lshl_b32 s8, s30, 11
	v_mul_f32_e32 v124, 0x3c800000, v123
	v_fma_f32 v122, -v123, v124, v122
	s_add_i32 s8, s7, s8
	v_max_f32_e32 v125, 0, v122
	v_lshl_add_u32 v122, v0, 5, s8
	ds_write_b64 v122, v[124:125] offset:1536
.LBB0_425:
	s_or_b64 exec, exec, s[26:27]
	v_add_f32_e32 v122, v94, v95
	v_add_f32_e32 v123, v96, v97
	v_add_f32_e32 v122, v122, v123
	v_mul_f32_e32 v123, v95, v95
	v_mul_f32_e32 v124, v97, v97
	v_fmac_f32_e32 v123, v94, v94
	v_fmac_f32_e32 v124, v96, v96
	v_add_f32_e32 v123, v123, v124
	v_add_f32_e32 v124, v90, v91
	v_add_f32_e32 v125, v92, v93
	v_add_f32_e32 v122, 0, v122
	v_add_f32_e32 v124, v124, v125
	v_add_f32_e32 v122, v124, v122
	v_mul_f32_e32 v124, v91, v91
	v_mul_f32_e32 v125, v93, v93
	v_fmac_f32_e32 v124, v90, v90
	v_fmac_f32_e32 v125, v92, v92
	v_add_f32_e32 v124, v124, v125
	v_add_f32_e32 v123, v123, v124
	v_add_f32_e32 v124, v30, v31
	v_add_f32_e32 v125, v32, v33
	v_add_f32_e32 v124, v124, v125
	v_add_f32_e32 v122, v124, v122
	v_mul_f32_e32 v124, v31, v31
	v_mul_f32_e32 v125, v33, v33
	v_fmac_f32_e32 v124, v30, v30
	v_fmac_f32_e32 v125, v32, v32
	v_add_f32_e32 v124, v124, v125
	v_add_f32_e32 v123, v124, v123
	v_add_f32_e32 v124, v26, v27
	v_add_f32_e32 v125, v28, v29
	v_add_f32_e32 v124, v124, v125
	v_add_f32_e32 v122, v124, v122
	v_mul_f32_e32 v124, v27, v27
	v_mul_f32_e32 v125, v29, v29
	v_fmac_f32_e32 v124, v26, v26
	v_fmac_f32_e32 v125, v28, v28
	v_add_f32_e32 v124, v124, v125
	v_add_f32_e32 v124, v124, v123
	ds_swizzle_b32 v123, v122 offset:swizzle(SWAP,16)
	ds_swizzle_b32 v125, v124 offset:swizzle(SWAP,16)
	s_waitcnt lgkmcnt(1)
	v_add_f32_e32 v123, v122, v123
	s_waitcnt lgkmcnt(0)
	v_add_f32_e32 v122, v124, v125
	v_mov_b32_e32 v125, v123
	v_mov_b32_e32 v124, v122
	s_nop 0
	v_permlane32_swap_b32_e32 v123, v125
	v_permlane32_swap_b32_e32 v122, v124
	s_and_saveexec_b64 s[26:27], vcc
	s_cbranch_execz .LBB0_427
	v_add_f32_e32 v122, v122, v124
	v_add_f32_e32 v123, v123, v125
	s_lshl_b32 s8, s30, 11
	v_mul_f32_e32 v124, 0x3c800000, v123
	v_fma_f32 v122, -v123, v124, v122
	s_add_i32 s8, s7, s8
	v_max_f32_e32 v125, 0, v122
	v_lshl_add_u32 v122, v0, 5, s8
	ds_write_b64 v122, v[124:125] offset:4096
.LBB0_427:
	s_or_b64 exec, exec, s[26:27]
	v_add_f32_e32 v122, v86, v87
	v_add_f32_e32 v123, v88, v89
	v_add_f32_e32 v122, v122, v123
	v_mul_f32_e32 v123, v87, v87
	v_mul_f32_e32 v124, v89, v89
	v_fmac_f32_e32 v123, v86, v86
	v_fmac_f32_e32 v124, v88, v88
	v_add_f32_e32 v123, v123, v124
	v_add_f32_e32 v124, v82, v83
	v_add_f32_e32 v125, v84, v85
	v_add_f32_e32 v122, 0, v122
	v_add_f32_e32 v124, v124, v125
	v_add_f32_e32 v122, v124, v122
	v_mul_f32_e32 v124, v83, v83
	v_mul_f32_e32 v125, v85, v85
	v_fmac_f32_e32 v124, v82, v82
	v_fmac_f32_e32 v125, v84, v84
	v_add_f32_e32 v124, v124, v125
	v_add_f32_e32 v123, v123, v124
	v_add_f32_e32 v124, v22, v23
	v_add_f32_e32 v125, v24, v25
	v_add_f32_e32 v124, v124, v125
	v_add_f32_e32 v122, v124, v122
	v_mul_f32_e32 v124, v23, v23
	v_mul_f32_e32 v125, v25, v25
	v_fmac_f32_e32 v124, v22, v22
	v_fmac_f32_e32 v125, v24, v24
	v_add_f32_e32 v124, v124, v125
	v_add_f32_e32 v123, v124, v123
	v_add_f32_e32 v124, v18, v19
	v_add_f32_e32 v125, v20, v21
	v_add_f32_e32 v124, v124, v125
	v_add_f32_e32 v122, v124, v122
	v_mul_f32_e32 v124, v19, v19
	v_mul_f32_e32 v125, v21, v21
	v_fmac_f32_e32 v124, v18, v18
	v_fmac_f32_e32 v125, v20, v20
	v_add_f32_e32 v124, v124, v125
	v_add_f32_e32 v124, v124, v123
	ds_swizzle_b32 v123, v122 offset:swizzle(SWAP,16)
	ds_swizzle_b32 v125, v124 offset:swizzle(SWAP,16)
	s_waitcnt lgkmcnt(1)
	v_add_f32_e32 v123, v122, v123
	s_waitcnt lgkmcnt(0)
	v_add_f32_e32 v122, v124, v125
	v_mov_b32_e32 v125, v123
	v_mov_b32_e32 v124, v122
	s_nop 0
	v_permlane32_swap_b32_e32 v123, v125
	v_permlane32_swap_b32_e32 v122, v124
	s_and_saveexec_b64 s[26:27], vcc
	s_cbranch_execz .LBB0_429
	v_add_f32_e32 v122, v122, v124
	v_add_f32_e32 v123, v123, v125
	s_lshl_b32 s8, s30, 11
	v_mul_f32_e32 v124, 0x3c800000, v123
	v_fma_f32 v122, -v123, v124, v122
	s_add_i32 s8, s7, s8
	v_max_f32_e32 v125, 0, v122
	v_lshl_add_u32 v122, v0, 5, s8
	ds_write_b64 v122, v[124:125] offset:4608
.LBB0_429:
	s_or_b64 exec, exec, s[26:27]
	v_add_f32_e32 v122, v78, v79
	v_add_f32_e32 v123, v80, v81
	v_add_f32_e32 v122, v122, v123
	v_mul_f32_e32 v123, v79, v79
	v_mul_f32_e32 v124, v81, v81
	v_fmac_f32_e32 v123, v78, v78
	v_fmac_f32_e32 v124, v80, v80
	v_add_f32_e32 v123, v123, v124
	v_add_f32_e32 v124, v74, v75
	v_add_f32_e32 v125, v76, v77
	v_add_f32_e32 v122, 0, v122
	v_add_f32_e32 v124, v124, v125
	v_add_f32_e32 v122, v124, v122
	v_mul_f32_e32 v124, v75, v75
	v_mul_f32_e32 v125, v77, v77
	v_fmac_f32_e32 v124, v74, v74
	v_fmac_f32_e32 v125, v76, v76
	v_add_f32_e32 v124, v124, v125
	v_add_f32_e32 v123, v123, v124
	v_add_f32_e32 v124, v14, v15
	v_add_f32_e32 v125, v16, v17
	v_add_f32_e32 v124, v124, v125
	v_add_f32_e32 v122, v124, v122
	v_mul_f32_e32 v124, v15, v15
	v_mul_f32_e32 v125, v17, v17
	v_fmac_f32_e32 v124, v14, v14
	v_fmac_f32_e32 v125, v16, v16
	v_add_f32_e32 v124, v124, v125
	v_add_f32_e32 v123, v124, v123
	v_add_f32_e32 v124, v10, v11
	v_add_f32_e32 v125, v12, v13
	v_add_f32_e32 v124, v124, v125
	v_add_f32_e32 v122, v124, v122
	v_mul_f32_e32 v124, v11, v11
	v_mul_f32_e32 v125, v13, v13
	v_fmac_f32_e32 v124, v10, v10
	v_fmac_f32_e32 v125, v12, v12
	v_add_f32_e32 v124, v124, v125
	v_add_f32_e32 v124, v124, v123
	ds_swizzle_b32 v123, v122 offset:swizzle(SWAP,16)
	ds_swizzle_b32 v125, v124 offset:swizzle(SWAP,16)
	s_waitcnt lgkmcnt(1)
	v_add_f32_e32 v123, v122, v123
	s_waitcnt lgkmcnt(0)
	v_add_f32_e32 v122, v124, v125
	v_mov_b32_e32 v125, v123
	v_mov_b32_e32 v124, v122
	s_nop 0
	v_permlane32_swap_b32_e32 v123, v125
	v_permlane32_swap_b32_e32 v122, v124
	s_and_saveexec_b64 s[26:27], vcc
	s_cbranch_execz .LBB0_431
	v_add_f32_e32 v122, v122, v124
	v_add_f32_e32 v123, v123, v125
	s_lshl_b32 s8, s30, 11
	v_mul_f32_e32 v124, 0x3c800000, v123
	v_fma_f32 v122, -v123, v124, v122
	s_add_i32 s8, s7, s8
	v_max_f32_e32 v125, 0, v122
	v_lshl_add_u32 v122, v0, 5, s8
	ds_write_b64 v122, v[124:125] offset:5120
.LBB0_431:
	s_or_b64 exec, exec, s[26:27]
	v_add_f32_e32 v122, v70, v71
	v_add_f32_e32 v123, v72, v73
	v_add_f32_e32 v122, v122, v123
	v_mul_f32_e32 v123, v71, v71
	v_mul_f32_e32 v124, v73, v73
	v_fmac_f32_e32 v123, v70, v70
	v_fmac_f32_e32 v124, v72, v72
	v_add_f32_e32 v123, v123, v124
	v_add_f32_e32 v124, v66, v67
	v_add_f32_e32 v125, v68, v69
	v_add_f32_e32 v122, 0, v122
	v_add_f32_e32 v124, v124, v125
	v_add_f32_e32 v122, v124, v122
	v_mul_f32_e32 v124, v67, v67
	v_mul_f32_e32 v125, v69, v69
	v_fmac_f32_e32 v124, v66, v66
	v_fmac_f32_e32 v125, v68, v68
	v_add_f32_e32 v124, v124, v125
	v_add_f32_e32 v123, v123, v124
	v_add_f32_e32 v124, v6, v7
	v_add_f32_e32 v125, v8, v9
	v_add_f32_e32 v124, v124, v125
	v_add_f32_e32 v122, v124, v122
	v_mul_f32_e32 v124, v7, v7
	v_mul_f32_e32 v125, v9, v9
	v_fmac_f32_e32 v124, v6, v6
	v_fmac_f32_e32 v125, v8, v8
	v_add_f32_e32 v124, v124, v125
	v_add_f32_e32 v123, v124, v123
	v_add_f32_e32 v124, v2, v3
	v_add_f32_e32 v125, v4, v5
	v_add_f32_e32 v124, v124, v125
	v_add_f32_e32 v122, v124, v122
	v_mul_f32_e32 v124, v3, v3
	v_mul_f32_e32 v125, v5, v5
	v_fmac_f32_e32 v124, v2, v2
	v_fmac_f32_e32 v125, v4, v4
	v_add_f32_e32 v124, v124, v125
	v_add_f32_e32 v124, v124, v123
	ds_swizzle_b32 v123, v122 offset:swizzle(SWAP,16)
	ds_swizzle_b32 v125, v124 offset:swizzle(SWAP,16)
	s_waitcnt lgkmcnt(1)
	v_add_f32_e32 v123, v122, v123
	s_waitcnt lgkmcnt(0)
	v_add_f32_e32 v122, v124, v125
	v_mov_b32_e32 v125, v123
	v_mov_b32_e32 v124, v122
	s_nop 0
	v_permlane32_swap_b32_e32 v123, v125
	v_permlane32_swap_b32_e32 v122, v124
	s_and_saveexec_b64 s[26:27], vcc
	s_cbranch_execz .LBB0_433
	v_add_f32_e32 v122, v122, v124
	v_add_f32_e32 v123, v123, v125
	s_lshl_b32 s8, s30, 11
	v_mul_f32_e32 v124, 0x3c800000, v123
	v_fma_f32 v122, -v123, v124, v122
	s_add_i32 s7, s7, s8
	v_max_f32_e32 v125, 0, v122
	v_lshl_add_u32 v0, v0, 5, s7
	ds_write_b64 v0, v[124:125] offset:5632
.LBB0_433:
	s_or_b64 exec, exec, s[26:27]
	v_or_b32_e32 v0, s1, v219
	v_cmp_eq_u32_e32 vcc, 0, v0
	s_and_saveexec_b64 s[26:27], vcc
	ds_write_b32 v1, v1 offset:10240
	s_or_b64 exec, exec, s[26:27]
	s_waitcnt lgkmcnt(0)
	s_barrier
	v_cmp_gt_i32_e32 vcc, 32, v219
	s_and_saveexec_b64 s[26:27], vcc
	s_cbranch_execz .LBB0_446
	s_lshl_b32 s1, s1, 5
	v_and_or_b32 v122, v219, 31, s1
	v_lshl_add_u32 v0, v122, 5, 0
	ds_read_b128 v[124:127], v0
	ds_read_b128 v[138:141], v0 offset:16
	s_ashr_i32 s1, s0, 31
	s_lshl_b64 s[0:1], s[0:1], 14
	s_add_u32 s0, s39, s0
	s_waitcnt lgkmcnt(1)
	v_add_f32_e32 v123, v124, v126
	s_waitcnt lgkmcnt(0)
	v_add_f32_e32 v123, v123, v138
	v_add_f32_e32 v123, v123, v140
	v_fmamk_f32 v124, v123, 0xbe800000, v124
	v_fmac_f32_e32 v126, 0xbe800000, v123
	v_fmamk_f32 v128, v123, 0xbe800000, v138
	v_fmac_f32_e32 v140, 0xbe800000, v123
	v_mul_f32_e32 v129, v124, v124
	v_mul_f32_e32 v145, v126, v126
	v_mul_f32_e32 v147, v128, v128
	v_mul_f32_e32 v149, v140, v140
	v_mov_b32_e32 v128, v125
	v_mov_b32_e32 v144, v127
	v_mov_b32_e32 v146, v139
	v_mov_b32_e32 v148, v141
	v_add_f32_e32 v124, v128, v144
	v_add_f32_e32 v125, v129, v145
	v_add_f32_e32 v126, v146, v148
	v_add_f32_e32 v127, v147, v149
	v_mul_f32_e32 v142, 0x3e800000, v123
	v_add_f32_e32 v124, v124, v126
	v_add_f32_e32 v125, v125, v127
	s_addc_u32 s1, s17, s1
	v_fmac_f32_e32 v124, 0x42800000, v125
	v_ashrrev_i32_e32 v123, 31, v122
	v_lshl_add_u64 v[128:129], v[122:123], 3, s[0:1]
	s_ashr_i32 s7, s6, 31
	v_and_b32_e32 v123, 0xffffffe0, v124
	s_mov_b64 s[0:1], 0x1000
	v_lshl_add_u64 v[126:127], s[6:7], 3, v[128:129]
	v_or_b32_e32 v143, s38, v123
	v_lshl_add_u64 v[140:141], v[128:129], 0, s[0:1]
	s_mov_b64 s[0:1], 0x1800
	global_store_dwordx2 v[126:127], v[142:143], off sc1
	s_memrealtime s[28:29]
	v_lshl_add_u64 v[142:143], v[128:129], 0, s[0:1]
	s_mov_b64 s[0:1], 0x2000
	v_lshl_add_u64 v[146:147], v[128:129], 0, s[0:1]
	s_mov_b64 s[0:1], 0x2800
	v_lshl_add_u64 v[148:149], v[128:129], 0, s[0:1]
	s_mov_b64 s[0:1], 0x3000
	v_lshl_add_u64 v[150:151], v[128:129], 0, s[0:1]
	s_mov_b64 s[0:1], 0x3800
	v_lshl_add_u64 v[152:153], v[128:129], 0, s[0:1]
	s_mov_b64 s[6:7], 0
	s_branch .LBB0_439

.LBB0_578:
	v_and_b32_e32 v183, 63, v126
	v_bfe_u32 v184, v126, 4, 2
	s_lshl_b32 s5, s9, 5
	s_lshl_b32 s4, s11, 8
	s_barrier
	s_or_b32 s5, s4, s5
	v_add_u32_e32 v182, s40, v0
	v_lshl_add_u32 v162, v184, 3, s5
	v_lshl_add_u32 v178, s0, 8, v182
	v_ashrrev_i32_e32 v163, 31, v162
	v_ashrrev_i32_e32 v179, 31, v178
	v_lshl_add_u64 v[180:181], v[162:163], 2, s[22:23]
	v_lshlrev_b64 v[126:127], 13, v[178:179]
	v_add_u32_e32 v174, 16, v178
	s_mov_b32 s6, 0.5
	s_mov_b32 s24, 0x3fd744fd
	s_mov_b32 s5, s26
	v_lshl_add_u64 v[134:135], v[180:181], 0, v[126:127]
	v_ashrrev_i32_e32 v175, 31, v174
	global_load_dwordx4 v[126:129], v[134:135], off offset:16
	global_load_dwordx4 v[154:157], v[134:135], off
	global_load_dwordx4 v[158:161], v[134:135], off offset:528
	global_load_dwordx4 v[164:167], v[134:135], off offset:512
	v_lshlrev_b64 v[134:135], 13, v[174:175]
	v_lshl_add_u64 v[134:135], v[180:181], 0, v[134:135]
	global_load_dwordx4 v[186:189], v[134:135], off offset:16
	global_load_dwordx4 v[190:193], v[134:135], off
	global_load_dwordx4 v[194:197], v[134:135], off offset:528
	global_load_dwordx4 v[198:201], v[134:135], off offset:512
	v_add_u32_e32 v172, 32, v178
	v_ashrrev_i32_e32 v173, 31, v172
	v_lshlrev_b64 v[134:135], 13, v[172:173]
	v_lshl_add_u64 v[134:135], v[180:181], 0, v[134:135]
	global_load_dwordx4 v[204:207], v[134:135], off offset:16
	global_load_dwordx4 v[208:211], v[134:135], off
	global_load_dwordx4 v[150:153], v[134:135], off offset:528
	global_load_dwordx4 v[212:215], v[134:135], off offset:512
	v_add_u32_e32 v170, 48, v178
	v_ashrrev_i32_e32 v171, 31, v170
	v_lshlrev_b64 v[134:135], 13, v[170:171]
	v_lshl_add_u64 v[142:143], v[180:181], 0, v[134:135]
	global_load_dwordx4 v[138:141], v[142:143], off offset:16
	global_load_dwordx4 v[146:149], v[142:143], off
	global_load_dwordx4 v[134:137], v[142:143], off offset:528
	s_nop 0
	global_load_dwordx4 v[142:145], v[142:143], off offset:512
	v_pk_mul_f32 v[118:119], v[118:119], s[6:7] op_sel_hi:[1,0]
	v_pk_mul_f32 v[120:121], v[120:121], s[6:7] op_sel_hi:[1,0]
	v_pk_mul_f32 v[122:123], v[122:123], s[6:7] op_sel_hi:[1,0]
	v_add_u32_e32 v176, 0x80, v178
	v_pk_mul_f32 v[124:125], v[124:125], s[6:7] op_sel_hi:[1,0]
	v_pk_mul_f32 v[30:31], v[30:31], s[6:7] op_sel_hi:[1,0]
	v_pk_mul_f32 v[32:33], v[32:33], s[6:7] op_sel_hi:[1,0]
	v_ashrrev_i32_e32 v177, 31, v176
	v_add_u32_e32 v168, 0x90, v178
	v_ashrrev_i32_e32 v169, 31, v168
	s_lshl_b32 s5, s9, 3
	v_cmp_eq_u32_e32 vcc, 0, v184
	s_add_i32 s5, s5, 0
	s_waitcnt vmcnt(15)
	v_pk_fma_f32 v[126:127], v[126:127], s[24:25], v[118:119] op_sel_hi:[1,0,1]
	v_pk_fma_f32 v[128:129], v[128:129], s[24:25], v[120:121] op_sel_hi:[1,0,1]
	s_waitcnt vmcnt(13)
	v_mul_f32_e32 v118, s24, v160
	v_mul_f32_e32 v119, s24, v161
	v_mul_f32_e32 v120, s24, v158
	v_mul_f32_e32 v121, s24, v159
	v_pk_fma_f32 v[36:37], v[36:37], s[6:7], v[118:119] op_sel_hi:[1,0,1]
	s_waitcnt vmcnt(10)
	v_mul_f32_e32 v118, s24, v192
	v_mul_f32_e32 v119, s24, v193
	v_pk_fma_f32 v[122:123], v[154:155], s[24:25], v[122:123] op_sel_hi:[1,0,1]
	v_pk_fma_f32 v[34:35], v[34:35], s[6:7], v[120:121] op_sel_hi:[1,0,1]
	v_mul_f32_e32 v120, s24, v190
	v_mul_f32_e32 v121, s24, v191
	v_pk_fma_f32 v[116:117], v[116:117], s[6:7], v[118:119] op_sel_hi:[1,0,1]
	v_mul_f32_e32 v118, s24, v188
	v_mul_f32_e32 v119, s24, v189
	v_mul_f32_e32 v154, s24, v186
	v_mul_f32_e32 v155, s24, v187
	v_pk_fma_f32 v[114:115], v[114:115], s[6:7], v[120:121] op_sel_hi:[1,0,1]
	v_pk_fma_f32 v[120:121], v[112:113], s[6:7], v[118:119] op_sel_hi:[1,0,1]
	v_pk_fma_f32 v[118:119], v[110:111], s[6:7], v[154:155] op_sel_hi:[1,0,1]
	s_waitcnt vmcnt(8)
	v_mul_f32_e32 v110, s24, v200
	v_mul_f32_e32 v111, s24, v201
	v_mul_f32_e32 v112, s24, v198
	v_mul_f32_e32 v113, s24, v199
	v_pk_fma_f32 v[12:13], v[12:13], s[6:7], v[110:111] op_sel_hi:[1,0,1]
	v_mul_f32_e32 v110, s24, v196
	v_mul_f32_e32 v111, s24, v197
	v_pk_fma_f32 v[10:11], v[10:11], s[6:7], v[112:113] op_sel_hi:[1,0,1]
	v_mul_f32_e32 v112, s24, v194
	v_mul_f32_e32 v113, s24, v195
	v_pk_fma_f32 v[16:17], v[16:17], s[6:7], v[110:111] op_sel_hi:[1,0,1]
	s_waitcnt vmcnt(6)
	v_mul_f32_e32 v110, s24, v210
	v_mul_f32_e32 v111, s24, v211
	v_pk_fma_f32 v[14:15], v[14:15], s[6:7], v[112:113] op_sel_hi:[1,0,1]
	v_mul_f32_e32 v112, s24, v208
	v_mul_f32_e32 v113, s24, v209
	v_pk_fma_f32 v[100:101], v[100:101], s[6:7], v[110:111] op_sel_hi:[1,0,1]
	v_mul_f32_e32 v110, s24, v206
	v_mul_f32_e32 v111, s24, v207
	v_mul_f32_e32 v154, s24, v204
	v_mul_f32_e32 v155, s24, v205
	v_pk_fma_f32 v[98:99], v[98:99], s[6:7], v[112:113] op_sel_hi:[1,0,1]
	v_pk_fma_f32 v[112:113], v[108:109], s[6:7], v[110:111] op_sel_hi:[1,0,1]
	v_pk_fma_f32 v[110:111], v[106:107], s[6:7], v[154:155] op_sel_hi:[1,0,1]
	s_waitcnt vmcnt(4)
	v_mul_f32_e32 v106, s24, v214
	v_mul_f32_e32 v107, s24, v215
	v_mul_f32_e32 v108, s24, v212
	v_mul_f32_e32 v109, s24, v213
	v_pk_fma_f32 v[20:21], v[20:21], s[6:7], v[106:107] op_sel_hi:[1,0,1]
	v_mul_f32_e32 v106, s24, v152
	v_mul_f32_e32 v107, s24, v153
	v_pk_fma_f32 v[18:19], v[18:19], s[6:7], v[108:109] op_sel_hi:[1,0,1]
	v_mul_f32_e32 v108, s24, v150
	v_mul_f32_e32 v109, s24, v151
	v_pk_fma_f32 v[24:25], v[24:25], s[6:7], v[106:107] op_sel_hi:[1,0,1]
	s_waitcnt vmcnt(2)
	v_mul_f32_e32 v106, s24, v148
	v_mul_f32_e32 v107, s24, v149
	v_pk_fma_f32 v[22:23], v[22:23], s[6:7], v[108:109] op_sel_hi:[1,0,1]
	v_mul_f32_e32 v108, s24, v146
	v_mul_f32_e32 v109, s24, v147
	v_pk_fma_f32 v[104:105], v[104:105], s[6:7], v[106:107] op_sel_hi:[1,0,1]
	v_mul_f32_e32 v106, s24, v140
	v_mul_f32_e32 v107, s24, v141
	v_mul_f32_e32 v138, s24, v138
	v_mul_f32_e32 v139, s24, v139
	v_pk_fma_f32 v[102:103], v[102:103], s[6:7], v[108:109] op_sel_hi:[1,0,1]
	v_pk_fma_f32 v[108:109], v[4:5], s[6:7], v[106:107] op_sel_hi:[1,0,1]
	v_pk_fma_f32 v[106:107], v[2:3], s[6:7], v[138:139] op_sel_hi:[1,0,1]
	s_waitcnt vmcnt(0)
	v_mul_f32_e32 v2, s24, v144
	v_mul_f32_e32 v3, s24, v145
	v_mul_f32_e32 v138, s24, v142
	v_mul_f32_e32 v139, s24, v143
	v_pk_fma_f32 v[4:5], v[96:97], s[6:7], v[2:3] op_sel_hi:[1,0,1]
	v_pk_fma_f32 v[2:3], v[94:95], s[6:7], v[138:139] op_sel_hi:[1,0,1]
	v_mul_f32_e32 v94, s24, v136
	v_mul_f32_e32 v95, s24, v137
	v_mul_f32_e32 v96, s24, v134
	v_mul_f32_e32 v97, s24, v135
	v_pk_fma_f32 v[124:125], v[156:157], s[24:25], v[124:125] op_sel_hi:[1,0,1]
	v_pk_fma_f32 v[32:33], s[24:25], v[166:167], v[32:33] op_sel_hi:[0,1,1]
	v_pk_fma_f32 v[30:31], s[24:25], v[164:165], v[30:31] op_sel_hi:[0,1,1]
	v_pk_fma_f32 v[8:9], v[8:9], s[6:7], v[94:95] op_sel_hi:[1,0,1]
	v_pk_fma_f32 v[6:7], v[6:7], s[6:7], v[96:97] op_sel_hi:[1,0,1]
	v_lshlrev_b64 v[94:95], 13, v[176:177]
	v_lshl_add_u64 v[94:95], v[180:181], 0, v[94:95]
	global_load_dwordx4 v[186:189], v[94:95], off offset:16
	global_load_dwordx4 v[190:193], v[94:95], off
	global_load_dwordx4 v[194:197], v[94:95], off offset:528
	global_load_dwordx4 v[198:201], v[94:95], off offset:512
	v_lshlrev_b64 v[94:95], 13, v[168:169]
	v_add_u32_e32 v166, 0xa0, v178
	v_lshl_add_u64 v[94:95], v[180:181], 0, v[94:95]
	v_ashrrev_i32_e32 v167, 31, v166
	global_load_dwordx4 v[204:207], v[94:95], off offset:16
	global_load_dwordx4 v[208:211], v[94:95], off
	global_load_dwordx4 v[212:215], v[94:95], off offset:528
	global_load_dwordx4 v[216:219], v[94:95], off offset:512
	v_lshlrev_b64 v[94:95], 13, v[166:167]
	v_lshl_add_u64 v[134:135], v[180:181], 0, v[94:95]
	global_load_dwordx4 v[94:97], v[134:135], off offset:16
	global_load_dwordx4 v[158:161], v[134:135], off
	global_load_dwordx4 v[150:153], v[134:135], off offset:528
	global_load_dwordx4 v[154:157], v[134:135], off offset:512
	v_add_u32_e32 v164, 0xb0, v178
	v_ashrrev_i32_e32 v165, 31, v164
	v_lshlrev_b64 v[134:135], 13, v[164:165]
	v_lshl_add_u64 v[142:143], v[180:181], 0, v[134:135]
	global_load_dwordx4 v[138:141], v[142:143], off offset:16
	global_load_dwordx4 v[146:149], v[142:143], off
	global_load_dwordx4 v[134:137], v[142:143], off offset:528
	s_nop 0
	global_load_dwordx4 v[142:145], v[142:143], off offset:512
	s_waitcnt vmcnt(15)
	v_mul_f32_e32 v186, s24, v186
	v_mul_f32_e32 v187, s24, v187
	s_waitcnt vmcnt(14)
	v_mul_f32_e32 v180, s24, v192
	v_mul_f32_e32 v181, s24, v193
	v_pk_fma_f32 v[76:77], v[76:77], s[6:7], v[180:181] op_sel_hi:[1,0,1]
	v_mul_f32_e32 v180, s24, v188
	v_mul_f32_e32 v181, s24, v189
	v_pk_fma_f32 v[84:85], v[84:85], s[6:7], v[180:181] op_sel_hi:[1,0,1]
	v_pk_fma_f32 v[82:83], v[82:83], s[6:7], v[186:187] op_sel_hi:[1,0,1]
	s_waitcnt vmcnt(12)
	v_mul_f32_e32 v180, s24, v200
	v_mul_f32_e32 v181, s24, v201
	v_mul_f32_e32 v186, s24, v198
	v_mul_f32_e32 v187, s24, v199
	s_waitcnt vmcnt(7)
	v_mul_f32_e32 v94, s24, v94
	v_mul_f32_e32 v95, s24, v95
	v_mul_f32_e32 v96, s24, v96
	v_mul_f32_e32 v97, s24, v97
	v_pk_fma_f32 v[94:95], v[50:51], s[6:7], v[94:95] op_sel_hi:[1,0,1]
	s_waitcnt vmcnt(4)
	v_mul_f32_e32 v50, s24, v156
	v_mul_f32_e32 v51, s24, v157
	v_mul_f32_e32 v154, s24, v154
	v_mul_f32_e32 v155, s24, v155
	v_pk_fma_f32 v[96:97], v[52:53], s[6:7], v[96:97] op_sel_hi:[1,0,1]
	v_pk_fma_f32 v[52:53], v[88:89], s[6:7], v[50:51] op_sel_hi:[1,0,1]
	v_pk_fma_f32 v[50:51], v[86:87], s[6:7], v[154:155] op_sel_hi:[1,0,1]
	v_mul_f32_e32 v86, s24, v152
	v_mul_f32_e32 v87, s24, v153
	v_mul_f32_e32 v88, s24, v150
	v_mul_f32_e32 v89, s24, v151
	v_pk_fma_f32 v[56:57], v[56:57], s[6:7], v[86:87] op_sel_hi:[1,0,1]
	s_waitcnt vmcnt(2)
	v_mul_f32_e32 v86, s24, v148
	v_mul_f32_e32 v87, s24, v149
	v_pk_fma_f32 v[54:55], v[54:55], s[6:7], v[88:89] op_sel_hi:[1,0,1]
	v_mul_f32_e32 v88, s24, v146
	v_mul_f32_e32 v89, s24, v147
	v_pk_fma_f32 v[80:81], v[80:81], s[6:7], v[86:87] op_sel_hi:[1,0,1]
	v_mul_f32_e32 v86, s24, v140
	v_mul_f32_e32 v87, s24, v141
	v_mul_f32_e32 v138, s24, v138
	v_mul_f32_e32 v139, s24, v139
	v_pk_fma_f32 v[78:79], v[78:79], s[6:7], v[88:89] op_sel_hi:[1,0,1]
	v_pk_fma_f32 v[88:89], v[44:45], s[6:7], v[86:87] op_sel_hi:[1,0,1]
	v_pk_fma_f32 v[86:87], v[42:43], s[6:7], v[138:139] op_sel_hi:[1,0,1]
	s_waitcnt vmcnt(0)
	v_mul_f32_e32 v42, s24, v144
	v_mul_f32_e32 v43, s24, v145
	v_mul_f32_e32 v138, s24, v142
	v_mul_f32_e32 v139, s24, v143
	v_pk_fma_f32 v[44:45], v[132:133], s[6:7], v[42:43] op_sel_hi:[1,0,1]
	v_pk_fma_f32 v[42:43], v[130:131], s[6:7], v[138:139] op_sel_hi:[1,0,1]
	v_mul_f32_e32 v130, s24, v136
	v_mul_f32_e32 v131, s24, v137
	v_mul_f32_e32 v132, s24, v134
	v_mul_f32_e32 v133, s24, v135
	v_pk_fma_f32 v[48:49], v[48:49], s[6:7], v[130:131] op_sel_hi:[1,0,1]
	v_add_f32_e32 v130, v122, v123
	v_add_f32_e32 v131, v124, v125
	v_pk_fma_f32 v[46:47], v[46:47], s[6:7], v[132:133] op_sel_hi:[1,0,1]
	v_add_f32_e32 v130, v130, v131
	v_mul_f32_e32 v131, v123, v123
	v_mul_f32_e32 v132, v125, v125
	v_fmac_f32_e32 v131, v122, v122
	v_fmac_f32_e32 v132, v124, v124
	v_add_f32_e32 v131, v131, v132
	v_add_f32_e32 v132, v126, v127
	v_add_f32_e32 v133, v128, v129
	v_add_f32_e32 v130, 0, v130
	v_add_f32_e32 v132, v132, v133
	v_add_f32_e32 v130, v132, v130
	v_mul_f32_e32 v132, v127, v127
	v_mul_f32_e32 v133, v129, v129
	v_fmac_f32_e32 v132, v126, v126
	v_fmac_f32_e32 v133, v128, v128
	v_add_f32_e32 v132, v132, v133
	v_add_f32_e32 v131, v131, v132
	v_add_f32_e32 v132, v30, v31
	v_add_f32_e32 v133, v32, v33
	v_add_f32_e32 v132, v132, v133
	v_add_f32_e32 v130, v132, v130
	v_mul_f32_e32 v132, v31, v31
	v_mul_f32_e32 v133, v33, v33
	v_fmac_f32_e32 v132, v30, v30
	v_fmac_f32_e32 v133, v32, v32
	v_add_f32_e32 v132, v132, v133
	v_add_f32_e32 v131, v132, v131
	v_add_f32_e32 v132, v34, v35
	v_add_f32_e32 v133, v36, v37
	v_add_f32_e32 v132, v132, v133
	v_add_f32_e32 v130, v132, v130
	v_mul_f32_e32 v132, v35, v35
	v_mul_f32_e32 v133, v37, v37
	v_fmac_f32_e32 v132, v34, v34
	v_fmac_f32_e32 v133, v36, v36
	v_add_f32_e32 v132, v132, v133
	v_add_f32_e32 v132, v132, v131
	ds_swizzle_b32 v131, v130 offset:swizzle(SWAP,16)
	v_pk_fma_f32 v[28:29], v[28:29], s[6:7], v[180:181] op_sel_hi:[1,0,1]
	v_pk_fma_f32 v[26:27], v[26:27], s[6:7], v[186:187] op_sel_hi:[1,0,1]
	v_mul_f32_e32 v180, s24, v196
	v_mul_f32_e32 v181, s24, v197
	v_mul_f32_e32 v186, s24, v194
	v_mul_f32_e32 v187, s24, v195
	v_pk_fma_f32 v[40:41], v[40:41], s[6:7], v[180:181] op_sel_hi:[1,0,1]
	v_pk_fma_f32 v[38:39], v[38:39], s[6:7], v[186:187] op_sel_hi:[1,0,1]
	v_mul_f32_e32 v180, s24, v210
	v_mul_f32_e32 v181, s24, v211
	v_mul_f32_e32 v186, s24, v208
	v_mul_f32_e32 v187, s24, v209
	s_waitcnt lgkmcnt(0)
	v_add_f32_e32 v131, v130, v131
	ds_swizzle_b32 v130, v132 offset:swizzle(SWAP,16)
	v_pk_fma_f32 v[68:69], v[68:69], s[6:7], v[180:181] op_sel_hi:[1,0,1]
	v_pk_fma_f32 v[66:67], v[66:67], s[6:7], v[186:187] op_sel_hi:[1,0,1]
	v_mul_f32_e32 v180, s24, v206
	v_mul_f32_e32 v181, s24, v207
	v_mul_f32_e32 v186, s24, v204
	v_mul_f32_e32 v187, s24, v205
	v_pk_fma_f32 v[72:73], v[72:73], s[6:7], v[180:181] op_sel_hi:[1,0,1]
	v_pk_fma_f32 v[70:71], v[70:71], s[6:7], v[186:187] op_sel_hi:[1,0,1]
	v_mul_f32_e32 v180, s24, v218
	v_mul_f32_e32 v181, s24, v219
	v_mul_f32_e32 v186, s24, v216
	v_mul_f32_e32 v187, s24, v217
	v_mul_f32_e32 v190, s24, v190
	v_mul_f32_e32 v191, s24, v191
	v_pk_fma_f32 v[60:61], v[60:61], s[6:7], v[180:181] op_sel_hi:[1,0,1]
	v_pk_fma_f32 v[58:59], v[58:59], s[6:7], v[186:187] op_sel_hi:[1,0,1]
	v_mul_f32_e32 v180, s24, v214
	v_mul_f32_e32 v181, s24, v215
	v_mul_f32_e32 v186, s24, v212
	v_mul_f32_e32 v187, s24, v213
	v_mul_f32_e32 v160, s24, v160
	v_mul_f32_e32 v161, s24, v161
	v_mul_f32_e32 v158, s24, v158
	v_mul_f32_e32 v159, s24, v159
	v_pk_fma_f32 v[74:75], v[74:75], s[6:7], v[190:191] op_sel_hi:[1,0,1]
	v_pk_fma_f32 v[64:65], v[64:65], s[6:7], v[180:181] op_sel_hi:[1,0,1]
	v_pk_fma_f32 v[62:63], v[62:63], s[6:7], v[186:187] op_sel_hi:[1,0,1]
	v_pk_fma_f32 v[92:93], v[92:93], s[6:7], v[160:161] op_sel_hi:[1,0,1]
	v_pk_fma_f32 v[90:91], v[90:91], s[6:7], v[158:159] op_sel_hi:[1,0,1]
	s_waitcnt lgkmcnt(0)
	v_add_f32_e32 v130, v132, v130
	v_mov_b32_e32 v133, v131
	v_mov_b32_e32 v132, v130
	s_nop 0
	v_permlane32_swap_b32_e32 v131, v133
	v_permlane32_swap_b32_e32 v130, v132
	s_and_saveexec_b64 s[6:7], vcc
	s_mov_b64 s[52:53], 0x400
	s_mov_b32 s36, s17
	s_cbranch_execz .LBB0_580
	v_add_f32_e32 v130, v130, v132
	v_add_f32_e32 v131, v131, v133
	s_lshl_b32 s9, s8, 11
	v_mul_f32_e32 v132, 0x3c800000, v131
	v_fma_f32 v130, -v131, v132, v130
	s_add_i32 s9, s5, s9
	v_max_f32_e32 v133, 0, v130
	v_lshl_add_u32 v130, v0, 5, s9
	ds_write_b64 v130, v[132:133]
.LBB0_580:
	s_or_b64 exec, exec, s[6:7]
	v_add_f32_e32 v130, v114, v115
	v_add_f32_e32 v131, v116, v117
	v_add_f32_e32 v130, v130, v131
	v_mul_f32_e32 v131, v115, v115
	v_mul_f32_e32 v132, v117, v117
	v_fmac_f32_e32 v131, v114, v114
	v_fmac_f32_e32 v132, v116, v116
	v_add_f32_e32 v131, v131, v132
	v_add_f32_e32 v132, v118, v119
	v_add_f32_e32 v133, v120, v121
	v_add_f32_e32 v130, 0, v130
	v_add_f32_e32 v132, v132, v133
	v_add_f32_e32 v130, v132, v130
	v_mul_f32_e32 v132, v119, v119
	v_mul_f32_e32 v133, v121, v121
	v_fmac_f32_e32 v132, v118, v118
	v_fmac_f32_e32 v133, v120, v120
	v_add_f32_e32 v132, v132, v133
	v_add_f32_e32 v131, v131, v132
	v_add_f32_e32 v132, v10, v11
	v_add_f32_e32 v133, v12, v13
	v_add_f32_e32 v132, v132, v133
	v_add_f32_e32 v130, v132, v130
	v_mul_f32_e32 v132, v11, v11
	v_mul_f32_e32 v133, v13, v13
	v_fmac_f32_e32 v132, v10, v10
	v_fmac_f32_e32 v133, v12, v12
	v_add_f32_e32 v132, v132, v133
	v_add_f32_e32 v131, v132, v131
	v_add_f32_e32 v132, v14, v15
	v_add_f32_e32 v133, v16, v17
	v_add_f32_e32 v132, v132, v133
	v_add_f32_e32 v130, v132, v130
	v_mul_f32_e32 v132, v15, v15
	v_mul_f32_e32 v133, v17, v17
	v_fmac_f32_e32 v132, v14, v14
	v_fmac_f32_e32 v133, v16, v16
	v_add_f32_e32 v132, v132, v133
	v_add_f32_e32 v132, v132, v131
	ds_swizzle_b32 v131, v130 offset:swizzle(SWAP,16)
	ds_swizzle_b32 v133, v132 offset:swizzle(SWAP,16)
	s_waitcnt lgkmcnt(1)
	v_add_f32_e32 v131, v130, v131
	s_waitcnt lgkmcnt(0)
	v_add_f32_e32 v130, v132, v133
	v_mov_b32_e32 v133, v131
	v_mov_b32_e32 v132, v130
	s_nop 0
	v_permlane32_swap_b32_e32 v131, v133
	v_permlane32_swap_b32_e32 v130, v132
	s_and_saveexec_b64 s[6:7], vcc
	s_cbranch_execz .LBB0_582
	v_add_f32_e32 v130, v130, v132
	v_add_f32_e32 v131, v131, v133
	s_lshl_b32 s9, s8, 11
	v_mul_f32_e32 v132, 0x3c800000, v131
	v_fma_f32 v130, -v131, v132, v130
	s_add_i32 s9, s5, s9
	v_max_f32_e32 v133, 0, v130
	v_lshl_add_u32 v130, v0, 5, s9
	ds_write_b64 v130, v[132:133] offset:512
.LBB0_582:
	s_or_b64 exec, exec, s[6:7]
	v_add_f32_e32 v130, v98, v99
	v_add_f32_e32 v131, v100, v101
	v_add_f32_e32 v130, v130, v131
	v_mul_f32_e32 v131, v99, v99
	v_mul_f32_e32 v132, v101, v101
	v_fmac_f32_e32 v131, v98, v98
	v_fmac_f32_e32 v132, v100, v100
	v_add_f32_e32 v131, v131, v132
	v_add_f32_e32 v132, v110, v111
	v_add_f32_e32 v133, v112, v113
	v_add_f32_e32 v130, 0, v130
	v_add_f32_e32 v132, v132, v133
	v_add_f32_e32 v130, v132, v130
	v_mul_f32_e32 v132, v111, v111
	v_mul_f32_e32 v133, v113, v113
	v_fmac_f32_e32 v132, v110, v110
	v_fmac_f32_e32 v133, v112, v112
	v_add_f32_e32 v132, v132, v133
	v_add_f32_e32 v131, v131, v132
	v_add_f32_e32 v132, v18, v19
	v_add_f32_e32 v133, v20, v21
	v_add_f32_e32 v132, v132, v133
	v_add_f32_e32 v130, v132, v130
	v_mul_f32_e32 v132, v19, v19
	v_mul_f32_e32 v133, v21, v21
	v_fmac_f32_e32 v132, v18, v18
	v_fmac_f32_e32 v133, v20, v20
	v_add_f32_e32 v132, v132, v133
	v_add_f32_e32 v131, v132, v131
	v_add_f32_e32 v132, v22, v23
	v_add_f32_e32 v133, v24, v25
	v_add_f32_e32 v132, v132, v133
	v_add_f32_e32 v130, v132, v130
	v_mul_f32_e32 v132, v23, v23
	v_mul_f32_e32 v133, v25, v25
	v_fmac_f32_e32 v132, v22, v22
	v_fmac_f32_e32 v133, v24, v24
	v_add_f32_e32 v132, v132, v133
	v_add_f32_e32 v132, v132, v131
	ds_swizzle_b32 v131, v130 offset:swizzle(SWAP,16)
	ds_swizzle_b32 v133, v132 offset:swizzle(SWAP,16)
	s_waitcnt lgkmcnt(1)
	v_add_f32_e32 v131, v130, v131
	s_waitcnt lgkmcnt(0)
	v_add_f32_e32 v130, v132, v133
	v_mov_b32_e32 v133, v131
	v_mov_b32_e32 v132, v130
	s_nop 0
	v_permlane32_swap_b32_e32 v131, v133
	v_permlane32_swap_b32_e32 v130, v132
	s_and_saveexec_b64 s[6:7], vcc
	s_cbranch_execz .LBB0_584
	v_add_f32_e32 v130, v130, v132
	v_add_f32_e32 v131, v131, v133
	s_lshl_b32 s9, s8, 11
	v_mul_f32_e32 v132, 0x3c800000, v131
	v_fma_f32 v130, -v131, v132, v130
	s_add_i32 s9, s5, s9
	v_max_f32_e32 v133, 0, v130
	v_lshl_add_u32 v130, v0, 5, s9
	ds_write_b64 v130, v[132:133] offset:1024
.LBB0_584:
	s_or_b64 exec, exec, s[6:7]
	v_add_f32_e32 v130, v102, v103
	v_add_f32_e32 v131, v104, v105
	v_add_f32_e32 v130, v130, v131
	v_mul_f32_e32 v131, v103, v103
	v_mul_f32_e32 v132, v105, v105
	v_fmac_f32_e32 v131, v102, v102
	v_fmac_f32_e32 v132, v104, v104
	v_add_f32_e32 v131, v131, v132
	v_add_f32_e32 v132, v106, v107
	v_add_f32_e32 v133, v108, v109
	v_add_f32_e32 v130, 0, v130
	v_add_f32_e32 v132, v132, v133
	v_add_f32_e32 v130, v132, v130
	v_mul_f32_e32 v132, v107, v107
	v_mul_f32_e32 v133, v109, v109
	v_fmac_f32_e32 v132, v106, v106
	v_fmac_f32_e32 v133, v108, v108
	v_add_f32_e32 v132, v132, v133
	v_add_f32_e32 v131, v131, v132
	v_add_f32_e32 v132, v2, v3
	v_add_f32_e32 v133, v4, v5
	v_add_f32_e32 v132, v132, v133
	v_add_f32_e32 v130, v132, v130
	v_mul_f32_e32 v132, v3, v3
	v_mul_f32_e32 v133, v5, v5
	v_fmac_f32_e32 v132, v2, v2
	v_fmac_f32_e32 v133, v4, v4
	v_add_f32_e32 v132, v132, v133
	v_add_f32_e32 v131, v132, v131
	v_add_f32_e32 v132, v6, v7
	v_add_f32_e32 v133, v8, v9
	v_add_f32_e32 v132, v132, v133
	v_add_f32_e32 v130, v132, v130
	v_mul_f32_e32 v132, v7, v7
	v_mul_f32_e32 v133, v9, v9
	v_fmac_f32_e32 v132, v6, v6
	v_fmac_f32_e32 v133, v8, v8
	v_add_f32_e32 v132, v132, v133
	v_add_f32_e32 v132, v132, v131
	ds_swizzle_b32 v131, v130 offset:swizzle(SWAP,16)
	ds_swizzle_b32 v133, v132 offset:swizzle(SWAP,16)
	s_waitcnt lgkmcnt(1)
	v_add_f32_e32 v131, v130, v131
	s_waitcnt lgkmcnt(0)
	v_add_f32_e32 v130, v132, v133
	v_mov_b32_e32 v133, v131
	v_mov_b32_e32 v132, v130
	s_nop 0
	v_permlane32_swap_b32_e32 v131, v133
	v_permlane32_swap_b32_e32 v130, v132
	s_and_saveexec_b64 s[6:7], vcc
	s_cbranch_execz .LBB0_586
	v_add_f32_e32 v130, v130, v132
	v_add_f32_e32 v131, v131, v133
	s_lshl_b32 s9, s8, 11
	v_mul_f32_e32 v132, 0x3c800000, v131
	v_fma_f32 v130, -v131, v132, v130
	s_add_i32 s9, s5, s9
	v_max_f32_e32 v133, 0, v130
	v_lshl_add_u32 v130, v0, 5, s9
	ds_write_b64 v130, v[132:133] offset:1536
.LBB0_586:
	s_or_b64 exec, exec, s[6:7]
	v_add_f32_e32 v130, v74, v75
	v_add_f32_e32 v131, v76, v77
	v_add_f32_e32 v130, v130, v131
	v_mul_f32_e32 v131, v75, v75
	v_mul_f32_e32 v132, v77, v77
	v_fmac_f32_e32 v131, v74, v74
	v_fmac_f32_e32 v132, v76, v76
	v_add_f32_e32 v131, v131, v132
	v_add_f32_e32 v132, v82, v83
	v_add_f32_e32 v133, v84, v85
	v_add_f32_e32 v130, 0, v130
	v_add_f32_e32 v132, v132, v133
	v_add_f32_e32 v130, v132, v130
	v_mul_f32_e32 v132, v83, v83
	v_mul_f32_e32 v133, v85, v85
	v_fmac_f32_e32 v132, v82, v82
	v_fmac_f32_e32 v133, v84, v84
	v_add_f32_e32 v132, v132, v133
	v_add_f32_e32 v131, v131, v132
	v_add_f32_e32 v132, v26, v27
	v_add_f32_e32 v133, v28, v29
	v_add_f32_e32 v132, v132, v133
	v_add_f32_e32 v130, v132, v130
	v_mul_f32_e32 v132, v27, v27
	v_mul_f32_e32 v133, v29, v29
	v_fmac_f32_e32 v132, v26, v26
	v_fmac_f32_e32 v133, v28, v28
	v_add_f32_e32 v132, v132, v133
	v_add_f32_e32 v131, v132, v131
	v_add_f32_e32 v132, v38, v39
	v_add_f32_e32 v133, v40, v41
	v_add_f32_e32 v132, v132, v133
	v_add_f32_e32 v130, v132, v130
	v_mul_f32_e32 v132, v39, v39
	v_mul_f32_e32 v133, v41, v41
	v_fmac_f32_e32 v132, v38, v38
	v_fmac_f32_e32 v133, v40, v40
	v_add_f32_e32 v132, v132, v133
	v_add_f32_e32 v132, v132, v131
	ds_swizzle_b32 v131, v130 offset:swizzle(SWAP,16)
	ds_swizzle_b32 v133, v132 offset:swizzle(SWAP,16)
	s_waitcnt lgkmcnt(1)
	v_add_f32_e32 v131, v130, v131
	s_waitcnt lgkmcnt(0)
	v_add_f32_e32 v130, v132, v133
	v_mov_b32_e32 v133, v131
	v_mov_b32_e32 v132, v130
	s_nop 0
	v_permlane32_swap_b32_e32 v131, v133
	v_permlane32_swap_b32_e32 v130, v132
	s_and_saveexec_b64 s[6:7], vcc
	s_cbranch_execz .LBB0_588
	v_add_f32_e32 v130, v130, v132
	v_add_f32_e32 v131, v131, v133
	s_lshl_b32 s9, s8, 11
	v_mul_f32_e32 v132, 0x3c800000, v131
	v_fma_f32 v130, -v131, v132, v130
	s_add_i32 s9, s5, s9
	v_max_f32_e32 v133, 0, v130
	v_lshl_add_u32 v130, v0, 5, s9
	ds_write_b64 v130, v[132:133] offset:4096
.LBB0_588:
	s_or_b64 exec, exec, s[6:7]
	v_add_f32_e32 v130, v66, v67
	v_add_f32_e32 v131, v68, v69
	v_add_f32_e32 v130, v130, v131
	v_mul_f32_e32 v131, v67, v67
	v_mul_f32_e32 v132, v69, v69
	v_fmac_f32_e32 v131, v66, v66
	v_fmac_f32_e32 v132, v68, v68
	v_add_f32_e32 v131, v131, v132
	v_add_f32_e32 v132, v70, v71
	v_add_f32_e32 v133, v72, v73
	v_add_f32_e32 v130, 0, v130
	v_add_f32_e32 v132, v132, v133
	v_add_f32_e32 v130, v132, v130
	v_mul_f32_e32 v132, v71, v71
	v_mul_f32_e32 v133, v73, v73
	v_fmac_f32_e32 v132, v70, v70
	v_fmac_f32_e32 v133, v72, v72
	v_add_f32_e32 v132, v132, v133
	v_add_f32_e32 v131, v131, v132
	v_add_f32_e32 v132, v58, v59
	v_add_f32_e32 v133, v60, v61
	v_add_f32_e32 v132, v132, v133
	v_add_f32_e32 v130, v132, v130
	v_mul_f32_e32 v132, v59, v59
	v_mul_f32_e32 v133, v61, v61
	v_fmac_f32_e32 v132, v58, v58
	v_fmac_f32_e32 v133, v60, v60
	v_add_f32_e32 v132, v132, v133
	v_add_f32_e32 v131, v132, v131
	v_add_f32_e32 v132, v62, v63
	v_add_f32_e32 v133, v64, v65
	v_add_f32_e32 v132, v132, v133
	v_add_f32_e32 v130, v132, v130
	v_mul_f32_e32 v132, v63, v63
	v_mul_f32_e32 v133, v65, v65
	v_fmac_f32_e32 v132, v62, v62
	v_fmac_f32_e32 v133, v64, v64
	v_add_f32_e32 v132, v132, v133
	v_add_f32_e32 v132, v132, v131
	ds_swizzle_b32 v131, v130 offset:swizzle(SWAP,16)
	ds_swizzle_b32 v133, v132 offset:swizzle(SWAP,16)
	s_waitcnt lgkmcnt(1)
	v_add_f32_e32 v131, v130, v131
	s_waitcnt lgkmcnt(0)
	v_add_f32_e32 v130, v132, v133
	v_mov_b32_e32 v133, v131
	v_mov_b32_e32 v132, v130
	s_nop 0
	v_permlane32_swap_b32_e32 v131, v133
	v_permlane32_swap_b32_e32 v130, v132
	s_and_saveexec_b64 s[6:7], vcc
	s_cbranch_execz .LBB0_590
	v_add_f32_e32 v130, v130, v132
	v_add_f32_e32 v131, v131, v133
	s_lshl_b32 s9, s8, 11
	v_mul_f32_e32 v132, 0x3c800000, v131
	v_fma_f32 v130, -v131, v132, v130
	s_add_i32 s9, s5, s9
	v_max_f32_e32 v133, 0, v130
	v_lshl_add_u32 v130, v0, 5, s9
	ds_write_b64 v130, v[132:133] offset:4608
.LBB0_590:
	s_or_b64 exec, exec, s[6:7]
	v_add_f32_e32 v130, v90, v91
	v_add_f32_e32 v131, v92, v93
	v_add_f32_e32 v130, v130, v131
	v_mul_f32_e32 v131, v91, v91
	v_mul_f32_e32 v132, v93, v93
	v_fmac_f32_e32 v131, v90, v90
	v_fmac_f32_e32 v132, v92, v92
	v_add_f32_e32 v131, v131, v132
	v_add_f32_e32 v132, v94, v95
	v_add_f32_e32 v133, v96, v97
	v_add_f32_e32 v130, 0, v130
	v_add_f32_e32 v132, v132, v133
	v_add_f32_e32 v130, v132, v130
	v_mul_f32_e32 v132, v95, v95
	v_mul_f32_e32 v133, v97, v97
	v_fmac_f32_e32 v132, v94, v94
	v_fmac_f32_e32 v133, v96, v96
	v_add_f32_e32 v132, v132, v133
	v_add_f32_e32 v131, v131, v132
	v_add_f32_e32 v132, v50, v51
	v_add_f32_e32 v133, v52, v53
	v_add_f32_e32 v132, v132, v133
	v_add_f32_e32 v130, v132, v130
	v_mul_f32_e32 v132, v51, v51
	v_mul_f32_e32 v133, v53, v53
	v_fmac_f32_e32 v132, v50, v50
	v_fmac_f32_e32 v133, v52, v52
	v_add_f32_e32 v132, v132, v133
	v_add_f32_e32 v131, v132, v131
	v_add_f32_e32 v132, v54, v55
	v_add_f32_e32 v133, v56, v57
	v_add_f32_e32 v132, v132, v133
	v_add_f32_e32 v130, v132, v130
	v_mul_f32_e32 v132, v55, v55
	v_mul_f32_e32 v133, v57, v57
	v_fmac_f32_e32 v132, v54, v54
	v_fmac_f32_e32 v133, v56, v56
	v_add_f32_e32 v132, v132, v133
	v_add_f32_e32 v132, v132, v131
	ds_swizzle_b32 v131, v130 offset:swizzle(SWAP,16)
	ds_swizzle_b32 v133, v132 offset:swizzle(SWAP,16)
	s_waitcnt lgkmcnt(1)
	v_add_f32_e32 v131, v130, v131
	s_waitcnt lgkmcnt(0)
	v_add_f32_e32 v130, v132, v133
	v_mov_b32_e32 v133, v131
	v_mov_b32_e32 v132, v130
	s_nop 0
	v_permlane32_swap_b32_e32 v131, v133
	v_permlane32_swap_b32_e32 v130, v132
	s_and_saveexec_b64 s[6:7], vcc
	s_cbranch_execz .LBB0_592
	v_add_f32_e32 v130, v130, v132
	v_add_f32_e32 v131, v131, v133
	s_lshl_b32 s9, s8, 11
	v_mul_f32_e32 v132, 0x3c800000, v131
	v_fma_f32 v130, -v131, v132, v130
	s_add_i32 s9, s5, s9
	v_max_f32_e32 v133, 0, v130
	v_lshl_add_u32 v130, v0, 5, s9
	ds_write_b64 v130, v[132:133] offset:5120
.LBB0_592:
	s_or_b64 exec, exec, s[6:7]
	v_add_f32_e32 v130, v78, v79
	v_add_f32_e32 v131, v80, v81
	v_add_f32_e32 v130, v130, v131
	v_mul_f32_e32 v131, v79, v79
	v_mul_f32_e32 v132, v81, v81
	v_fmac_f32_e32 v131, v78, v78
	v_fmac_f32_e32 v132, v80, v80
	v_add_f32_e32 v131, v131, v132
	v_add_f32_e32 v132, v86, v87
	v_add_f32_e32 v133, v88, v89
	v_add_f32_e32 v130, 0, v130
	v_add_f32_e32 v132, v132, v133
	v_add_f32_e32 v130, v132, v130
	v_mul_f32_e32 v132, v87, v87
	v_mul_f32_e32 v133, v89, v89
	v_fmac_f32_e32 v132, v86, v86
	v_fmac_f32_e32 v133, v88, v88
	v_add_f32_e32 v132, v132, v133
	v_add_f32_e32 v131, v131, v132
	v_add_f32_e32 v132, v42, v43
	v_add_f32_e32 v133, v44, v45
	v_add_f32_e32 v132, v132, v133
	v_add_f32_e32 v130, v132, v130
	v_mul_f32_e32 v132, v43, v43
	v_mul_f32_e32 v133, v45, v45
	v_fmac_f32_e32 v132, v42, v42
	v_fmac_f32_e32 v133, v44, v44
	v_add_f32_e32 v132, v132, v133
	v_add_f32_e32 v131, v132, v131
	v_add_f32_e32 v132, v46, v47
	v_add_f32_e32 v133, v48, v49
	v_add_f32_e32 v132, v132, v133
	v_add_f32_e32 v130, v132, v130
	v_mul_f32_e32 v132, v47, v47
	v_mul_f32_e32 v133, v49, v49
	v_fmac_f32_e32 v132, v46, v46
	v_fmac_f32_e32 v133, v48, v48
	v_add_f32_e32 v132, v132, v133
	v_add_f32_e32 v132, v132, v131
	ds_swizzle_b32 v131, v130 offset:swizzle(SWAP,16)
	ds_swizzle_b32 v133, v132 offset:swizzle(SWAP,16)
	s_waitcnt lgkmcnt(1)
	v_add_f32_e32 v131, v130, v131
	s_waitcnt lgkmcnt(0)
	v_add_f32_e32 v130, v132, v133
	v_mov_b32_e32 v133, v131
	v_mov_b32_e32 v132, v130
	s_nop 0
	v_permlane32_swap_b32_e32 v131, v133
	v_permlane32_swap_b32_e32 v130, v132
	s_and_saveexec_b64 s[6:7], vcc
	s_cbranch_execz .LBB0_594
	v_add_f32_e32 v130, v130, v132
	v_add_f32_e32 v131, v131, v133
	s_lshl_b32 s8, s8, 11
	v_mul_f32_e32 v132, 0x3c800000, v131
	v_fma_f32 v130, -v131, v132, v130
	s_add_i32 s5, s5, s8
	v_max_f32_e32 v133, 0, v130
	v_lshl_add_u32 v0, v0, 5, s5
	ds_write_b64 v0, v[132:133] offset:5632
.LBB0_594:
	s_or_b64 exec, exec, s[6:7]
	v_or_b32_e32 v0, s1, v183
	v_cmp_eq_u32_e32 vcc, 0, v0
	s_and_saveexec_b64 s[6:7], vcc
	ds_write_b32 v1, v1 offset:10240
	s_or_b64 exec, exec, s[6:7]
	s_waitcnt lgkmcnt(0)
	s_barrier
	v_cmp_gt_i32_e32 vcc, 32, v183
	s_and_saveexec_b64 s[6:7], vcc
	s_cbranch_execz .LBB0_607
	s_lshl_b32 s1, s1, 5
	v_and_or_b32 v130, v183, 31, s1
	v_lshl_add_u32 v0, v130, 5, 0
	ds_read_b128 v[132:135], v0
	ds_read_b128 v[136:139], v0 offset:16
	s_ashr_i32 s1, s0, 31
	s_lshl_b64 s[0:1], s[0:1], 14
	s_add_u32 s0, s39, s0
	s_waitcnt lgkmcnt(1)
	v_add_f32_e32 v131, v132, v134
	s_waitcnt lgkmcnt(0)
	v_add_f32_e32 v131, v131, v136
	v_add_f32_e32 v131, v131, v138
	v_fmamk_f32 v132, v131, 0xbe800000, v132
	v_fmac_f32_e32 v134, 0xbe800000, v131
	v_fmamk_f32 v136, v131, 0xbe800000, v136
	v_fmac_f32_e32 v138, 0xbe800000, v131
	v_mul_f32_e32 v143, v132, v132
	v_mul_f32_e32 v145, v134, v134
	v_mul_f32_e32 v147, v136, v136
	v_mul_f32_e32 v149, v138, v138
	v_mov_b32_e32 v142, v133
	v_mov_b32_e32 v144, v135
	v_mov_b32_e32 v146, v137
	v_mov_b32_e32 v148, v139
	v_add_f32_e32 v132, v142, v144
	v_add_f32_e32 v133, v143, v145
	v_add_f32_e32 v134, v146, v148
	v_add_f32_e32 v135, v147, v149
	v_mul_f32_e32 v140, 0x3e800000, v131
	v_add_f32_e32 v132, v132, v134
	v_add_f32_e32 v133, v133, v135
	s_addc_u32 s1, s41, s1
	v_fmac_f32_e32 v132, 0x42800000, v133
	v_ashrrev_i32_e32 v131, 31, v130
	v_lshl_add_u64 v[136:137], v[130:131], 3, s[0:1]
	s_ashr_i32 s5, s4, 31
	v_and_b32_e32 v131, 0xffffffe0, v132
	v_lshl_add_u64 v[134:135], s[4:5], 3, v[136:137]
	v_or_b32_e32 v141, s38, v131
	s_mov_b64 s[0:1], 0x1000
	global_store_dwordx2 v[134:135], v[140:141], off sc1
	v_lshl_add_u64 v[140:141], v[136:137], 0, s[0:1]
	s_mov_b64 s[0:1], 0x1800
	s_memrealtime s[22:23]
	v_lshl_add_u64 v[142:143], v[136:137], 0, s[0:1]
	s_mov_b64 s[0:1], 0x2000
	v_lshl_add_u64 v[146:147], v[136:137], 0, s[0:1]
	s_mov_b64 s[0:1], 0x2800
	v_lshl_add_u64 v[148:149], v[136:137], 0, s[0:1]
	s_mov_b64 s[0:1], 0x3000
	v_lshl_add_u64 v[150:151], v[136:137], 0, s[0:1]
	s_mov_b64 s[0:1], 0x3800
	v_lshl_add_u64 v[152:153], v[136:137], 0, s[0:1]
	s_mov_b64 s[4:5], 0
	s_branch .LBB0_600

.LBB0_681:
	s_lshl_b32 s1, s29, 5
	s_add_u32 s22, s14, 0x32e00000
	s_addc_u32 s23, s15, 0
	v_and_b32_e32 v211, 63, v162
	v_bfe_u32 v212, v162, 4, 2
	s_add_u32 s24, s14, 0x46e00000
	s_addc_u32 s25, s15, 0
	s_barrier
	s_lshl_b32 s0, s9, 8
	v_add_u32_e32 v210, s39, v0
	s_or_b32 s1, s0, s1
	v_lshl_add_u32 v200, s20, 8, v210
	v_lshl_add_u32 v184, v212, 3, s1
	v_ashrrev_i32_e32 v201, 31, v200
	v_ashrrev_i32_e32 v185, 31, v184
	v_lshlrev_b64 v[186:187], 11, v[200:201]
	v_lshl_add_u64 v[198:199], v[186:187], 0, v[184:185]
	v_lshlrev_b64 v[6:7], 1, v[198:199]
	s_mov_b32 s1, 1.0
	s_mov_b32 s2, 0x3fd744fd
	s_mov_b32 s26, s52
	v_lshl_add_u64 v[12:13], s[24:25], 0, v[6:7]
	v_lshl_add_u64 v[10:11], s[22:23], 0, v[6:7]
	global_load_dwordx4 v[6:9], v[12:13], off
	global_load_dwordx4 v[204:207], v[12:13], off offset:256
	global_load_dwordx4 v[2:5], v[10:11], off
	global_load_dwordx4 v[188:191], v[10:11], off offset:256
	v_mov_b32_e32 v14, 0xbfb8aa3b
	v_mul_f32_e32 v213, s1, v14
	v_mul_f32_e32 v15, v62, v213
	v_mul_f32_e32 v17, v63, v213
	v_mul_f32_e32 v19, v64, v213
	v_add_u32_e32 v14, 16, v200
	v_add_u32_e32 v16, 32, v200
	v_add_u32_e32 v18, 48, v200
	v_exp_f32_e32 v21, v15
	v_exp_f32_e32 v22, v17
	v_exp_f32_e32 v23, v19
	v_ashrrev_i32_e32 v15, 31, v14
	v_ashrrev_i32_e32 v17, 31, v16
	v_ashrrev_i32_e32 v19, 31, v18
	v_lshlrev_b64 v[182:183], 11, v[14:15]
	v_lshlrev_b64 v[180:181], 11, v[16:17]
	v_lshlrev_b64 v[178:179], 11, v[18:19]
	v_lshl_add_u64 v[196:197], v[182:183], 0, v[184:185]
	v_lshl_add_u64 v[194:195], v[180:181], 0, v[184:185]
	v_lshl_add_u64 v[192:193], v[178:179], 0, v[184:185]
	v_mul_f32_e32 v20, v65, v213
	v_add_f32_e32 v16, 1.0, v21
	v_add_f32_e32 v17, 1.0, v22
	v_lshlrev_b64 v[10:11], 1, v[196:197]
	v_lshlrev_b64 v[12:13], 1, v[194:195]
	v_lshlrev_b64 v[14:15], 1, v[192:193]
	v_exp_f32_e32 v201, v20
	v_rcp_f32_e32 v62, v16
	v_rcp_f32_e32 v63, v17
	v_lshl_add_u64 v[16:17], s[22:23], 0, v[10:11]
	v_lshl_add_u64 v[10:11], s[24:25], 0, v[10:11]
	v_lshl_add_u64 v[18:19], s[22:23], 0, v[12:13]
	v_lshl_add_u64 v[20:21], s[24:25], 0, v[12:13]
	v_lshl_add_u64 v[26:27], s[22:23], 0, v[14:15]
	v_lshl_add_u64 v[28:29], s[24:25], 0, v[14:15]
	v_add_f32_e32 v226, 1.0, v23
	global_load_dwordx4 v[214:217], v[16:17], off
	s_nop 0
	global_load_dwordx4 v[14:17], v[16:17], off offset:256
	s_nop 0
	global_load_dwordx4 v[218:221], v[10:11], off
	s_nop 0
	global_load_dwordx4 v[10:13], v[10:11], off offset:256
	s_nop 0
	global_load_dwordx4 v[174:177], v[18:19], off
	global_load_dwordx4 v[22:25], v[18:19], off offset:256
	global_load_dwordx4 v[170:173], v[20:21], off
	s_nop 0
	global_load_dwordx4 v[18:21], v[20:21], off offset:256
	s_nop 0
	global_load_dwordx4 v[166:169], v[26:27], off
	global_load_dwordx4 v[30:33], v[26:27], off offset:256
	global_load_dwordx4 v[162:165], v[28:29], off
	s_nop 0
	global_load_dwordx4 v[26:29], v[28:29], off offset:256
	v_mul_f32_e32 v58, v58, v213
	v_exp_f32_e32 v58, v58
	v_mul_f32_e32 v59, v59, v213
	v_exp_f32_e32 v59, v59
	v_add_f32_e32 v201, 1.0, v201
	v_add_f32_e32 v58, 1.0, v58
	v_rcp_f32_e32 v226, v226
	v_rcp_f32_e32 v227, v201
	v_mul_f32_e32 v158, v158, v213
	v_mul_f32_e32 v159, v159, v213
	v_exp_f32_e32 v158, v158
	v_exp_f32_e32 v159, v159
	v_mul_f32_e32 v160, v160, v213
	v_mul_f32_e32 v161, v161, v213
	v_add_f32_e32 v158, 1.0, v158
	v_add_f32_e32 v159, 1.0, v159
	v_exp_f32_e32 v160, v160
	v_exp_f32_e32 v161, v161
	v_mul_f32_e32 v78, v78, v213
	v_mul_f32_e32 v79, v79, v213
	v_rcp_f32_e32 v158, v158
	v_rcp_f32_e32 v159, v159
	v_exp_f32_e32 v78, v78
	v_exp_f32_e32 v79, v79
	v_mul_f32_e32 v154, v154, v213
	v_add_f32_e32 v160, 1.0, v160
	v_add_f32_e32 v161, 1.0, v161
	v_exp_f32_e32 v201, v154
	v_mul_f32_e32 v154, v155, v213
	v_mul_f32_e32 v80, v80, v213
	v_mul_f32_e32 v81, v81, v213
	v_rcp_f32_e32 v160, v160
	v_rcp_f32_e32 v161, v161
	v_add_f32_e32 v78, 1.0, v78
	v_add_f32_e32 v79, 1.0, v79
	v_exp_f32_e32 v80, v80
	v_exp_f32_e32 v81, v81
	v_rcp_f32_e32 v78, v78
	v_rcp_f32_e32 v79, v79
	s_waitcnt vmcnt(15)
	v_lshlrev_b32_e32 v224, 16, v6
	v_and_b32_e32 v225, 0xffff0000, v6
	v_pk_mul_f32 v[62:63], v[62:63], v[224:225]
	v_rcp_f32_e32 v224, v58
	v_add_f32_e32 v58, 1.0, v59
	v_mul_f32_e32 v59, v60, v213
	v_exp_f32_e32 v59, v59
	v_mul_f32_e32 v60, v61, v213
	v_exp_f32_e32 v60, v60
	v_lshlrev_b32_e32 v6, 16, v7
	v_and_b32_e32 v7, 0xffff0000, v7
	v_rcp_f32_e32 v225, v58
	v_add_f32_e32 v58, 1.0, v59
	v_pk_mul_f32 v[6:7], v[226:227], v[6:7]
	v_rcp_f32_e32 v226, v58
	v_add_f32_e32 v58, 1.0, v60
	v_rcp_f32_e32 v227, v58
	s_waitcnt vmcnt(13)
	v_lshlrev_b32_e32 v64, 16, v2
	v_and_b32_e32 v65, 0xffff0000, v2
	v_lshlrev_b32_e32 v2, 16, v3
	v_and_b32_e32 v3, 0xffff0000, v3
	v_lshlrev_b32_e32 v222, 16, v8
	v_and_b32_e32 v223, 0xffff0000, v8
	v_lshlrev_b32_e32 v8, 16, v9
	v_and_b32_e32 v9, 0xffff0000, v9
	v_lshlrev_b32_e32 v208, 16, v4
	v_and_b32_e32 v209, 0xffff0000, v4
	v_lshlrev_b32_e32 v4, 16, v5
	v_and_b32_e32 v5, 0xffff0000, v5
	v_pk_fma_f32 v[60:61], s[2:3], v[2:3], v[6:7] op_sel_hi:[0,1,1]
	v_pk_mul_f32 v[2:3], v[224:225], v[222:223]
	v_pk_mul_f32 v[6:7], v[226:227], v[8:9]
	v_pk_fma_f32 v[58:59], s[2:3], v[64:65], v[62:63] op_sel_hi:[0,1,1]
	v_pk_fma_f32 v[64:65], s[2:3], v[4:5], v[6:7] op_sel_hi:[0,1,1]
	v_pk_fma_f32 v[62:63], s[2:3], v[208:209], v[2:3] op_sel_hi:[0,1,1]
	s_waitcnt vmcnt(12)
	v_lshlrev_b32_e32 v6, 16, v190
	v_and_b32_e32 v7, 0xffff0000, v190
	v_lshlrev_b32_e32 v8, 16, v191
	v_and_b32_e32 v9, 0xffff0000, v191
	v_lshlrev_b32_e32 v2, 16, v188
	v_and_b32_e32 v3, 0xffff0000, v188
	v_lshlrev_b32_e32 v4, 16, v189
	v_and_b32_e32 v5, 0xffff0000, v189
	v_lshlrev_b32_e32 v188, 16, v206
	v_and_b32_e32 v189, 0xffff0000, v206
	v_lshlrev_b32_e32 v190, 16, v207
	v_and_b32_e32 v191, 0xffff0000, v207
	v_lshlrev_b32_e32 v206, 16, v204
	v_and_b32_e32 v207, 0xffff0000, v204
	v_pk_mul_f32 v[158:159], v[158:159], v[206:207]
	v_exp_f32_e32 v206, v154
	v_mul_f32_e32 v150, v150, v213
	v_mul_f32_e32 v151, v151, v213
	v_exp_f32_e32 v150, v150
	v_exp_f32_e32 v151, v151
	v_lshlrev_b32_e32 v204, 16, v205
	v_and_b32_e32 v205, 0xffff0000, v205
	v_mul_f32_e32 v74, v74, v213
	v_mul_f32_e32 v76, v76, v213
	v_pk_mul_f32 v[154:155], v[160:161], v[204:205]
	v_add_f32_e32 v160, 1.0, v201
	v_add_f32_e32 v161, 1.0, v206
	s_waitcnt vmcnt(9)
	v_lshlrev_b32_e32 v204, 16, v218
	v_and_b32_e32 v205, 0xffff0000, v218
	v_add_f32_e32 v80, 1.0, v80
	v_add_f32_e32 v81, 1.0, v81
	v_exp_f32_e32 v201, v74
	v_mul_f32_e32 v74, v75, v213
	v_exp_f32_e32 v76, v76
	v_mul_f32_e32 v77, v77, v213
	v_rcp_f32_e32 v160, v160
	v_rcp_f32_e32 v161, v161
	v_rcp_f32_e32 v80, v80
	v_rcp_f32_e32 v81, v81
	v_pk_mul_f32 v[78:79], v[78:79], v[204:205]
	v_exp_f32_e32 v204, v74
	v_exp_f32_e32 v77, v77
	v_add_f32_e32 v150, 1.0, v150
	v_add_f32_e32 v151, 1.0, v151
	v_rcp_f32_e32 v150, v150
	v_rcp_f32_e32 v151, v151
	v_lshlrev_b32_e32 v206, 16, v219
	v_and_b32_e32 v207, 0xffff0000, v219
	v_add_f32_e32 v76, 1.0, v76
	v_pk_fma_f32 v[4:5], s[2:3], v[4:5], v[154:155] op_sel_hi:[0,1,1]
	v_pk_fma_f32 v[2:3], s[2:3], v[2:3], v[158:159] op_sel_hi:[0,1,1]
	v_pk_mul_f32 v[154:155], v[160:161], v[188:189]
	v_lshlrev_b32_e32 v158, 16, v214
	v_and_b32_e32 v159, 0xffff0000, v214
	v_lshlrev_b32_e32 v160, 16, v215
	v_and_b32_e32 v161, 0xffff0000, v215
	v_pk_mul_f32 v[74:75], v[80:81], v[206:207]
	v_add_f32_e32 v81, 1.0, v204
	v_rcp_f32_e32 v204, v76
	v_add_f32_e32 v76, 1.0, v77
	v_rcp_f32_e32 v205, v76
	v_pk_fma_f32 v[76:77], s[2:3], v[160:161], v[74:75] op_sel_hi:[0,1,1]
	v_pk_fma_f32 v[74:75], s[2:3], v[158:159], v[78:79] op_sel_hi:[0,1,1]
	s_waitcnt vmcnt(8)
	v_lshlrev_b32_e32 v158, 16, v12
	v_and_b32_e32 v159, 0xffff0000, v12
	v_lshlrev_b32_e32 v160, 16, v13
	v_and_b32_e32 v161, 0xffff0000, v13
	v_lshlrev_b32_e32 v12, 16, v10
	v_and_b32_e32 v13, 0xffff0000, v10
	v_mul_f32_e32 v156, v156, v213
	v_mul_f32_e32 v157, v157, v213
	v_pk_mul_f32 v[150:151], v[150:151], v[12:13]
	v_mul_f32_e32 v12, v146, v213
	v_exp_f32_e32 v156, v156
	v_exp_f32_e32 v157, v157
	v_exp_f32_e32 v12, v12
	v_mul_f32_e32 v13, v147, v213
	v_mul_f32_e32 v152, v152, v213
	v_mul_f32_e32 v153, v153, v213
	v_exp_f32_e32 v13, v13
	v_exp_f32_e32 v152, v152
	v_exp_f32_e32 v153, v153
	v_mul_f32_e32 v94, v94, v213
	v_mul_f32_e32 v95, v95, v213
	v_add_f32_e32 v156, 1.0, v156
	v_add_f32_e32 v157, 1.0, v157
	v_add_f32_e32 v12, 1.0, v12
	v_exp_f32_e32 v94, v94
	v_exp_f32_e32 v95, v95
	v_rcp_f32_e32 v156, v156
	v_rcp_f32_e32 v157, v157
	v_add_f32_e32 v80, 1.0, v201
	v_rcp_f32_e32 v146, v12
	v_add_f32_e32 v12, 1.0, v13
	v_mul_f32_e32 v13, v148, v213
	v_rcp_f32_e32 v80, v80
	v_rcp_f32_e32 v81, v81
	v_add_f32_e32 v152, 1.0, v152
	v_add_f32_e32 v153, 1.0, v153
	v_exp_f32_e32 v13, v13
	v_mul_f32_e32 v147, v149, v213
	v_rcp_f32_e32 v152, v152
	v_rcp_f32_e32 v153, v153
	v_exp_f32_e32 v149, v147
	v_mul_f32_e32 v96, v96, v213
	v_mul_f32_e32 v97, v97, v213
	v_rcp_f32_e32 v147, v12
	v_add_f32_e32 v94, 1.0, v94
	v_add_f32_e32 v95, 1.0, v95
	v_exp_f32_e32 v96, v96
	v_exp_f32_e32 v97, v97
	v_pk_mul_f32 v[156:157], v[156:157], v[190:191]
	v_lshlrev_b32_e32 v188, 16, v220
	v_and_b32_e32 v189, 0xffff0000, v220
	v_lshlrev_b32_e32 v190, 16, v221
	v_and_b32_e32 v191, 0xffff0000, v221
	v_rcp_f32_e32 v94, v94
	v_rcp_f32_e32 v95, v95
	v_mul_f32_e32 v142, v142, v213
	v_mul_f32_e32 v143, v143, v213
	v_pk_fma_f32 v[8:9], s[2:3], v[8:9], v[156:157] op_sel_hi:[0,1,1]
	v_lshlrev_b32_e32 v156, 16, v217
	v_and_b32_e32 v157, 0xffff0000, v217
	v_pk_mul_f32 v[78:79], v[80:81], v[188:189]
	v_pk_mul_f32 v[80:81], v[204:205], v[190:191]
	v_lshlrev_b32_e32 v10, 16, v11
	v_and_b32_e32 v11, 0xffff0000, v11
	v_add_f32_e32 v12, 1.0, v13
	v_exp_f32_e32 v142, v142
	v_exp_f32_e32 v143, v143
	v_pk_fma_f32 v[80:81], s[2:3], v[156:157], v[80:81] op_sel_hi:[0,1,1]
	v_lshlrev_b32_e32 v156, 16, v14
	v_and_b32_e32 v157, 0xffff0000, v14
	v_lshlrev_b32_e32 v14, 16, v15
	v_and_b32_e32 v15, 0xffff0000, v15
	v_pk_mul_f32 v[10:11], v[152:153], v[10:11]
	v_rcp_f32_e32 v148, v12
	v_add_f32_e32 v12, 1.0, v149
	v_mul_f32_e32 v92, v92, v213
	v_rcp_f32_e32 v149, v12
	v_pk_fma_f32 v[12:13], s[2:3], v[14:15], v[10:11] op_sel_hi:[0,1,1]
	v_pk_mul_f32 v[14:15], v[146:147], v[158:159]
	s_waitcnt vmcnt(5)
	v_lshlrev_b32_e32 v158, 16, v170
	v_and_b32_e32 v159, 0xffff0000, v170
	v_add_f32_e32 v96, 1.0, v96
	v_add_f32_e32 v97, 1.0, v97
	v_mul_f32_e32 v90, v90, v213
	v_exp_f32_e32 v92, v92
	v_mul_f32_e32 v93, v93, v213
	v_rcp_f32_e32 v96, v96
	v_rcp_f32_e32 v97, v97
	v_pk_mul_f32 v[94:95], v[94:95], v[158:159]
	v_exp_f32_e32 v158, v90
	v_mul_f32_e32 v90, v91, v213
	v_exp_f32_e32 v93, v93
	v_exp_f32_e32 v159, v90
	v_add_f32_e32 v142, 1.0, v142
	v_add_f32_e32 v143, 1.0, v143
	v_rcp_f32_e32 v142, v142
	v_rcp_f32_e32 v143, v143
	v_pk_mul_f32 v[146:147], v[148:149], v[160:161]
	v_lshlrev_b32_e32 v160, 16, v171
	v_and_b32_e32 v161, 0xffff0000, v171
	v_add_f32_e32 v92, 1.0, v92
	v_pk_fma_f32 v[10:11], s[2:3], v[156:157], v[150:151] op_sel_hi:[0,1,1]
	v_lshlrev_b32_e32 v150, 16, v174
	v_and_b32_e32 v151, 0xffff0000, v174
	v_lshlrev_b32_e32 v152, 16, v175
	v_and_b32_e32 v153, 0xffff0000, v175
	v_pk_mul_f32 v[90:91], v[96:97], v[160:161]
	v_add_f32_e32 v96, 1.0, v158
	v_rcp_f32_e32 v158, v92
	v_add_f32_e32 v92, 1.0, v93
	v_add_f32_e32 v97, 1.0, v159
	v_rcp_f32_e32 v159, v92
	v_pk_fma_f32 v[92:93], s[2:3], v[152:153], v[90:91] op_sel_hi:[0,1,1]
	v_pk_fma_f32 v[90:91], s[2:3], v[150:151], v[94:95] op_sel_hi:[0,1,1]
	s_waitcnt vmcnt(4)
	v_lshlrev_b32_e32 v150, 16, v20
	v_and_b32_e32 v151, 0xffff0000, v20
	v_lshlrev_b32_e32 v152, 16, v21
	v_and_b32_e32 v153, 0xffff0000, v21
	v_lshlrev_b32_e32 v20, 16, v18
	v_and_b32_e32 v21, 0xffff0000, v18
	v_pk_mul_f32 v[142:143], v[142:143], v[20:21]
	v_mul_f32_e32 v20, v138, v213
	v_exp_f32_e32 v20, v20
	v_mul_f32_e32 v21, v139, v213
	v_mul_f32_e32 v144, v144, v213
	v_mul_f32_e32 v145, v145, v213
	v_exp_f32_e32 v21, v21
	v_exp_f32_e32 v144, v144
	v_exp_f32_e32 v145, v145
	v_mul_f32_e32 v106, v106, v213
	v_mul_f32_e32 v107, v107, v213
	v_add_f32_e32 v20, 1.0, v20
	v_exp_f32_e32 v106, v106
	v_exp_f32_e32 v107, v107
	v_rcp_f32_e32 v138, v20
	v_add_f32_e32 v20, 1.0, v21
	v_mul_f32_e32 v21, v140, v213
	v_rcp_f32_e32 v96, v96
	v_rcp_f32_e32 v97, v97
	v_add_f32_e32 v144, 1.0, v144
	v_add_f32_e32 v145, 1.0, v145
	v_exp_f32_e32 v21, v21
	v_mul_f32_e32 v139, v141, v213
	v_pk_fma_f32 v[6:7], s[2:3], v[6:7], v[154:155] op_sel_hi:[0,1,1]
	v_lshlrev_b32_e32 v154, 16, v216
	v_and_b32_e32 v155, 0xffff0000, v216
	v_rcp_f32_e32 v144, v144
	v_rcp_f32_e32 v145, v145
	v_exp_f32_e32 v141, v139
	v_mul_f32_e32 v108, v108, v213
	v_mul_f32_e32 v109, v109, v213
	v_pk_fma_f32 v[78:79], s[2:3], v[154:155], v[78:79] op_sel_hi:[0,1,1]
	v_lshlrev_b32_e32 v154, 16, v16
	v_and_b32_e32 v155, 0xffff0000, v16
	v_rcp_f32_e32 v139, v20
	v_add_f32_e32 v106, 1.0, v106
	v_add_f32_e32 v107, 1.0, v107
	v_exp_f32_e32 v108, v108
	v_exp_f32_e32 v109, v109
	v_pk_fma_f32 v[14:15], s[2:3], v[154:155], v[14:15] op_sel_hi:[0,1,1]
	v_lshlrev_b32_e32 v154, 16, v172
	v_and_b32_e32 v155, 0xffff0000, v172
	v_lshlrev_b32_e32 v156, 16, v173
	v_and_b32_e32 v157, 0xffff0000, v173
	v_rcp_f32_e32 v106, v106
	v_rcp_f32_e32 v107, v107
	v_mul_f32_e32 v134, v134, v213
	v_mul_f32_e32 v135, v135, v213
	v_lshlrev_b32_e32 v148, 16, v177
	v_and_b32_e32 v149, 0xffff0000, v177
	v_pk_mul_f32 v[94:95], v[96:97], v[154:155]
	v_pk_mul_f32 v[96:97], v[158:159], v[156:157]
	v_lshlrev_b32_e32 v18, 16, v19
	v_and_b32_e32 v19, 0xffff0000, v19
	v_add_f32_e32 v20, 1.0, v21
	v_exp_f32_e32 v134, v134
	v_exp_f32_e32 v135, v135
	v_pk_fma_f32 v[96:97], s[2:3], v[148:149], v[96:97] op_sel_hi:[0,1,1]
	v_lshlrev_b32_e32 v148, 16, v22
	v_and_b32_e32 v149, 0xffff0000, v22
	v_lshlrev_b32_e32 v22, 16, v23
	v_and_b32_e32 v23, 0xffff0000, v23
	v_pk_mul_f32 v[18:19], v[144:145], v[18:19]
	v_rcp_f32_e32 v140, v20
	v_add_f32_e32 v20, 1.0, v141
	v_mul_f32_e32 v104, v104, v213
	v_rcp_f32_e32 v141, v20
	v_pk_fma_f32 v[20:21], s[2:3], v[22:23], v[18:19] op_sel_hi:[0,1,1]
	v_pk_mul_f32 v[22:23], v[138:139], v[150:151]
	s_waitcnt vmcnt(1)
	v_lshlrev_b32_e32 v150, 16, v162
	v_and_b32_e32 v151, 0xffff0000, v162
	v_add_f32_e32 v108, 1.0, v108
	v_add_f32_e32 v109, 1.0, v109
	v_mul_f32_e32 v102, v102, v213
	v_exp_f32_e32 v104, v104
	v_mul_f32_e32 v105, v105, v213
	v_rcp_f32_e32 v108, v108
	v_rcp_f32_e32 v109, v109
	v_pk_mul_f32 v[106:107], v[106:107], v[150:151]
	v_exp_f32_e32 v150, v102
	v_mul_f32_e32 v102, v103, v213
	v_exp_f32_e32 v105, v105
	v_exp_f32_e32 v151, v102
	v_add_f32_e32 v134, 1.0, v134
	v_add_f32_e32 v135, 1.0, v135
	v_rcp_f32_e32 v134, v134
	v_rcp_f32_e32 v135, v135
	v_pk_mul_f32 v[138:139], v[140:141], v[152:153]
	v_lshlrev_b32_e32 v152, 16, v163
	v_and_b32_e32 v153, 0xffff0000, v163
	v_add_f32_e32 v104, 1.0, v104
	v_pk_fma_f32 v[18:19], s[2:3], v[148:149], v[142:143] op_sel_hi:[0,1,1]
	v_lshlrev_b32_e32 v142, 16, v166
	v_and_b32_e32 v143, 0xffff0000, v166
	v_lshlrev_b32_e32 v144, 16, v167
	v_and_b32_e32 v145, 0xffff0000, v167
	v_pk_mul_f32 v[102:103], v[108:109], v[152:153]
	v_add_f32_e32 v108, 1.0, v150
	v_rcp_f32_e32 v150, v104
	v_add_f32_e32 v104, 1.0, v105
	v_add_f32_e32 v109, 1.0, v151
	v_rcp_f32_e32 v151, v104
	v_pk_fma_f32 v[104:105], s[2:3], v[144:145], v[102:103] op_sel_hi:[0,1,1]
	v_pk_fma_f32 v[102:103], s[2:3], v[142:143], v[106:107] op_sel_hi:[0,1,1]
	s_waitcnt vmcnt(0)
	v_lshlrev_b32_e32 v142, 16, v28
	v_and_b32_e32 v143, 0xffff0000, v28
	v_lshlrev_b32_e32 v144, 16, v29
	v_and_b32_e32 v145, 0xffff0000, v29
	v_lshlrev_b32_e32 v28, 16, v26
	v_and_b32_e32 v29, 0xffff0000, v26
	v_pk_mul_f32 v[134:135], v[134:135], v[28:29]
	v_mul_f32_e32 v28, v130, v213
	v_exp_f32_e32 v28, v28
	v_mul_f32_e32 v29, v131, v213
	v_exp_f32_e32 v29, v29
	v_mul_f32_e32 v136, v136, v213
	v_add_f32_e32 v28, 1.0, v28
	v_mul_f32_e32 v137, v137, v213
	v_rcp_f32_e32 v130, v28
	v_add_f32_e32 v28, 1.0, v29
	v_mul_f32_e32 v29, v132, v213
	v_exp_f32_e32 v136, v136
	v_exp_f32_e32 v137, v137
	v_exp_f32_e32 v29, v29
	v_mul_f32_e32 v131, v133, v213
	v_exp_f32_e32 v133, v131
	v_lshlrev_b32_e32 v16, 16, v17
	v_and_b32_e32 v17, 0xffff0000, v17
	v_rcp_f32_e32 v108, v108
	v_rcp_f32_e32 v109, v109
	v_add_f32_e32 v136, 1.0, v136
	v_add_f32_e32 v137, 1.0, v137
	v_rcp_f32_e32 v131, v28
	v_add_f32_e32 v28, 1.0, v29
	v_pk_fma_f32 v[16:17], s[2:3], v[16:17], v[146:147] op_sel_hi:[0,1,1]
	v_lshlrev_b32_e32 v146, 16, v176
	v_and_b32_e32 v147, 0xffff0000, v176
	v_rcp_f32_e32 v136, v136
	v_rcp_f32_e32 v137, v137
	v_rcp_f32_e32 v132, v28
	v_add_f32_e32 v28, 1.0, v133
	v_pk_fma_f32 v[94:95], s[2:3], v[146:147], v[94:95] op_sel_hi:[0,1,1]
	v_lshlrev_b32_e32 v146, 16, v24
	v_and_b32_e32 v147, 0xffff0000, v24
	v_rcp_f32_e32 v133, v28
	v_pk_fma_f32 v[22:23], s[2:3], v[146:147], v[22:23] op_sel_hi:[0,1,1]
	v_lshlrev_b32_e32 v146, 16, v164
	v_and_b32_e32 v147, 0xffff0000, v164
	v_lshlrev_b32_e32 v148, 16, v165
	v_and_b32_e32 v149, 0xffff0000, v165
	v_lshlrev_b32_e32 v24, 16, v25
	v_and_b32_e32 v25, 0xffff0000, v25
	v_lshlrev_b32_e32 v140, 16, v169
	v_and_b32_e32 v141, 0xffff0000, v169
	v_pk_mul_f32 v[106:107], v[108:109], v[146:147]
	v_pk_mul_f32 v[108:109], v[150:151], v[148:149]
	v_lshlrev_b32_e32 v26, 16, v27
	v_and_b32_e32 v27, 0xffff0000, v27
	v_pk_fma_f32 v[24:25], s[2:3], v[24:25], v[138:139] op_sel_hi:[0,1,1]
	v_lshlrev_b32_e32 v138, 16, v168
	v_and_b32_e32 v139, 0xffff0000, v168
	v_pk_fma_f32 v[108:109], s[2:3], v[140:141], v[108:109] op_sel_hi:[0,1,1]
	v_lshlrev_b32_e32 v140, 16, v30
	v_and_b32_e32 v141, 0xffff0000, v30
	v_lshlrev_b32_e32 v30, 16, v31
	v_and_b32_e32 v31, 0xffff0000, v31
	v_pk_mul_f32 v[26:27], v[136:137], v[26:27]
	v_pk_fma_f32 v[106:107], s[2:3], v[138:139], v[106:107] op_sel_hi:[0,1,1]
	v_lshlrev_b32_e32 v138, 16, v32
	v_and_b32_e32 v139, 0xffff0000, v32
	v_lshlrev_b32_e32 v32, 16, v33
	v_and_b32_e32 v33, 0xffff0000, v33
	v_pk_fma_f32 v[28:29], s[2:3], v[30:31], v[26:27] op_sel_hi:[0,1,1]
	v_pk_mul_f32 v[30:31], v[130:131], v[142:143]
	v_pk_mul_f32 v[130:131], v[132:133], v[144:145]
	v_pk_fma_f32 v[26:27], s[2:3], v[140:141], v[134:135] op_sel_hi:[0,1,1]
	v_pk_fma_f32 v[32:33], s[2:3], v[32:33], v[130:131] op_sel_hi:[0,1,1]
	v_add_u32_e32 v130, 0x80, v200
	v_ashrrev_i32_e32 v131, 31, v130
	v_lshlrev_b64 v[190:191], 11, v[130:131]
	v_lshl_add_u64 v[208:209], v[190:191], 0, v[184:185]
	v_pk_fma_f32 v[30:31], s[2:3], v[138:139], v[30:31] op_sel_hi:[0,1,1]
	v_lshlrev_b64 v[130:131], 1, v[208:209]
	v_lshl_add_u64 v[132:133], s[22:23], 0, v[130:131]
	global_load_dwordx4 v[134:137], v[132:133], off
	v_lshl_add_u64 v[130:131], s[24:25], 0, v[130:131]
	global_load_dwordx4 v[142:145], v[130:131], off
	global_load_dwordx4 v[214:217], v[132:133], off offset:256
	global_load_dwordx4 v[218:221], v[130:131], off offset:256
	v_add_u32_e32 v130, 0x90, v200
	v_ashrrev_i32_e32 v131, 31, v130
	v_lshlrev_b64 v[188:189], 11, v[130:131]
	v_lshl_add_u64 v[206:207], v[188:189], 0, v[184:185]
	v_lshlrev_b64 v[130:131], 1, v[206:207]
	v_lshl_add_u64 v[132:133], s[22:23], 0, v[130:131]
	v_lshl_add_u64 v[130:131], s[24:25], 0, v[130:131]
	global_load_dwordx4 v[222:225], v[132:133], off
	global_load_dwordx4 v[166:169], v[132:133], off offset:256
	global_load_dwordx4 v[170:173], v[130:131], off
	global_load_dwordx4 v[162:165], v[130:131], off offset:256
	v_add_u32_e32 v130, 0xa0, v200
	v_ashrrev_i32_e32 v131, 31, v130
	v_lshlrev_b64 v[176:177], 11, v[130:131]
	v_lshl_add_u64 v[204:205], v[176:177], 0, v[184:185]
	v_lshlrev_b64 v[130:131], 1, v[204:205]
	v_lshl_add_u64 v[132:133], s[22:23], 0, v[130:131]
	v_lshl_add_u64 v[130:131], s[24:25], 0, v[130:131]
	global_load_dwordx4 v[158:161], v[132:133], off
	global_load_dwordx4 v[150:153], v[132:133], off offset:256
	global_load_dwordx4 v[154:157], v[130:131], off
	global_load_dwordx4 v[146:149], v[130:131], off offset:256
	v_add_u32_e32 v130, 0xb0, v200
	v_ashrrev_i32_e32 v131, 31, v130
	v_lshlrev_b64 v[174:175], 11, v[130:131]
	v_lshl_add_u64 v[200:201], v[174:175], 0, v[184:185]
	v_lshlrev_b64 v[130:131], 1, v[200:201]
	v_lshl_add_u64 v[132:133], s[22:23], 0, v[130:131]
	v_lshl_add_u64 v[226:227], s[24:25], 0, v[130:131]
	global_load_dwordx4 v[138:141], v[132:133], off
	s_nop 0
	global_load_dwordx4 v[130:133], v[132:133], off offset:256
	v_mul_f32_e32 v118, v118, v213
	v_mul_f32_e32 v119, v119, v213
	v_mul_f32_e32 v120, v120, v213
	v_mul_f32_e32 v121, v121, v213
	v_exp_f32_e32 v118, v118
	v_exp_f32_e32 v119, v119
	v_exp_f32_e32 v120, v120
	v_exp_f32_e32 v121, v121
	v_mul_f32_e32 v38, v38, v213
	v_mul_f32_e32 v39, v39, v213
	v_exp_f32_e32 v38, v38
	v_exp_f32_e32 v39, v39
	v_mul_f32_e32 v116, v116, v213
	v_add_f32_e32 v118, 1.0, v118
	v_add_f32_e32 v119, 1.0, v119
	v_add_f32_e32 v120, 1.0, v120
	v_add_f32_e32 v121, 1.0, v121
	v_mul_f32_e32 v114, v114, v213
	v_exp_f32_e32 v116, v116
	v_mul_f32_e32 v117, v117, v213
	v_rcp_f32_e32 v118, v118
	v_rcp_f32_e32 v119, v119
	v_rcp_f32_e32 v120, v120
	v_rcp_f32_e32 v121, v121
	v_exp_f32_e32 v117, v117
	v_add_f32_e32 v38, 1.0, v38
	v_add_f32_e32 v39, 1.0, v39
	v_mul_f32_e32 v40, v40, v213
	v_mul_f32_e32 v41, v41, v213
	v_rcp_f32_e32 v38, v38
	v_exp_f32_e32 v40, v40
	v_exp_f32_e32 v41, v41
	v_rcp_f32_e32 v39, v39
	v_add_f32_e32 v116, 1.0, v116
	v_mul_f32_e32 v34, v34, v213
	v_mul_f32_e32 v36, v36, v213
	v_add_f32_e32 v40, 1.0, v40
	v_add_f32_e32 v41, 1.0, v41
	v_exp_f32_e32 v36, v36
	v_mul_f32_e32 v37, v37, v213
	v_rcp_f32_e32 v40, v40
	v_rcp_f32_e32 v41, v41
	v_exp_f32_e32 v37, v37
	v_mul_f32_e32 v126, v126, v213
	v_mul_f32_e32 v127, v127, v213
	v_exp_f32_e32 v126, v126
	v_exp_f32_e32 v127, v127
	v_add_f32_e32 v36, 1.0, v36
	v_mul_f32_e32 v128, v128, v213
	v_add_f32_e32 v126, 1.0, v126
	v_add_f32_e32 v127, 1.0, v127
	v_mul_f32_e32 v129, v129, v213
	v_rcp_f32_e32 v126, v126
	s_waitcnt vmcnt(13)
	v_lshlrev_b32_e32 v228, 16, v136
	v_and_b32_e32 v229, 0xffff0000, v136
	v_lshlrev_b32_e32 v230, 16, v137
	v_and_b32_e32 v231, 0xffff0000, v137
	v_lshlrev_b32_e32 v232, 16, v134
	v_and_b32_e32 v233, 0xffff0000, v134
	v_lshlrev_b32_e32 v238, 16, v135
	v_and_b32_e32 v239, 0xffff0000, v135
	s_waitcnt vmcnt(12)
	v_lshlrev_b32_e32 v240, 16, v144
	v_and_b32_e32 v241, 0xffff0000, v144
	v_lshlrev_b32_e32 v244, 16, v145
	v_and_b32_e32 v245, 0xffff0000, v145
	v_lshlrev_b32_e32 v246, 16, v142
	v_and_b32_e32 v247, 0xffff0000, v142
	v_lshlrev_b32_e32 v250, 16, v143
	v_and_b32_e32 v251, 0xffff0000, v143
	global_load_dwordx4 v[142:145], v[226:227], off
	global_load_dwordx4 v[134:137], v[226:227], off offset:256
	v_exp_f32_e32 v226, v114
	v_mul_f32_e32 v114, v115, v213
	v_exp_f32_e32 v227, v114
	v_pk_mul_f32 v[118:119], v[118:119], v[246:247]
	v_pk_mul_f32 v[114:115], v[120:121], v[250:251]
	v_add_f32_e32 v120, 1.0, v226
	v_rcp_f32_e32 v226, v116
	v_add_f32_e32 v116, 1.0, v117
	v_add_f32_e32 v121, 1.0, v227
	v_rcp_f32_e32 v227, v116
	v_pk_fma_f32 v[116:117], s[2:3], v[238:239], v[114:115] op_sel_hi:[0,1,1]
	v_pk_fma_f32 v[114:115], s[2:3], v[232:233], v[118:119] op_sel_hi:[0,1,1]
	s_waitcnt vmcnt(12)
	v_lshlrev_b32_e32 v232, 16, v218
	v_and_b32_e32 v233, 0xffff0000, v218
	v_pk_mul_f32 v[38:39], v[38:39], v[232:233]
	v_exp_f32_e32 v232, v34
	v_mul_f32_e32 v34, v35, v213
	v_exp_f32_e32 v233, v34
	v_rcp_f32_e32 v120, v120
	v_rcp_f32_e32 v121, v121
	v_lshlrev_b32_e32 v218, 16, v219
	v_and_b32_e32 v219, 0xffff0000, v219
	v_pk_mul_f32 v[34:35], v[40:41], v[218:219]
	v_add_f32_e32 v40, 1.0, v232
	v_add_f32_e32 v41, 1.0, v233
	v_rcp_f32_e32 v218, v36
	v_add_f32_e32 v36, 1.0, v37
	v_rcp_f32_e32 v40, v40
	v_rcp_f32_e32 v41, v41
	v_rcp_f32_e32 v219, v36
	v_pk_mul_f32 v[118:119], v[120:121], v[240:241]
	v_pk_mul_f32 v[120:121], v[226:227], v[244:245]
	v_exp_f32_e32 v128, v128
	v_exp_f32_e32 v129, v129
	v_rcp_f32_e32 v127, v127
	v_pk_fma_f32 v[120:121], s[2:3], v[230:231], v[120:121] op_sel_hi:[0,1,1]
	v_pk_fma_f32 v[118:119], s[2:3], v[228:229], v[118:119] op_sel_hi:[0,1,1]
	v_lshlrev_b32_e32 v228, 16, v214
	v_and_b32_e32 v229, 0xffff0000, v214
	v_lshlrev_b32_e32 v214, 16, v215
	v_and_b32_e32 v215, 0xffff0000, v215
	v_lshlrev_b32_e32 v230, 16, v220
	v_and_b32_e32 v231, 0xffff0000, v220
	v_lshlrev_b32_e32 v220, 16, v221
	v_and_b32_e32 v221, 0xffff0000, v221
	v_lshlrev_b32_e32 v226, 16, v216
	v_and_b32_e32 v227, 0xffff0000, v216
	v_lshlrev_b32_e32 v216, 16, v217
	v_and_b32_e32 v217, 0xffff0000, v217
	v_pk_fma_f32 v[36:37], s[2:3], v[214:215], v[34:35] op_sel_hi:[0,1,1]
	v_pk_fma_f32 v[34:35], s[2:3], v[228:229], v[38:39] op_sel_hi:[0,1,1]
	v_pk_mul_f32 v[38:39], v[40:41], v[230:231]
	v_pk_mul_f32 v[40:41], v[218:219], v[220:221]
	s_waitcnt vmcnt(11)
	v_lshlrev_b32_e32 v214, 16, v224
	v_pk_fma_f32 v[40:41], s[2:3], v[216:217], v[40:41] op_sel_hi:[0,1,1]
	v_and_b32_e32 v215, 0xffff0000, v224
	v_lshlrev_b32_e32 v216, 16, v225
	v_and_b32_e32 v217, 0xffff0000, v225
	s_waitcnt vmcnt(9)
	v_lshlrev_b32_e32 v224, 16, v170
	v_and_b32_e32 v225, 0xffff0000, v170
	v_mul_f32_e32 v122, v122, v213
	v_mul_f32_e32 v124, v124, v213
	v_add_f32_e32 v128, 1.0, v128
	v_add_f32_e32 v129, 1.0, v129
	v_pk_mul_f32 v[126:127], v[126:127], v[224:225]
	v_exp_f32_e32 v224, v122
	v_mul_f32_e32 v122, v123, v213
	v_exp_f32_e32 v124, v124
	v_mul_f32_e32 v125, v125, v213
	v_rcp_f32_e32 v128, v128
	v_rcp_f32_e32 v129, v129
	v_exp_f32_e32 v225, v122
	v_exp_f32_e32 v125, v125
	v_mul_f32_e32 v46, v46, v213
	v_mul_f32_e32 v47, v47, v213
	v_exp_f32_e32 v46, v46
	v_exp_f32_e32 v47, v47
	v_lshlrev_b32_e32 v170, 16, v171
	v_and_b32_e32 v171, 0xffff0000, v171
	v_add_f32_e32 v124, 1.0, v124
	v_pk_mul_f32 v[122:123], v[128:129], v[170:171]
	v_add_f32_e32 v128, 1.0, v224
	v_add_f32_e32 v129, 1.0, v225
	v_rcp_f32_e32 v170, v124
	v_add_f32_e32 v124, 1.0, v125
	v_rcp_f32_e32 v128, v128
	v_rcp_f32_e32 v129, v129
	v_rcp_f32_e32 v171, v124
	v_add_f32_e32 v46, 1.0, v46
	v_add_f32_e32 v47, 1.0, v47
	v_mul_f32_e32 v48, v48, v213
	v_mul_f32_e32 v49, v49, v213
	v_rcp_f32_e32 v46, v46
	v_exp_f32_e32 v48, v48
	v_exp_f32_e32 v49, v49
	v_rcp_f32_e32 v47, v47
	v_lshlrev_b32_e32 v218, 16, v222
	v_and_b32_e32 v219, 0xffff0000, v222
	v_lshlrev_b32_e32 v220, 16, v223
	v_and_b32_e32 v221, 0xffff0000, v223
	v_lshlrev_b32_e32 v222, 16, v172
	v_and_b32_e32 v223, 0xffff0000, v172
	v_lshlrev_b32_e32 v172, 16, v173
	v_and_b32_e32 v173, 0xffff0000, v173
	v_pk_fma_f32 v[124:125], s[2:3], v[220:221], v[122:123] op_sel_hi:[0,1,1]
	v_pk_fma_f32 v[122:123], s[2:3], v[218:219], v[126:127] op_sel_hi:[0,1,1]
	v_pk_mul_f32 v[126:127], v[128:129], v[222:223]
	v_pk_mul_f32 v[128:129], v[170:171], v[172:173]
	v_mul_f32_e32 v42, v42, v213
	v_pk_fma_f32 v[128:129], s[2:3], v[216:217], v[128:129] op_sel_hi:[0,1,1]
	s_waitcnt vmcnt(8)
	v_lshlrev_b32_e32 v216, 16, v162
	v_and_b32_e32 v217, 0xffff0000, v162
	v_mul_f32_e32 v44, v44, v213
	v_add_f32_e32 v48, 1.0, v48
	v_add_f32_e32 v49, 1.0, v49
	v_pk_mul_f32 v[46:47], v[46:47], v[216:217]
	v_exp_f32_e32 v216, v42
	v_mul_f32_e32 v42, v43, v213
	v_exp_f32_e32 v44, v44
	v_mul_f32_e32 v45, v45, v213
	v_rcp_f32_e32 v48, v48
	v_rcp_f32_e32 v49, v49
	v_exp_f32_e32 v217, v42
	v_exp_f32_e32 v45, v45
	v_mul_f32_e32 v110, v110, v213
	v_mul_f32_e32 v111, v111, v213
	v_exp_f32_e32 v110, v110
	v_exp_f32_e32 v111, v111
	v_lshlrev_b32_e32 v162, 16, v163
	v_and_b32_e32 v163, 0xffff0000, v163
	v_add_f32_e32 v44, 1.0, v44
	v_pk_mul_f32 v[42:43], v[48:49], v[162:163]
	v_add_f32_e32 v48, 1.0, v216
	v_add_f32_e32 v49, 1.0, v217
	v_rcp_f32_e32 v162, v44
	v_add_f32_e32 v44, 1.0, v45
	v_rcp_f32_e32 v48, v48
	v_rcp_f32_e32 v49, v49
	v_rcp_f32_e32 v163, v44
	v_add_f32_e32 v110, 1.0, v110
	v_add_f32_e32 v111, 1.0, v111
	v_mul_f32_e32 v112, v112, v213
	v_mul_f32_e32 v113, v113, v213
	v_rcp_f32_e32 v110, v110
	v_exp_f32_e32 v112, v112
	v_exp_f32_e32 v113, v113
	v_rcp_f32_e32 v111, v111
	v_pk_fma_f32 v[126:127], s[2:3], v[214:215], v[126:127] op_sel_hi:[0,1,1]
	v_lshlrev_b32_e32 v172, 16, v166
	v_and_b32_e32 v173, 0xffff0000, v166
	v_lshlrev_b32_e32 v166, 16, v167
	v_and_b32_e32 v167, 0xffff0000, v167
	v_lshlrev_b32_e32 v214, 16, v164
	v_and_b32_e32 v215, 0xffff0000, v164
	v_lshlrev_b32_e32 v164, 16, v165
	v_and_b32_e32 v165, 0xffff0000, v165
	v_lshlrev_b32_e32 v170, 16, v168
	v_and_b32_e32 v171, 0xffff0000, v168
	v_lshlrev_b32_e32 v168, 16, v169
	v_and_b32_e32 v169, 0xffff0000, v169
	v_pk_fma_f32 v[44:45], s[2:3], v[166:167], v[42:43] op_sel_hi:[0,1,1]
	v_pk_fma_f32 v[42:43], s[2:3], v[172:173], v[46:47] op_sel_hi:[0,1,1]
	v_pk_mul_f32 v[46:47], v[48:49], v[214:215]
	v_pk_mul_f32 v[48:49], v[162:163], v[164:165]
	v_mul_f32_e32 v98, v98, v213
	v_pk_fma_f32 v[48:49], s[2:3], v[168:169], v[48:49] op_sel_hi:[0,1,1]
	s_waitcnt vmcnt(5)
	v_lshlrev_b32_e32 v168, 16, v154
	v_and_b32_e32 v169, 0xffff0000, v154
	v_mul_f32_e32 v100, v100, v213
	v_add_f32_e32 v112, 1.0, v112
	v_add_f32_e32 v113, 1.0, v113
	v_pk_mul_f32 v[110:111], v[110:111], v[168:169]
	v_exp_f32_e32 v168, v98
	v_mul_f32_e32 v98, v99, v213
	v_exp_f32_e32 v100, v100
	v_mul_f32_e32 v101, v101, v213
	v_rcp_f32_e32 v112, v112
	v_rcp_f32_e32 v113, v113
	v_exp_f32_e32 v169, v98
	v_exp_f32_e32 v101, v101
	v_mul_f32_e32 v54, v54, v213
	v_mul_f32_e32 v55, v55, v213
	v_exp_f32_e32 v54, v54
	v_exp_f32_e32 v55, v55
	v_lshlrev_b32_e32 v154, 16, v155
	v_and_b32_e32 v155, 0xffff0000, v155
	v_add_f32_e32 v100, 1.0, v100
	v_pk_mul_f32 v[98:99], v[112:113], v[154:155]
	v_add_f32_e32 v112, 1.0, v168
	v_add_f32_e32 v113, 1.0, v169
	v_rcp_f32_e32 v154, v100
	v_add_f32_e32 v100, 1.0, v101
	v_rcp_f32_e32 v112, v112
	v_rcp_f32_e32 v113, v113
	v_rcp_f32_e32 v155, v100
	v_add_f32_e32 v54, 1.0, v54
	v_add_f32_e32 v55, 1.0, v55
	v_mul_f32_e32 v56, v56, v213
	v_mul_f32_e32 v57, v57, v213
	v_rcp_f32_e32 v54, v54
	v_exp_f32_e32 v56, v56
	v_exp_f32_e32 v57, v57
	v_rcp_f32_e32 v55, v55
	v_lshlrev_b32_e32 v164, 16, v158
	v_and_b32_e32 v165, 0xffff0000, v158
	v_lshlrev_b32_e32 v158, 16, v159
	v_and_b32_e32 v159, 0xffff0000, v159
	v_lshlrev_b32_e32 v166, 16, v156
	v_and_b32_e32 v167, 0xffff0000, v156
	v_lshlrev_b32_e32 v156, 16, v157
	v_and_b32_e32 v157, 0xffff0000, v157
	v_lshlrev_b32_e32 v162, 16, v160
	v_and_b32_e32 v163, 0xffff0000, v160
	v_lshlrev_b32_e32 v160, 16, v161
	v_and_b32_e32 v161, 0xffff0000, v161
	v_pk_fma_f32 v[100:101], s[2:3], v[158:159], v[98:99] op_sel_hi:[0,1,1]
	v_pk_fma_f32 v[98:99], s[2:3], v[164:165], v[110:111] op_sel_hi:[0,1,1]
	v_pk_mul_f32 v[110:111], v[112:113], v[166:167]
	v_pk_mul_f32 v[112:113], v[154:155], v[156:157]
	v_mul_f32_e32 v50, v50, v213
	v_pk_fma_f32 v[112:113], s[2:3], v[160:161], v[112:113] op_sel_hi:[0,1,1]
	s_waitcnt vmcnt(4)
	v_lshlrev_b32_e32 v160, 16, v146
	v_and_b32_e32 v161, 0xffff0000, v146
	v_mul_f32_e32 v52, v52, v213
	v_add_f32_e32 v56, 1.0, v56
	v_add_f32_e32 v57, 1.0, v57
	v_pk_mul_f32 v[54:55], v[54:55], v[160:161]
	v_exp_f32_e32 v160, v50
	v_mul_f32_e32 v50, v51, v213
	v_exp_f32_e32 v52, v52
	v_mul_f32_e32 v53, v53, v213
	v_rcp_f32_e32 v56, v56
	v_rcp_f32_e32 v57, v57
	v_exp_f32_e32 v161, v50
	v_exp_f32_e32 v53, v53
	v_mul_f32_e32 v86, v86, v213
	v_mul_f32_e32 v87, v87, v213
	v_exp_f32_e32 v86, v86
	v_exp_f32_e32 v87, v87
	v_lshlrev_b32_e32 v146, 16, v147
	v_and_b32_e32 v147, 0xffff0000, v147
	v_add_f32_e32 v52, 1.0, v52
	v_pk_mul_f32 v[50:51], v[56:57], v[146:147]
	v_add_f32_e32 v56, 1.0, v160
	v_add_f32_e32 v57, 1.0, v161
	v_rcp_f32_e32 v146, v52
	v_add_f32_e32 v52, 1.0, v53
	v_rcp_f32_e32 v56, v56
	v_rcp_f32_e32 v57, v57
	v_rcp_f32_e32 v147, v52
	v_add_f32_e32 v86, 1.0, v86
	v_add_f32_e32 v87, 1.0, v87
	v_mul_f32_e32 v88, v88, v213
	v_mul_f32_e32 v89, v89, v213
	v_rcp_f32_e32 v86, v86
	v_exp_f32_e32 v88, v88
	v_exp_f32_e32 v89, v89
	v_rcp_f32_e32 v87, v87
	v_lshlrev_b32_e32 v156, 16, v150
	v_and_b32_e32 v157, 0xffff0000, v150
	v_lshlrev_b32_e32 v150, 16, v151
	v_and_b32_e32 v151, 0xffff0000, v151
	v_lshlrev_b32_e32 v158, 16, v148
	v_and_b32_e32 v159, 0xffff0000, v148
	v_lshlrev_b32_e32 v148, 16, v149
	v_and_b32_e32 v149, 0xffff0000, v149
	v_lshlrev_b32_e32 v154, 16, v152
	v_and_b32_e32 v155, 0xffff0000, v152
	v_lshlrev_b32_e32 v152, 16, v153
	v_and_b32_e32 v153, 0xffff0000, v153
	v_pk_fma_f32 v[52:53], s[2:3], v[150:151], v[50:51] op_sel_hi:[0,1,1]
	v_pk_fma_f32 v[50:51], s[2:3], v[156:157], v[54:55] op_sel_hi:[0,1,1]
	v_pk_mul_f32 v[54:55], v[56:57], v[158:159]
	v_pk_mul_f32 v[56:57], v[146:147], v[148:149]
	v_mul_f32_e32 v82, v82, v213
	v_pk_fma_f32 v[56:57], s[2:3], v[152:153], v[56:57] op_sel_hi:[0,1,1]
	s_waitcnt vmcnt(1)
	v_lshlrev_b32_e32 v152, 16, v142
	v_and_b32_e32 v153, 0xffff0000, v142
	v_mul_f32_e32 v84, v84, v213
	v_add_f32_e32 v88, 1.0, v88
	v_add_f32_e32 v89, 1.0, v89
	v_pk_mul_f32 v[86:87], v[86:87], v[152:153]
	v_exp_f32_e32 v152, v82
	v_mul_f32_e32 v82, v83, v213
	v_exp_f32_e32 v84, v84
	v_mul_f32_e32 v85, v85, v213
	v_rcp_f32_e32 v88, v88
	v_rcp_f32_e32 v89, v89
	v_exp_f32_e32 v153, v82
	v_exp_f32_e32 v85, v85
	v_mul_f32_e32 v70, v70, v213
	v_mul_f32_e32 v71, v71, v213
	v_exp_f32_e32 v70, v70
	v_exp_f32_e32 v71, v71
	v_lshlrev_b32_e32 v142, 16, v143
	v_and_b32_e32 v143, 0xffff0000, v143
	v_add_f32_e32 v84, 1.0, v84
	v_pk_mul_f32 v[82:83], v[88:89], v[142:143]
	v_add_f32_e32 v88, 1.0, v152
	v_add_f32_e32 v89, 1.0, v153
	v_rcp_f32_e32 v142, v84
	v_add_f32_e32 v84, 1.0, v85
	v_rcp_f32_e32 v88, v88
	v_rcp_f32_e32 v89, v89
	v_rcp_f32_e32 v143, v84
	v_add_f32_e32 v70, 1.0, v70
	v_add_f32_e32 v71, 1.0, v71
	v_mul_f32_e32 v72, v72, v213
	v_mul_f32_e32 v73, v73, v213
	v_rcp_f32_e32 v70, v70
	v_exp_f32_e32 v72, v72
	v_exp_f32_e32 v73, v73
	v_rcp_f32_e32 v71, v71
	v_lshlrev_b32_e32 v148, 16, v138
	v_and_b32_e32 v149, 0xffff0000, v138
	v_lshlrev_b32_e32 v138, 16, v139
	v_and_b32_e32 v139, 0xffff0000, v139
	v_lshlrev_b32_e32 v150, 16, v144
	v_and_b32_e32 v151, 0xffff0000, v144
	v_lshlrev_b32_e32 v144, 16, v145
	v_and_b32_e32 v145, 0xffff0000, v145
	v_pk_fma_f32 v[84:85], s[2:3], v[138:139], v[82:83] op_sel_hi:[0,1,1]
	v_pk_fma_f32 v[82:83], s[2:3], v[148:149], v[86:87] op_sel_hi:[0,1,1]
	v_pk_mul_f32 v[86:87], v[88:89], v[150:151]
	v_pk_mul_f32 v[88:89], v[142:143], v[144:145]
	s_waitcnt vmcnt(0)
	v_lshlrev_b32_e32 v144, 16, v134
	v_and_b32_e32 v145, 0xffff0000, v134
	v_mul_f32_e32 v66, v66, v213
	v_mul_f32_e32 v68, v68, v213
	v_add_f32_e32 v72, 1.0, v72
	v_add_f32_e32 v73, 1.0, v73
	v_pk_mul_f32 v[70:71], v[70:71], v[144:145]
	v_exp_f32_e32 v144, v66
	v_mul_f32_e32 v66, v67, v213
	v_exp_f32_e32 v68, v68
	v_mul_f32_e32 v69, v69, v213
	v_rcp_f32_e32 v72, v72
	v_rcp_f32_e32 v73, v73
	v_exp_f32_e32 v145, v66
	v_exp_f32_e32 v69, v69
	v_lshlrev_b32_e32 v134, 16, v135
	v_and_b32_e32 v135, 0xffff0000, v135
	v_add_f32_e32 v68, 1.0, v68
	v_pk_mul_f32 v[66:67], v[72:73], v[134:135]
	v_add_f32_e32 v72, 1.0, v144
	v_add_f32_e32 v73, 1.0, v145
	v_rcp_f32_e32 v134, v68
	v_add_f32_e32 v68, 1.0, v69
	v_rcp_f32_e32 v72, v72
	v_rcp_f32_e32 v73, v73
	v_rcp_f32_e32 v135, v68
	v_lshlrev_b32_e32 v146, 16, v140
	v_and_b32_e32 v147, 0xffff0000, v140
	v_lshlrev_b32_e32 v140, 16, v141
	v_and_b32_e32 v141, 0xffff0000, v141
	v_pk_fma_f32 v[88:89], s[2:3], v[140:141], v[88:89] op_sel_hi:[0,1,1]
	v_lshlrev_b32_e32 v140, 16, v130
	v_and_b32_e32 v141, 0xffff0000, v130
	v_lshlrev_b32_e32 v130, 16, v131
	v_and_b32_e32 v131, 0xffff0000, v131
	v_lshlrev_b32_e32 v142, 16, v136
	v_and_b32_e32 v143, 0xffff0000, v136
	v_lshlrev_b32_e32 v136, 16, v137
	v_and_b32_e32 v137, 0xffff0000, v137
	v_lshlrev_b32_e32 v138, 16, v132
	v_and_b32_e32 v139, 0xffff0000, v132
	v_lshlrev_b32_e32 v132, 16, v133
	v_and_b32_e32 v133, 0xffff0000, v133
	v_pk_fma_f32 v[68:69], s[2:3], v[130:131], v[66:67] op_sel_hi:[0,1,1]
	v_pk_fma_f32 v[66:67], s[2:3], v[140:141], v[70:71] op_sel_hi:[0,1,1]
	v_pk_mul_f32 v[70:71], v[72:73], v[142:143]
	v_pk_mul_f32 v[72:73], v[134:135], v[136:137]
	v_add_f32_e32 v130, v58, v59
	v_add_f32_e32 v131, v60, v61
	v_pk_fma_f32 v[72:73], s[2:3], v[132:133], v[72:73] op_sel_hi:[0,1,1]
	v_add_f32_e32 v130, v130, v131
	v_mul_f32_e32 v131, v59, v59
	v_mul_f32_e32 v132, v61, v61
	v_fmac_f32_e32 v131, v58, v58
	v_fmac_f32_e32 v132, v60, v60
	v_add_f32_e32 v131, v131, v132
	v_add_f32_e32 v132, v62, v63
	v_add_f32_e32 v133, v64, v65
	v_add_f32_e32 v130, 0, v130
	v_add_f32_e32 v132, v132, v133
	v_add_f32_e32 v130, v132, v130
	v_mul_f32_e32 v132, v63, v63
	v_mul_f32_e32 v133, v65, v65
	v_fmac_f32_e32 v132, v62, v62
	v_fmac_f32_e32 v133, v64, v64
	v_add_f32_e32 v132, v132, v133
	v_add_f32_e32 v131, v131, v132
	v_add_f32_e32 v132, v2, v3
	v_add_f32_e32 v133, v4, v5
	v_add_f32_e32 v132, v132, v133
	v_add_f32_e32 v130, v132, v130
	v_mul_f32_e32 v132, v3, v3
	v_mul_f32_e32 v133, v5, v5
	v_fmac_f32_e32 v132, v2, v2
	v_fmac_f32_e32 v133, v4, v4
	v_add_f32_e32 v132, v132, v133
	v_add_f32_e32 v131, v132, v131
	v_add_f32_e32 v132, v6, v7
	v_add_f32_e32 v133, v8, v9
	v_add_f32_e32 v132, v132, v133
	v_add_f32_e32 v130, v132, v130
	v_mul_f32_e32 v132, v7, v7
	v_mul_f32_e32 v133, v9, v9
	v_fmac_f32_e32 v132, v6, v6
	v_fmac_f32_e32 v133, v8, v8
	v_add_f32_e32 v132, v132, v133
	v_add_f32_e32 v132, v132, v131
	ds_swizzle_b32 v131, v130 offset:swizzle(SWAP,16)
	ds_swizzle_b32 v133, v132 offset:swizzle(SWAP,16)
	v_pk_fma_f32 v[38:39], s[2:3], v[226:227], v[38:39] op_sel_hi:[0,1,1]
	v_pk_fma_f32 v[46:47], s[2:3], v[170:171], v[46:47] op_sel_hi:[0,1,1]
	v_pk_fma_f32 v[110:111], s[2:3], v[162:163], v[110:111] op_sel_hi:[0,1,1]
	v_pk_fma_f32 v[54:55], s[2:3], v[154:155], v[54:55] op_sel_hi:[0,1,1]
	v_pk_fma_f32 v[86:87], s[2:3], v[146:147], v[86:87] op_sel_hi:[0,1,1]
	v_pk_fma_f32 v[70:71], s[2:3], v[138:139], v[70:71] op_sel_hi:[0,1,1]
	s_waitcnt lgkmcnt(1)
	v_add_f32_e32 v131, v130, v131
	s_waitcnt lgkmcnt(0)
	v_add_f32_e32 v130, v132, v133
	s_lshl_b32 s1, s29, 3
	v_mov_b32_e32 v133, v131
	v_mov_b32_e32 v132, v130
	v_cmp_eq_u32_e32 vcc, 0, v212
	s_add_i32 s1, s1, 0
	v_permlane32_swap_b32_e32 v131, v133
	v_permlane32_swap_b32_e32 v130, v132
	s_and_saveexec_b64 s[2:3], vcc
	s_cbranch_execz .LBB0_683
	v_add_f32_e32 v130, v130, v132
	v_add_f32_e32 v131, v131, v133
	s_lshl_b32 s8, s27, 11
	v_mul_f32_e32 v132, 0x3c800000, v131
	v_fma_f32 v130, -v131, v132, v130
	s_add_i32 s8, s1, s8
	v_max_f32_e32 v133, 0, v130
	v_lshl_add_u32 v130, v0, 5, s8
	ds_write_b64 v130, v[132:133]
.LBB0_683:
	s_or_b64 exec, exec, s[2:3]
	v_add_f32_e32 v130, v74, v75
	v_add_f32_e32 v131, v76, v77
	v_add_f32_e32 v130, v130, v131
	v_mul_f32_e32 v131, v75, v75
	v_mul_f32_e32 v132, v77, v77
	v_fmac_f32_e32 v131, v74, v74
	v_fmac_f32_e32 v132, v76, v76
	v_add_f32_e32 v131, v131, v132
	v_add_f32_e32 v132, v78, v79
	v_add_f32_e32 v133, v80, v81
	v_add_f32_e32 v130, 0, v130
	v_add_f32_e32 v132, v132, v133
	v_add_f32_e32 v130, v132, v130
	v_mul_f32_e32 v132, v79, v79
	v_mul_f32_e32 v133, v81, v81
	v_fmac_f32_e32 v132, v78, v78
	v_fmac_f32_e32 v133, v80, v80
	v_add_f32_e32 v132, v132, v133
	v_add_f32_e32 v131, v131, v132
	v_add_f32_e32 v132, v10, v11
	v_add_f32_e32 v133, v12, v13
	v_add_f32_e32 v132, v132, v133
	v_add_f32_e32 v130, v132, v130
	v_mul_f32_e32 v132, v11, v11
	v_mul_f32_e32 v133, v13, v13
	v_fmac_f32_e32 v132, v10, v10
	v_fmac_f32_e32 v133, v12, v12
	v_add_f32_e32 v132, v132, v133
	v_add_f32_e32 v131, v132, v131
	v_add_f32_e32 v132, v14, v15
	v_add_f32_e32 v133, v16, v17
	v_add_f32_e32 v132, v132, v133
	v_add_f32_e32 v130, v132, v130
	v_mul_f32_e32 v132, v15, v15
	v_mul_f32_e32 v133, v17, v17
	v_fmac_f32_e32 v132, v14, v14
	v_fmac_f32_e32 v133, v16, v16
	v_add_f32_e32 v132, v132, v133
	v_add_f32_e32 v132, v132, v131
	ds_swizzle_b32 v131, v130 offset:swizzle(SWAP,16)
	ds_swizzle_b32 v133, v132 offset:swizzle(SWAP,16)
	s_waitcnt lgkmcnt(1)
	v_add_f32_e32 v131, v130, v131
	s_waitcnt lgkmcnt(0)
	v_add_f32_e32 v130, v132, v133
	v_mov_b32_e32 v133, v131
	v_mov_b32_e32 v132, v130
	s_nop 0
	v_permlane32_swap_b32_e32 v131, v133
	v_permlane32_swap_b32_e32 v130, v132
	s_and_saveexec_b64 s[2:3], vcc
	s_mov_b64 s[52:53], 0x400
	s_cbranch_execz .LBB0_685
	v_add_f32_e32 v130, v130, v132
	v_add_f32_e32 v131, v131, v133
	s_lshl_b32 s8, s27, 11
	v_mul_f32_e32 v132, 0x3c800000, v131
	v_fma_f32 v130, -v131, v132, v130
	s_add_i32 s8, s1, s8
	v_max_f32_e32 v133, 0, v130
	v_lshl_add_u32 v130, v0, 5, s8
	ds_write_b64 v130, v[132:133] offset:512
.LBB0_685:
	s_or_b64 exec, exec, s[2:3]
	v_add_f32_e32 v130, v90, v91
	v_add_f32_e32 v131, v92, v93
	v_add_f32_e32 v130, v130, v131
	v_mul_f32_e32 v131, v91, v91
	v_mul_f32_e32 v132, v93, v93
	v_fmac_f32_e32 v131, v90, v90
	v_fmac_f32_e32 v132, v92, v92
	v_add_f32_e32 v131, v131, v132
	v_add_f32_e32 v132, v94, v95
	v_add_f32_e32 v133, v96, v97
	v_add_f32_e32 v130, 0, v130
	v_add_f32_e32 v132, v132, v133
	v_add_f32_e32 v130, v132, v130
	v_mul_f32_e32 v132, v95, v95
	v_mul_f32_e32 v133, v97, v97
	v_fmac_f32_e32 v132, v94, v94
	v_fmac_f32_e32 v133, v96, v96
	v_add_f32_e32 v132, v132, v133
	v_add_f32_e32 v131, v131, v132
	v_add_f32_e32 v132, v18, v19
	v_add_f32_e32 v133, v20, v21
	v_add_f32_e32 v132, v132, v133
	v_add_f32_e32 v130, v132, v130
	v_mul_f32_e32 v132, v19, v19
	v_mul_f32_e32 v133, v21, v21
	v_fmac_f32_e32 v132, v18, v18
	v_fmac_f32_e32 v133, v20, v20
	v_add_f32_e32 v132, v132, v133
	v_add_f32_e32 v131, v132, v131
	v_add_f32_e32 v132, v22, v23
	v_add_f32_e32 v133, v24, v25
	v_add_f32_e32 v132, v132, v133
	v_add_f32_e32 v130, v132, v130
	v_mul_f32_e32 v132, v23, v23
	v_mul_f32_e32 v133, v25, v25
	v_fmac_f32_e32 v132, v22, v22
	v_fmac_f32_e32 v133, v24, v24
	v_add_f32_e32 v132, v132, v133
	v_add_f32_e32 v132, v132, v131
	ds_swizzle_b32 v131, v130 offset:swizzle(SWAP,16)
	ds_swizzle_b32 v133, v132 offset:swizzle(SWAP,16)
	s_waitcnt lgkmcnt(1)
	v_add_f32_e32 v131, v130, v131
	s_waitcnt lgkmcnt(0)
	v_add_f32_e32 v130, v132, v133
	v_mov_b32_e32 v133, v131
	v_mov_b32_e32 v132, v130
	s_nop 0
	v_permlane32_swap_b32_e32 v131, v133
	v_permlane32_swap_b32_e32 v130, v132
	s_and_saveexec_b64 s[2:3], vcc
	s_cbranch_execz .LBB0_687
	v_add_f32_e32 v130, v130, v132
	v_add_f32_e32 v131, v131, v133
	s_lshl_b32 s8, s27, 11
	v_mul_f32_e32 v132, 0x3c800000, v131
	v_fma_f32 v130, -v131, v132, v130
	s_add_i32 s8, s1, s8
	v_max_f32_e32 v133, 0, v130
	v_lshl_add_u32 v130, v0, 5, s8
	ds_write_b64 v130, v[132:133] offset:1024
.LBB0_687:
	s_or_b64 exec, exec, s[2:3]
	v_add_f32_e32 v130, v102, v103
	v_add_f32_e32 v131, v104, v105
	v_add_f32_e32 v130, v130, v131
	v_mul_f32_e32 v131, v103, v103
	v_mul_f32_e32 v132, v105, v105
	v_fmac_f32_e32 v131, v102, v102
	v_fmac_f32_e32 v132, v104, v104
	v_add_f32_e32 v131, v131, v132
	v_add_f32_e32 v132, v106, v107
	v_add_f32_e32 v133, v108, v109
	v_add_f32_e32 v130, 0, v130
	v_add_f32_e32 v132, v132, v133
	v_add_f32_e32 v130, v132, v130
	v_mul_f32_e32 v132, v107, v107
	v_mul_f32_e32 v133, v109, v109
	v_fmac_f32_e32 v132, v106, v106
	v_fmac_f32_e32 v133, v108, v108
	v_add_f32_e32 v132, v132, v133
	v_add_f32_e32 v131, v131, v132
	v_add_f32_e32 v132, v26, v27
	v_add_f32_e32 v133, v28, v29
	v_add_f32_e32 v132, v132, v133
	v_add_f32_e32 v130, v132, v130
	v_mul_f32_e32 v132, v27, v27
	v_mul_f32_e32 v133, v29, v29
	v_fmac_f32_e32 v132, v26, v26
	v_fmac_f32_e32 v133, v28, v28
	v_add_f32_e32 v132, v132, v133
	v_add_f32_e32 v131, v132, v131
	v_add_f32_e32 v132, v30, v31
	v_add_f32_e32 v133, v32, v33
	v_add_f32_e32 v132, v132, v133
	v_add_f32_e32 v130, v132, v130
	v_mul_f32_e32 v132, v31, v31
	v_mul_f32_e32 v133, v33, v33
	v_fmac_f32_e32 v132, v30, v30
	v_fmac_f32_e32 v133, v32, v32
	v_add_f32_e32 v132, v132, v133
	v_add_f32_e32 v132, v132, v131
	ds_swizzle_b32 v131, v130 offset:swizzle(SWAP,16)
	ds_swizzle_b32 v133, v132 offset:swizzle(SWAP,16)
	s_waitcnt lgkmcnt(1)
	v_add_f32_e32 v131, v130, v131
	s_waitcnt lgkmcnt(0)
	v_add_f32_e32 v130, v132, v133
	v_mov_b32_e32 v133, v131
	v_mov_b32_e32 v132, v130
	s_nop 0
	v_permlane32_swap_b32_e32 v131, v133
	v_permlane32_swap_b32_e32 v130, v132
	s_and_saveexec_b64 s[2:3], vcc
	s_cbranch_execz .LBB0_689
	v_add_f32_e32 v130, v130, v132
	v_add_f32_e32 v131, v131, v133
	s_lshl_b32 s8, s27, 11
	v_mul_f32_e32 v132, 0x3c800000, v131
	v_fma_f32 v130, -v131, v132, v130
	s_add_i32 s8, s1, s8
	v_max_f32_e32 v133, 0, v130
	v_lshl_add_u32 v130, v0, 5, s8
	ds_write_b64 v130, v[132:133] offset:1536
.LBB0_689:
	s_or_b64 exec, exec, s[2:3]
	v_add_f32_e32 v130, v114, v115
	v_add_f32_e32 v131, v116, v117
	v_add_f32_e32 v130, v130, v131
	v_mul_f32_e32 v131, v115, v115
	v_mul_f32_e32 v132, v117, v117
	v_fmac_f32_e32 v131, v114, v114
	v_fmac_f32_e32 v132, v116, v116
	v_add_f32_e32 v131, v131, v132
	v_add_f32_e32 v132, v118, v119
	v_add_f32_e32 v133, v120, v121
	v_add_f32_e32 v130, 0, v130
	v_add_f32_e32 v132, v132, v133
	v_add_f32_e32 v130, v132, v130
	v_mul_f32_e32 v132, v119, v119
	v_mul_f32_e32 v133, v121, v121
	v_fmac_f32_e32 v132, v118, v118
	v_fmac_f32_e32 v133, v120, v120
	v_add_f32_e32 v132, v132, v133
	v_add_f32_e32 v131, v131, v132
	v_add_f32_e32 v132, v34, v35
	v_add_f32_e32 v133, v36, v37
	v_add_f32_e32 v132, v132, v133
	v_add_f32_e32 v130, v132, v130
	v_mul_f32_e32 v132, v35, v35
	v_mul_f32_e32 v133, v37, v37
	v_fmac_f32_e32 v132, v34, v34
	v_fmac_f32_e32 v133, v36, v36
	v_add_f32_e32 v132, v132, v133
	v_add_f32_e32 v131, v132, v131
	v_add_f32_e32 v132, v38, v39
	v_add_f32_e32 v133, v40, v41
	v_add_f32_e32 v132, v132, v133
	v_add_f32_e32 v130, v132, v130
	v_mul_f32_e32 v132, v39, v39
	v_mul_f32_e32 v133, v41, v41
	v_fmac_f32_e32 v132, v38, v38
	v_fmac_f32_e32 v133, v40, v40
	v_add_f32_e32 v132, v132, v133
	v_add_f32_e32 v132, v132, v131
	ds_swizzle_b32 v131, v130 offset:swizzle(SWAP,16)
	ds_swizzle_b32 v133, v132 offset:swizzle(SWAP,16)
	s_waitcnt lgkmcnt(1)
	v_add_f32_e32 v131, v130, v131
	s_waitcnt lgkmcnt(0)
	v_add_f32_e32 v130, v132, v133
	v_mov_b32_e32 v133, v131
	v_mov_b32_e32 v132, v130
	s_nop 0
	v_permlane32_swap_b32_e32 v131, v133
	v_permlane32_swap_b32_e32 v130, v132
	s_and_saveexec_b64 s[2:3], vcc
	s_cbranch_execz .LBB0_691
	v_add_f32_e32 v130, v130, v132
	v_add_f32_e32 v131, v131, v133
	s_lshl_b32 s8, s27, 11
	v_mul_f32_e32 v132, 0x3c800000, v131
	v_fma_f32 v130, -v131, v132, v130
	s_add_i32 s8, s1, s8
	v_max_f32_e32 v133, 0, v130
	v_lshl_add_u32 v130, v0, 5, s8
	ds_write_b64 v130, v[132:133] offset:4096
.LBB0_691:
	s_or_b64 exec, exec, s[2:3]
	v_add_f32_e32 v130, v122, v123
	v_add_f32_e32 v131, v124, v125
	v_add_f32_e32 v130, v130, v131
	v_mul_f32_e32 v131, v123, v123
	v_mul_f32_e32 v132, v125, v125
	v_fmac_f32_e32 v131, v122, v122
	v_fmac_f32_e32 v132, v124, v124
	v_add_f32_e32 v131, v131, v132
	v_add_f32_e32 v132, v126, v127
	v_add_f32_e32 v133, v128, v129
	v_add_f32_e32 v130, 0, v130
	v_add_f32_e32 v132, v132, v133
	v_add_f32_e32 v130, v132, v130
	v_mul_f32_e32 v132, v127, v127
	v_mul_f32_e32 v133, v129, v129
	v_fmac_f32_e32 v132, v126, v126
	v_fmac_f32_e32 v133, v128, v128
	v_add_f32_e32 v132, v132, v133
	v_add_f32_e32 v131, v131, v132
	v_add_f32_e32 v132, v42, v43
	v_add_f32_e32 v133, v44, v45
	v_add_f32_e32 v132, v132, v133
	v_add_f32_e32 v130, v132, v130
	v_mul_f32_e32 v132, v43, v43
	v_mul_f32_e32 v133, v45, v45
	v_fmac_f32_e32 v132, v42, v42
	v_fmac_f32_e32 v133, v44, v44
	v_add_f32_e32 v132, v132, v133
	v_add_f32_e32 v131, v132, v131
	v_add_f32_e32 v132, v46, v47
	v_add_f32_e32 v133, v48, v49
	v_add_f32_e32 v132, v132, v133
	v_add_f32_e32 v130, v132, v130
	v_mul_f32_e32 v132, v47, v47
	v_mul_f32_e32 v133, v49, v49
	v_fmac_f32_e32 v132, v46, v46
	v_fmac_f32_e32 v133, v48, v48
	v_add_f32_e32 v132, v132, v133
	v_add_f32_e32 v132, v132, v131
	ds_swizzle_b32 v131, v130 offset:swizzle(SWAP,16)
	ds_swizzle_b32 v133, v132 offset:swizzle(SWAP,16)
	s_waitcnt lgkmcnt(1)
	v_add_f32_e32 v131, v130, v131
	s_waitcnt lgkmcnt(0)
	v_add_f32_e32 v130, v132, v133
	v_mov_b32_e32 v133, v131
	v_mov_b32_e32 v132, v130
	s_nop 0
	v_permlane32_swap_b32_e32 v131, v133
	v_permlane32_swap_b32_e32 v130, v132
	s_and_saveexec_b64 s[2:3], vcc
	s_cbranch_execz .LBB0_693
	v_add_f32_e32 v130, v130, v132
	v_add_f32_e32 v131, v131, v133
	s_lshl_b32 s8, s27, 11
	v_mul_f32_e32 v132, 0x3c800000, v131
	v_fma_f32 v130, -v131, v132, v130
	s_add_i32 s8, s1, s8
	v_max_f32_e32 v133, 0, v130
	v_lshl_add_u32 v130, v0, 5, s8
	ds_write_b64 v130, v[132:133] offset:4608
.LBB0_693:
	s_or_b64 exec, exec, s[2:3]
	v_add_f32_e32 v130, v98, v99
	v_add_f32_e32 v131, v100, v101
	v_add_f32_e32 v130, v130, v131
	v_mul_f32_e32 v131, v99, v99
	v_mul_f32_e32 v132, v101, v101
	v_fmac_f32_e32 v131, v98, v98
	v_fmac_f32_e32 v132, v100, v100
	v_add_f32_e32 v131, v131, v132
	v_add_f32_e32 v132, v110, v111
	v_add_f32_e32 v133, v112, v113
	v_add_f32_e32 v130, 0, v130
	v_add_f32_e32 v132, v132, v133
	v_add_f32_e32 v130, v132, v130
	v_mul_f32_e32 v132, v111, v111
	v_mul_f32_e32 v133, v113, v113
	v_fmac_f32_e32 v132, v110, v110
	v_fmac_f32_e32 v133, v112, v112
	v_add_f32_e32 v132, v132, v133
	v_add_f32_e32 v131, v131, v132
	v_add_f32_e32 v132, v50, v51
	v_add_f32_e32 v133, v52, v53
	v_add_f32_e32 v132, v132, v133
	v_add_f32_e32 v130, v132, v130
	v_mul_f32_e32 v132, v51, v51
	v_mul_f32_e32 v133, v53, v53
	v_fmac_f32_e32 v132, v50, v50
	v_fmac_f32_e32 v133, v52, v52
	v_add_f32_e32 v132, v132, v133
	v_add_f32_e32 v131, v132, v131
	v_add_f32_e32 v132, v54, v55
	v_add_f32_e32 v133, v56, v57
	v_add_f32_e32 v132, v132, v133
	v_add_f32_e32 v130, v132, v130
	v_mul_f32_e32 v132, v55, v55
	v_mul_f32_e32 v133, v57, v57
	v_fmac_f32_e32 v132, v54, v54
	v_fmac_f32_e32 v133, v56, v56
	v_add_f32_e32 v132, v132, v133
	v_add_f32_e32 v132, v132, v131
	ds_swizzle_b32 v131, v130 offset:swizzle(SWAP,16)
	ds_swizzle_b32 v133, v132 offset:swizzle(SWAP,16)
	s_waitcnt lgkmcnt(1)
	v_add_f32_e32 v131, v130, v131
	s_waitcnt lgkmcnt(0)
	v_add_f32_e32 v130, v132, v133
	v_mov_b32_e32 v133, v131
	v_mov_b32_e32 v132, v130
	s_nop 0
	v_permlane32_swap_b32_e32 v131, v133
	v_permlane32_swap_b32_e32 v130, v132
	s_and_saveexec_b64 s[2:3], vcc
	s_cbranch_execz .LBB0_695
	v_add_f32_e32 v130, v130, v132
	v_add_f32_e32 v131, v131, v133
	s_lshl_b32 s8, s27, 11
	v_mul_f32_e32 v132, 0x3c800000, v131
	v_fma_f32 v130, -v131, v132, v130
	s_add_i32 s8, s1, s8
	v_max_f32_e32 v133, 0, v130
	v_lshl_add_u32 v130, v0, 5, s8
	ds_write_b64 v130, v[132:133] offset:5120
.LBB0_695:
	s_or_b64 exec, exec, s[2:3]
	v_add_f32_e32 v130, v82, v83
	v_add_f32_e32 v131, v84, v85
	v_add_f32_e32 v130, v130, v131
	v_mul_f32_e32 v131, v83, v83
	v_mul_f32_e32 v132, v85, v85
	v_fmac_f32_e32 v131, v82, v82
	v_fmac_f32_e32 v132, v84, v84
	v_add_f32_e32 v131, v131, v132
	v_add_f32_e32 v132, v86, v87
	v_add_f32_e32 v133, v88, v89
	v_add_f32_e32 v130, 0, v130
	v_add_f32_e32 v132, v132, v133
	v_add_f32_e32 v130, v132, v130
	v_mul_f32_e32 v132, v87, v87
	v_mul_f32_e32 v133, v89, v89
	v_fmac_f32_e32 v132, v86, v86
	v_fmac_f32_e32 v133, v88, v88
	v_add_f32_e32 v132, v132, v133
	v_add_f32_e32 v131, v131, v132
	v_add_f32_e32 v132, v66, v67
	v_add_f32_e32 v133, v68, v69
	v_add_f32_e32 v132, v132, v133
	v_add_f32_e32 v130, v132, v130
	v_mul_f32_e32 v132, v67, v67
	v_mul_f32_e32 v133, v69, v69
	v_fmac_f32_e32 v132, v66, v66
	v_fmac_f32_e32 v133, v68, v68
	v_add_f32_e32 v132, v132, v133
	v_add_f32_e32 v131, v132, v131
	v_add_f32_e32 v132, v70, v71
	v_add_f32_e32 v133, v72, v73
	v_add_f32_e32 v132, v132, v133
	v_add_f32_e32 v130, v132, v130
	v_mul_f32_e32 v132, v71, v71
	v_mul_f32_e32 v133, v73, v73
	v_fmac_f32_e32 v132, v70, v70
	v_fmac_f32_e32 v133, v72, v72
	v_add_f32_e32 v132, v132, v133
	v_add_f32_e32 v132, v132, v131
	ds_swizzle_b32 v131, v130 offset:swizzle(SWAP,16)
	ds_swizzle_b32 v133, v132 offset:swizzle(SWAP,16)
	s_waitcnt lgkmcnt(1)
	v_add_f32_e32 v131, v130, v131
	s_waitcnt lgkmcnt(0)
	v_add_f32_e32 v130, v132, v133
	v_mov_b32_e32 v133, v131
	v_mov_b32_e32 v132, v130
	s_nop 0
	v_permlane32_swap_b32_e32 v131, v133
	v_permlane32_swap_b32_e32 v130, v132
	s_and_saveexec_b64 s[2:3], vcc
	s_cbranch_execz .LBB0_697
	v_add_f32_e32 v130, v130, v132
	v_add_f32_e32 v131, v131, v133
	s_lshl_b32 s8, s27, 11
	v_mul_f32_e32 v132, 0x3c800000, v131
	v_fma_f32 v130, -v131, v132, v130
	s_add_i32 s1, s1, s8
	v_max_f32_e32 v133, 0, v130
	v_lshl_add_u32 v0, v0, 5, s1
	ds_write_b64 v0, v[132:133] offset:5632
.LBB0_697:
	s_or_b64 exec, exec, s[2:3]
	v_or_b32_e32 v0, s21, v211
	v_cmp_eq_u32_e32 vcc, 0, v0
	s_and_saveexec_b64 s[2:3], vcc
	ds_write_b32 v1, v1 offset:10240
	s_or_b64 exec, exec, s[2:3]
	s_waitcnt lgkmcnt(0)
	s_barrier
	v_cmp_gt_i32_e32 vcc, 32, v211
	s_and_saveexec_b64 s[2:3], vcc
	s_cbranch_execz .LBB0_710
	s_lshl_b32 s1, s21, 5
	v_and_or_b32 v130, v211, 31, s1
	v_lshl_add_u32 v0, v130, 5, 0
	ds_read_b128 v[132:135], v0
	ds_read_b128 v[136:139], v0 offset:16
	s_lshl_b32 s8, s56, 2
	s_ashr_i32 s21, s20, 31
	s_add_i32 s8, s8, 4
	s_waitcnt lgkmcnt(1)
	v_add_f32_e32 v131, v132, v134
	s_waitcnt lgkmcnt(0)
	v_add_f32_e32 v131, v131, v136
	v_add_f32_e32 v131, v131, v138
	v_fmamk_f32 v132, v131, 0xbe800000, v132
	v_fmac_f32_e32 v134, 0xbe800000, v131
	v_fmamk_f32 v136, v131, 0xbe800000, v136
	v_fmac_f32_e32 v138, 0xbe800000, v131
	v_mul_f32_e32 v143, v132, v132
	v_mul_f32_e32 v145, v134, v134
	v_mul_f32_e32 v147, v136, v136
	v_mul_f32_e32 v149, v138, v138
	v_mov_b32_e32 v142, v133
	v_mov_b32_e32 v144, v135
	v_mov_b32_e32 v146, v137
	v_mov_b32_e32 v148, v139
	s_lshl_b64 s[10:11], s[20:21], 14
	v_add_f32_e32 v132, v142, v144
	v_add_f32_e32 v133, v143, v145
	v_add_f32_e32 v134, v146, v148
	v_add_f32_e32 v135, v147, v149
	s_add_u32 s10, s14, s10
	v_mul_f32_e32 v140, 0x3e800000, v131
	v_add_f32_e32 v132, v132, v134
	v_add_f32_e32 v133, v133, v135
	s_addc_u32 s11, s15, s11
	v_ashrrev_i32_e32 v131, 31, v130
	v_fmac_f32_e32 v132, 0x42800000, v133
	v_lshl_add_u64 v[134:135], v[130:131], 3, s[10:11]
	s_mov_b64 s[10:11], 0x80000
	v_lshl_add_u64 v[136:137], v[134:135], 0, s[10:11]
	s_ashr_i32 s1, s0, 31
	v_and_b32_e32 v131, 0xffffffe0, v132
	v_lshl_add_u64 v[138:139], s[0:1], 3, v[136:137]
	v_or_b32_e32 v141, s8, v131
	s_mov_b64 s[0:1], 0x81000
	global_store_dwordx2 v[138:139], v[140:141], off sc1
	v_lshl_add_u64 v[140:141], v[134:135], 0, s[0:1]
	s_mov_b64 s[0:1], 0x81800
	s_memrealtime s[22:23]
	v_lshl_add_u64 v[142:143], v[134:135], 0, s[0:1]
	s_mov_b64 s[0:1], 0x82000
	v_lshl_add_u64 v[146:147], v[134:135], 0, s[0:1]
	s_mov_b64 s[0:1], 0x82800
	v_lshl_add_u64 v[148:149], v[134:135], 0, s[0:1]
	s_mov_b64 s[0:1], 0x83000
	v_lshl_add_u64 v[150:151], v[134:135], 0, s[0:1]
	s_mov_b64 s[0:1], 0x83800
	v_lshl_add_u64 v[152:153], v[134:135], 0, s[0:1]
	s_mov_b64 s[20:21], 0
	s_branch .LBB0_703

.LBB0_1230:
	v_add_co_u32_e32 v18, vcc, 0xfff49000, v8
	s_add_i32 s8, s8, 16
	s_nop 0
	v_addc_co_u32_e32 v19, vcc, -1, v9, vcc
	v_add_co_u32_e32 v22, vcc, 0xfff55000, v8
	global_load_dwordx4 v[18:21], v[18:19], off offset:-3072
	s_nop 0
	v_addc_co_u32_e32 v23, vcc, -1, v9, vcc
	global_load_dwordx4 v[26:29], v[22:23], off offset:-2048
	v_add_co_u32_e32 v22, vcc, 0xfff61000, v8
	s_mov_b64 s[12:13], 0xc4000
	s_nop 0
	v_addc_co_u32_e32 v23, vcc, -1, v9, vcc
	global_load_dwordx4 v[30:33], v[22:23], off offset:-1024
	v_add_co_u32_e32 v22, vcc, 0xfff6d000, v8
	s_cmp_lt_u32 s8, 48
	s_nop 0
	v_addc_co_u32_e32 v23, vcc, -1, v9, vcc
	global_load_dwordx4 v[34:37], v[22:23], off
	v_add_co_u32_e32 v22, vcc, 0xfff7a000, v8
	s_nop 1
	v_addc_co_u32_e32 v23, vcc, -1, v9, vcc
	global_load_dwordx4 v[38:41], v[22:23], off offset:-3072
	v_add_co_u32_e32 v22, vcc, 0xfff86000, v8
	s_nop 1
	v_addc_co_u32_e32 v23, vcc, -1, v9, vcc
	global_load_dwordx4 v[42:45], v[22:23], off offset:-2048
	v_add_co_u32_e32 v22, vcc, 0xfff92000, v8
	s_nop 1
	v_addc_co_u32_e32 v23, vcc, -1, v9, vcc
	global_load_dwordx4 v[46:49], v[22:23], off offset:-1024
	v_add_co_u32_e32 v22, vcc, 0xfff9e000, v8
	s_nop 1
	v_addc_co_u32_e32 v23, vcc, -1, v9, vcc
	global_load_dwordx4 v[50:53], v[22:23], off
	v_add_co_u32_e32 v22, vcc, 0xfffab000, v8
	s_nop 1
	v_addc_co_u32_e32 v23, vcc, -1, v9, vcc
	global_load_dwordx4 v[54:57], v[22:23], off offset:-3072
	v_add_co_u32_e32 v22, vcc, 0xfffb7000, v8
	s_nop 1
	v_addc_co_u32_e32 v23, vcc, -1, v9, vcc
	global_load_dwordx4 v[58:61], v[22:23], off offset:-2048
	v_add_co_u32_e32 v22, vcc, 0xfffc3000, v8
	s_nop 1
	v_addc_co_u32_e32 v23, vcc, -1, v9, vcc
	global_load_dwordx4 v[62:65], v[22:23], off offset:-1024
	v_add_co_u32_e32 v22, vcc, 0xfffcf000, v8
	s_nop 1
	v_addc_co_u32_e32 v23, vcc, -1, v9, vcc
	global_load_dwordx4 v[66:69], v[22:23], off
	v_add_co_u32_e32 v22, vcc, 0xfffdc000, v8
	s_nop 1
	v_addc_co_u32_e32 v23, vcc, -1, v9, vcc
	global_load_dwordx4 v[70:73], v[22:23], off offset:-3072
	v_add_co_u32_e32 v22, vcc, 0xfffe8000, v8
	s_nop 1
	v_addc_co_u32_e32 v23, vcc, -1, v9, vcc
	global_load_dwordx4 v[74:77], v[22:23], off offset:-2048
	v_add_co_u32_e32 v22, vcc, 0xffff4000, v8
	s_nop 1
	v_addc_co_u32_e32 v23, vcc, -1, v9, vcc
	global_load_dwordx4 v[78:81], v[22:23], off offset:-1024
	global_load_dwordx4 v[82:85], v[8:9], off
	s_waitcnt vmcnt(15)
	v_lshlrev_b32_e32 v22, 16, v18
	v_and_b32_e32 v23, 0xffff0000, v18
	v_lshlrev_b32_e32 v18, 16, v19
	v_and_b32_e32 v19, 0xffff0000, v19
	v_add_f32_e32 v16, v16, v18
	v_add_f32_e32 v17, v17, v19
	s_waitcnt vmcnt(14)
	v_lshlrev_b32_e32 v18, 16, v27
	v_and_b32_e32 v19, 0xffff0000, v27
	v_add_f32_e32 v16, v16, v18
	v_add_f32_e32 v17, v17, v19
	s_waitcnt vmcnt(13)
	v_lshlrev_b32_e32 v18, 16, v31
	v_and_b32_e32 v19, 0xffff0000, v31
	v_add_f32_e32 v16, v16, v18
	v_add_f32_e32 v17, v17, v19
	v_add_f32_e32 v14, v14, v22
	v_add_f32_e32 v15, v15, v23
	v_lshlrev_b32_e32 v22, 16, v26
	s_waitcnt vmcnt(12)
	v_lshlrev_b32_e32 v18, 16, v35
	v_and_b32_e32 v19, 0xffff0000, v35
	v_add_f32_e32 v16, v16, v18
	v_add_f32_e32 v17, v17, v19
	v_and_b32_e32 v23, 0xffff0000, v26
	v_add_f32_e32 v14, v14, v22
	v_add_f32_e32 v15, v15, v23
	v_lshlrev_b32_e32 v22, 16, v30
	s_waitcnt vmcnt(11)
	v_lshlrev_b32_e32 v18, 16, v39
	v_and_b32_e32 v19, 0xffff0000, v39
	v_add_f32_e32 v16, v16, v18
	v_add_f32_e32 v17, v17, v19
	v_lshlrev_b32_e32 v18, 16, v20
	v_and_b32_e32 v19, 0xffff0000, v20
	v_add_f32_e32 v12, v12, v18
	v_add_f32_e32 v13, v13, v19
	v_lshlrev_b32_e32 v18, 16, v28
	v_and_b32_e32 v19, 0xffff0000, v28
	v_add_f32_e32 v12, v12, v18
	v_add_f32_e32 v13, v13, v19
	v_lshlrev_b32_e32 v18, 16, v32
	v_and_b32_e32 v19, 0xffff0000, v32
	v_add_f32_e32 v12, v12, v18
	v_add_f32_e32 v13, v13, v19
	v_lshlrev_b32_e32 v18, 16, v36
	v_and_b32_e32 v19, 0xffff0000, v36
	v_add_f32_e32 v12, v12, v18
	v_add_f32_e32 v13, v13, v19
	v_lshlrev_b32_e32 v18, 16, v40
	v_and_b32_e32 v19, 0xffff0000, v40
	v_add_f32_e32 v12, v12, v18
	v_add_f32_e32 v13, v13, v19
	v_lshlrev_b32_e32 v18, 16, v21
	v_and_b32_e32 v19, 0xffff0000, v21
	v_add_f32_e32 v10, v10, v18
	v_add_f32_e32 v11, v11, v19
	v_lshlrev_b32_e32 v18, 16, v29
	v_and_b32_e32 v19, 0xffff0000, v29
	v_and_b32_e32 v23, 0xffff0000, v30
	v_add_f32_e32 v10, v10, v18
	v_add_f32_e32 v11, v11, v19
	v_lshlrev_b32_e32 v18, 16, v33
	v_and_b32_e32 v19, 0xffff0000, v33
	v_add_f32_e32 v14, v14, v22
	v_add_f32_e32 v15, v15, v23
	v_lshlrev_b32_e32 v22, 16, v34
	v_and_b32_e32 v23, 0xffff0000, v34
	v_add_f32_e32 v10, v10, v18
	v_add_f32_e32 v11, v11, v19
	v_lshlrev_b32_e32 v18, 16, v37
	v_and_b32_e32 v19, 0xffff0000, v37
	v_add_f32_e32 v14, v14, v22
	v_add_f32_e32 v15, v15, v23
	v_lshlrev_b32_e32 v22, 16, v38
	v_and_b32_e32 v23, 0xffff0000, v38
	v_add_f32_e32 v10, v10, v18
	v_add_f32_e32 v11, v11, v19
	v_lshlrev_b32_e32 v18, 16, v41
	v_and_b32_e32 v19, 0xffff0000, v41
	v_add_f32_e32 v14, v14, v22
	v_add_f32_e32 v15, v15, v23
	v_add_f32_e32 v10, v10, v18
	v_add_f32_e32 v11, v11, v19
	s_waitcnt vmcnt(10)
	v_lshlrev_b32_e32 v18, 16, v42
	v_and_b32_e32 v19, 0xffff0000, v42
	s_waitcnt vmcnt(9)
	v_lshlrev_b32_e32 v28, 16, v46
	v_and_b32_e32 v29, 0xffff0000, v46
	v_add_f32_e32 v14, v14, v18
	v_add_f32_e32 v15, v15, v19
	s_waitcnt vmcnt(8)
	v_lshlrev_b32_e32 v36, 16, v50
	v_and_b32_e32 v37, 0xffff0000, v50
	v_add_f32_e32 v14, v14, v28
	v_add_f32_e32 v15, v15, v29
	s_waitcnt vmcnt(7)
	v_lshlrev_b32_e32 v18, 16, v54
	v_add_f32_e32 v14, v14, v36
	v_add_f32_e32 v15, v15, v37
	v_and_b32_e32 v19, 0xffff0000, v54
	v_add_f32_e32 v14, v14, v18
	v_add_f32_e32 v15, v15, v19
	s_waitcnt vmcnt(6)
	v_lshlrev_b32_e32 v18, 16, v58
	v_and_b32_e32 v19, 0xffff0000, v58
	v_add_f32_e32 v14, v14, v18
	v_add_f32_e32 v15, v15, v19
	s_waitcnt vmcnt(5)
	v_lshlrev_b32_e32 v18, 16, v62
	v_and_b32_e32 v19, 0xffff0000, v62
	v_add_f32_e32 v14, v14, v18
	v_add_f32_e32 v15, v15, v19
	s_waitcnt vmcnt(4)
	v_lshlrev_b32_e32 v18, 16, v66
	v_and_b32_e32 v19, 0xffff0000, v66
	v_add_f32_e32 v14, v14, v18
	v_add_f32_e32 v15, v15, v19
	s_waitcnt vmcnt(3)
	v_lshlrev_b32_e32 v18, 16, v70
	v_and_b32_e32 v19, 0xffff0000, v70
	v_lshlrev_b32_e32 v20, 16, v43
	v_and_b32_e32 v21, 0xffff0000, v43
	v_add_f32_e32 v14, v14, v18
	v_add_f32_e32 v15, v15, v19
	s_waitcnt vmcnt(2)
	v_lshlrev_b32_e32 v18, 16, v74
	v_and_b32_e32 v19, 0xffff0000, v74
	v_lshlrev_b32_e32 v30, 16, v47
	v_and_b32_e32 v31, 0xffff0000, v47
	v_add_f32_e32 v14, v14, v18
	v_add_f32_e32 v15, v15, v19
	s_waitcnt vmcnt(1)
	v_lshlrev_b32_e32 v18, 16, v78
	v_and_b32_e32 v19, 0xffff0000, v78
	v_add_f32_e32 v16, v16, v20
	v_add_f32_e32 v17, v17, v21
	v_lshlrev_b32_e32 v38, 16, v51
	v_and_b32_e32 v39, 0xffff0000, v51
	v_add_f32_e32 v14, v14, v18
	v_add_f32_e32 v15, v15, v19
	s_waitcnt vmcnt(0)
	v_lshlrev_b32_e32 v18, 16, v82
	v_and_b32_e32 v19, 0xffff0000, v82
	v_add_f32_e32 v16, v16, v30
	v_add_f32_e32 v17, v17, v31
	v_add_f32_e32 v14, v14, v18
	v_add_f32_e32 v15, v15, v19
	v_add_f32_e32 v16, v16, v38
	v_add_f32_e32 v17, v17, v39
	v_lshlrev_b32_e32 v18, 16, v55
	v_and_b32_e32 v19, 0xffff0000, v55
	v_add_f32_e32 v16, v16, v18
	v_add_f32_e32 v17, v17, v19
	v_lshlrev_b32_e32 v18, 16, v59
	v_and_b32_e32 v19, 0xffff0000, v59
	v_add_f32_e32 v16, v16, v18
	v_add_f32_e32 v17, v17, v19
	v_lshlrev_b32_e32 v18, 16, v63
	v_and_b32_e32 v19, 0xffff0000, v63
	v_add_f32_e32 v16, v16, v18
	v_add_f32_e32 v17, v17, v19
	v_lshlrev_b32_e32 v18, 16, v67
	v_and_b32_e32 v19, 0xffff0000, v67
	v_add_f32_e32 v16, v16, v18
	v_add_f32_e32 v17, v17, v19
	v_lshlrev_b32_e32 v18, 16, v71
	v_and_b32_e32 v19, 0xffff0000, v71
	v_lshlrev_b32_e32 v22, 16, v44
	v_and_b32_e32 v23, 0xffff0000, v44
	v_add_f32_e32 v16, v16, v18
	v_add_f32_e32 v17, v17, v19
	v_lshlrev_b32_e32 v18, 16, v75
	v_and_b32_e32 v19, 0xffff0000, v75
	v_lshlrev_b32_e32 v32, 16, v48
	v_and_b32_e32 v33, 0xffff0000, v48
	v_add_f32_e32 v16, v16, v18
	v_add_f32_e32 v17, v17, v19
	v_lshlrev_b32_e32 v18, 16, v79
	v_and_b32_e32 v19, 0xffff0000, v79
	v_add_f32_e32 v12, v12, v22
	v_add_f32_e32 v13, v13, v23
	v_lshlrev_b32_e32 v40, 16, v52
	v_and_b32_e32 v41, 0xffff0000, v52
	v_add_f32_e32 v16, v16, v18
	v_add_f32_e32 v17, v17, v19
	v_lshlrev_b32_e32 v18, 16, v83
	v_and_b32_e32 v19, 0xffff0000, v83
	v_add_f32_e32 v12, v12, v32
	v_add_f32_e32 v13, v13, v33
	v_add_f32_e32 v16, v16, v18
	v_add_f32_e32 v17, v17, v19
	v_add_f32_e32 v12, v12, v40
	v_add_f32_e32 v13, v13, v41
	v_lshlrev_b32_e32 v18, 16, v56
	v_and_b32_e32 v19, 0xffff0000, v56
	v_add_f32_e32 v12, v12, v18
	v_add_f32_e32 v13, v13, v19
	v_lshlrev_b32_e32 v18, 16, v60
	v_and_b32_e32 v19, 0xffff0000, v60
	v_add_f32_e32 v12, v12, v18
	v_add_f32_e32 v13, v13, v19
	v_lshlrev_b32_e32 v18, 16, v64
	v_and_b32_e32 v19, 0xffff0000, v64
	v_add_f32_e32 v12, v12, v18
	v_add_f32_e32 v13, v13, v19
	v_lshlrev_b32_e32 v18, 16, v68
	v_and_b32_e32 v19, 0xffff0000, v68
	v_add_f32_e32 v12, v12, v18
	v_add_f32_e32 v13, v13, v19
	v_lshlrev_b32_e32 v18, 16, v72
	v_and_b32_e32 v19, 0xffff0000, v72
	v_lshlrev_b32_e32 v26, 16, v45
	v_and_b32_e32 v27, 0xffff0000, v45
	v_add_f32_e32 v12, v12, v18
	v_add_f32_e32 v13, v13, v19
	v_lshlrev_b32_e32 v18, 16, v76
	v_and_b32_e32 v19, 0xffff0000, v76
	v_lshlrev_b32_e32 v34, 16, v49
	v_and_b32_e32 v35, 0xffff0000, v49
	v_add_f32_e32 v12, v12, v18
	v_add_f32_e32 v13, v13, v19
	v_lshlrev_b32_e32 v18, 16, v80
	v_and_b32_e32 v19, 0xffff0000, v80
	v_add_f32_e32 v10, v10, v26
	v_add_f32_e32 v11, v11, v27
	v_lshlrev_b32_e32 v42, 16, v53
	v_and_b32_e32 v43, 0xffff0000, v53
	v_add_f32_e32 v12, v12, v18
	v_add_f32_e32 v13, v13, v19
	v_lshlrev_b32_e32 v18, 16, v84
	v_and_b32_e32 v19, 0xffff0000, v84
	v_add_f32_e32 v10, v10, v34
	v_add_f32_e32 v11, v11, v35
	v_add_f32_e32 v12, v12, v18
	v_add_f32_e32 v13, v13, v19
	v_add_f32_e32 v10, v10, v42
	v_add_f32_e32 v11, v11, v43
	v_lshlrev_b32_e32 v18, 16, v57
	v_and_b32_e32 v19, 0xffff0000, v57
	v_add_f32_e32 v10, v10, v18
	v_add_f32_e32 v11, v11, v19
	v_lshlrev_b32_e32 v18, 16, v61
	v_and_b32_e32 v19, 0xffff0000, v61
	v_add_f32_e32 v10, v10, v18
	v_add_f32_e32 v11, v11, v19
	v_lshlrev_b32_e32 v18, 16, v65
	v_and_b32_e32 v19, 0xffff0000, v65
	v_add_f32_e32 v10, v10, v18
	v_add_f32_e32 v11, v11, v19
	v_lshlrev_b32_e32 v18, 16, v69
	v_and_b32_e32 v19, 0xffff0000, v69
	v_add_f32_e32 v10, v10, v18
	v_add_f32_e32 v11, v11, v19
	v_lshlrev_b32_e32 v18, 16, v73
	v_and_b32_e32 v19, 0xffff0000, v73
	v_add_f32_e32 v10, v10, v18
	v_add_f32_e32 v11, v11, v19
	v_lshlrev_b32_e32 v18, 16, v77
	v_and_b32_e32 v19, 0xffff0000, v77
	v_add_f32_e32 v10, v10, v18
	v_add_f32_e32 v11, v11, v19
	v_lshlrev_b32_e32 v18, 16, v81
	v_and_b32_e32 v19, 0xffff0000, v81
	v_add_f32_e32 v10, v10, v18
	v_add_f32_e32 v11, v11, v19
	v_lshlrev_b32_e32 v18, 16, v85
	v_and_b32_e32 v19, 0xffff0000, v85
	v_add_f32_e32 v10, v10, v18
	v_add_f32_e32 v11, v11, v19
	v_lshl_add_u64 v[8:9], v[8:9], 0, s[12:13]
	s_cbranch_scc1 .LBB0_1230
	ds_swizzle_b32 v8, v14 offset:swizzle(SWAP,16)
	ds_swizzle_b32 v9, v15 offset:swizzle(SWAP,16)
	ds_swizzle_b32 v18, v16 offset:swizzle(SWAP,16)
	ds_swizzle_b32 v19, v17 offset:swizzle(SWAP,16)
	ds_swizzle_b32 v20, v12 offset:swizzle(SWAP,16)
	ds_swizzle_b32 v21, v13 offset:swizzle(SWAP,16)
	ds_swizzle_b32 v22, v10 offset:swizzle(SWAP,16)
	ds_swizzle_b32 v23, v11 offset:swizzle(SWAP,16)
	s_waitcnt lgkmcnt(7)
	v_add_f32_e32 v8, v14, v8
	s_waitcnt lgkmcnt(6)
	v_add_f32_e32 v9, v15, v9
	s_waitcnt lgkmcnt(5)
	v_add_f32_e32 v16, v16, v18
	s_waitcnt lgkmcnt(4)
	v_add_f32_e32 v17, v17, v19
	s_waitcnt lgkmcnt(3)
	v_add_f32_e32 v12, v12, v20
	s_waitcnt lgkmcnt(2)
	v_add_f32_e32 v13, v13, v21
	s_waitcnt lgkmcnt(1)
	v_add_f32_e32 v10, v10, v22
	s_waitcnt lgkmcnt(0)
	v_add_f32_e32 v11, v11, v23
	v_mov_b32_e32 v14, v8
	v_mov_b32_e32 v15, v9
	v_mov_b32_e32 v18, v16
	v_mov_b32_e32 v19, v17
	v_mov_b32_e32 v20, v12
	v_mov_b32_e32 v21, v13
	v_mov_b32_e32 v22, v10
	v_mov_b32_e32 v23, v11
	v_permlane32_swap_b32_e32 v8, v14
	v_permlane32_swap_b32_e32 v9, v15
	v_permlane32_swap_b32_e32 v16, v18
	v_permlane32_swap_b32_e32 v17, v19
	v_permlane32_swap_b32_e32 v12, v20
	v_permlane32_swap_b32_e32 v13, v21
	v_permlane32_swap_b32_e32 v10, v22
	v_permlane32_swap_b32_e32 v11, v23
	s_and_saveexec_b64 s[8:9], s[2:3]
	s_cbranch_execz .LBB0_1233
	v_add_f32_e32 v8, v8, v14
	v_add_f32_e32 v9, v9, v15
	s_mov_b32 s12, 0x3b800000
	v_pk_mul_f32 v[14:15], v[8:9], s[12:13] op_sel_hi:[1,0]
	v_add_f32_e32 v8, v16, v18
	v_add_f32_e32 v9, v17, v19
	v_add_f32_e32 v10, v10, v22
	v_add_f32_e32 v11, v11, v23
	v_pk_mul_f32 v[16:17], v[8:9], s[12:13] op_sel_hi:[1,0]
	v_add_f32_e32 v8, v12, v20
	v_add_f32_e32 v9, v13, v21
	v_pk_mul_f32 v[10:11], v[10:11], s[12:13] op_sel_hi:[1,0]
	v_pk_mul_f32 v[8:9], v[8:9], s[12:13] op_sel_hi:[1,0]
	ds_write_b128 v24, v[14:17] offset:16384
	ds_write_b128 v24, v[8:11] offset:16400

.LBB0_1803:
	v_and_b32_e32 v231, 63, v130
	v_bfe_u32 v232, v130, 4, 2
	s_lshl_b32 s1, s29, 5
	s_lshl_b32 s0, s31, 8
	s_barrier
	s_or_b32 s1, s0, s1
	v_add_u32_e32 v230, s44, v0
	v_lshl_add_u32 v194, v232, 3, s1
	v_lshl_add_u32 v228, s18, 8, v230
	v_ashrrev_i32_e32 v195, 31, v194
	v_ashrrev_i32_e32 v229, 31, v228
	v_lshl_add_u64 v[142:143], v[194:195], 1, s[12:13]
	v_lshlrev_b64 v[130:131], 12, v[228:229]
	s_mov_b32 s2, 1.0
	s_mov_b32 s20, 0x3fd744fd
	v_lshl_add_u64 v[226:227], v[142:143], 0, v[130:131]
	global_load_dwordx4 v[190:193], v[226:227], off
	global_load_dwordx4 v[186:189], v[226:227], off offset:256
	v_add_u32_e32 v224, 16, v228
	v_ashrrev_i32_e32 v225, 31, v224
	v_lshlrev_b64 v[130:131], 12, v[224:225]
	v_lshl_add_u64 v[222:223], v[142:143], 0, v[130:131]
	global_load_dwordx4 v[182:185], v[222:223], off
	global_load_dwordx4 v[178:181], v[222:223], off offset:256
	v_add_u32_e32 v220, 32, v228
	v_ashrrev_i32_e32 v221, 31, v220
	v_lshlrev_b64 v[130:131], 12, v[220:221]
	v_lshl_add_u64 v[218:219], v[142:143], 0, v[130:131]
	global_load_dwordx4 v[174:177], v[218:219], off
	global_load_dwordx4 v[170:173], v[218:219], off offset:256
	v_add_u32_e32 v216, 48, v228
	v_ashrrev_i32_e32 v217, 31, v216
	v_lshlrev_b64 v[130:131], 12, v[216:217]
	v_lshl_add_u64 v[214:215], v[142:143], 0, v[130:131]
	global_load_dwordx4 v[166:169], v[214:215], off
	global_load_dwordx4 v[162:165], v[214:215], off offset:256
	v_add_u32_e32 v212, 0x80, v228
	v_ashrrev_i32_e32 v213, 31, v212
	v_lshlrev_b64 v[130:131], 12, v[212:213]
	v_lshl_add_u64 v[210:211], v[142:143], 0, v[130:131]
	global_load_dwordx4 v[158:161], v[210:211], off
	global_load_dwordx4 v[154:157], v[210:211], off offset:256
	v_add_u32_e32 v208, 0x90, v228
	v_ashrrev_i32_e32 v209, 31, v208
	v_lshlrev_b64 v[130:131], 12, v[208:209]
	v_lshl_add_u64 v[206:207], v[142:143], 0, v[130:131]
	global_load_dwordx4 v[146:149], v[206:207], off
	global_load_dwordx4 v[138:141], v[206:207], off offset:256
	v_add_u32_e32 v204, 0xa0, v228
	v_ashrrev_i32_e32 v205, 31, v204
	v_lshlrev_b64 v[130:131], 12, v[204:205]
	v_lshl_add_u64 v[200:201], v[142:143], 0, v[130:131]
	global_load_dwordx4 v[134:137], v[200:201], off
	global_load_dwordx4 v[130:133], v[200:201], off offset:256
	v_add_u32_e32 v196, 0xb0, v228
	v_ashrrev_i32_e32 v197, 31, v196
	v_lshlrev_b64 v[144:145], 12, v[196:197]
	v_lshl_add_u64 v[198:199], v[142:143], 0, v[144:145]
	global_load_dwordx4 v[150:153], v[198:199], off
	global_load_dwordx4 v[142:145], v[198:199], off offset:256
	s_lshl_b32 s1, s29, 3
	v_cmp_eq_u32_e32 vcc, 0, v232
	s_add_i32 s1, s1, 0
	s_waitcnt vmcnt(15)
	v_lshlrev_b32_e32 v238, 16, v192
	v_and_b32_e32 v239, 0xffff0000, v192
	v_lshlrev_b32_e32 v192, 16, v193
	v_and_b32_e32 v193, 0xffff0000, v193
	v_lshlrev_b32_e32 v240, 16, v190
	v_and_b32_e32 v241, 0xffff0000, v190
	v_lshlrev_b32_e32 v190, 16, v191
	v_and_b32_e32 v191, 0xffff0000, v191
	v_mul_f32_e32 v190, s20, v190
	v_mul_f32_e32 v191, s20, v191
	v_mul_f32_e32 v192, s20, v192
	v_mul_f32_e32 v193, s20, v193
	v_pk_fma_f32 v[124:125], v[124:125], s[2:3], v[190:191] op_sel_hi:[1,0,1]
	v_mul_f32_e32 v190, s20, v238
	v_mul_f32_e32 v191, s20, v239
	v_pk_fma_f32 v[128:129], v[128:129], s[2:3], v[192:193] op_sel_hi:[1,0,1]
	s_waitcnt vmcnt(14)
	v_lshlrev_b32_e32 v192, 16, v186
	v_and_b32_e32 v193, 0xffff0000, v186
	v_lshlrev_b32_e32 v186, 16, v187
	v_and_b32_e32 v187, 0xffff0000, v187
	v_pk_fma_f32 v[126:127], v[126:127], s[2:3], v[190:191] op_sel_hi:[1,0,1]
	v_lshlrev_b32_e32 v190, 16, v188
	v_and_b32_e32 v191, 0xffff0000, v188
	v_lshlrev_b32_e32 v188, 16, v189
	v_and_b32_e32 v189, 0xffff0000, v189
	v_mul_f32_e32 v186, s20, v186
	v_mul_f32_e32 v187, s20, v187
	v_pk_fma_f32 v[60:61], v[60:61], s[2:3], v[186:187] op_sel_hi:[1,0,1]
	v_mul_f32_e32 v186, s20, v190
	v_mul_f32_e32 v187, s20, v191
	v_mul_f32_e32 v188, s20, v188
	v_mul_f32_e32 v189, s20, v189
	v_pk_fma_f32 v[64:65], v[64:65], s[2:3], v[188:189] op_sel_hi:[1,0,1]
	v_pk_fma_f32 v[62:63], v[62:63], s[2:3], v[186:187] op_sel_hi:[1,0,1]
	s_waitcnt vmcnt(13)
	v_lshlrev_b32_e32 v186, 16, v184
	v_and_b32_e32 v187, 0xffff0000, v184
	v_lshlrev_b32_e32 v184, 16, v185
	v_and_b32_e32 v185, 0xffff0000, v185
	v_lshlrev_b32_e32 v188, 16, v182
	v_and_b32_e32 v189, 0xffff0000, v182
	v_lshlrev_b32_e32 v182, 16, v183
	v_and_b32_e32 v183, 0xffff0000, v183
	v_mul_f32_e32 v182, s20, v182
	v_mul_f32_e32 v183, s20, v183
	v_mul_f32_e32 v184, s20, v184
	v_mul_f32_e32 v185, s20, v185
	v_pk_fma_f32 v[116:117], v[116:117], s[2:3], v[182:183] op_sel_hi:[1,0,1]
	v_mul_f32_e32 v182, s20, v186
	v_mul_f32_e32 v183, s20, v187
	v_pk_fma_f32 v[120:121], v[120:121], s[2:3], v[184:185] op_sel_hi:[1,0,1]
	s_waitcnt vmcnt(12)
	v_lshlrev_b32_e32 v184, 16, v178
	v_and_b32_e32 v185, 0xffff0000, v178
	v_lshlrev_b32_e32 v178, 16, v179
	v_and_b32_e32 v179, 0xffff0000, v179
	v_pk_fma_f32 v[118:119], v[118:119], s[2:3], v[182:183] op_sel_hi:[1,0,1]
	v_lshlrev_b32_e32 v182, 16, v180
	v_and_b32_e32 v183, 0xffff0000, v180
	v_lshlrev_b32_e32 v180, 16, v181
	v_and_b32_e32 v181, 0xffff0000, v181
	v_mul_f32_e32 v178, s20, v178
	v_mul_f32_e32 v179, s20, v179
	v_pk_fma_f32 v[52:53], v[52:53], s[2:3], v[178:179] op_sel_hi:[1,0,1]
	v_mul_f32_e32 v178, s20, v182
	v_mul_f32_e32 v179, s20, v183
	v_mul_f32_e32 v180, s20, v180
	v_mul_f32_e32 v181, s20, v181
	v_pk_fma_f32 v[56:57], v[56:57], s[2:3], v[180:181] op_sel_hi:[1,0,1]
	v_pk_fma_f32 v[54:55], v[54:55], s[2:3], v[178:179] op_sel_hi:[1,0,1]
	s_waitcnt vmcnt(11)
	v_lshlrev_b32_e32 v178, 16, v176
	v_and_b32_e32 v179, 0xffff0000, v176
	v_lshlrev_b32_e32 v176, 16, v177
	v_and_b32_e32 v177, 0xffff0000, v177
	v_lshlrev_b32_e32 v180, 16, v174
	v_and_b32_e32 v181, 0xffff0000, v174
	v_lshlrev_b32_e32 v174, 16, v175
	v_and_b32_e32 v175, 0xffff0000, v175
	v_mul_f32_e32 v174, s20, v174
	v_mul_f32_e32 v175, s20, v175
	v_mul_f32_e32 v176, s20, v176
	v_mul_f32_e32 v177, s20, v177
	v_pk_fma_f32 v[112:113], v[112:113], s[2:3], v[174:175] op_sel_hi:[1,0,1]
	v_mul_f32_e32 v174, s20, v178
	v_mul_f32_e32 v175, s20, v179
	v_pk_fma_f32 v[108:109], v[108:109], s[2:3], v[176:177] op_sel_hi:[1,0,1]
	s_waitcnt vmcnt(10)
	v_lshlrev_b32_e32 v176, 16, v170
	v_and_b32_e32 v177, 0xffff0000, v170
	v_lshlrev_b32_e32 v170, 16, v171
	v_and_b32_e32 v171, 0xffff0000, v171
	v_pk_fma_f32 v[106:107], v[106:107], s[2:3], v[174:175] op_sel_hi:[1,0,1]
	v_lshlrev_b32_e32 v174, 16, v172
	v_and_b32_e32 v175, 0xffff0000, v172
	v_lshlrev_b32_e32 v172, 16, v173
	v_and_b32_e32 v173, 0xffff0000, v173
	v_mul_f32_e32 v170, s20, v170
	v_mul_f32_e32 v171, s20, v171
	v_pk_fma_f32 v[44:45], v[44:45], s[2:3], v[170:171] op_sel_hi:[1,0,1]
	v_mul_f32_e32 v170, s20, v174
	v_mul_f32_e32 v171, s20, v175
	v_mul_f32_e32 v172, s20, v172
	v_mul_f32_e32 v173, s20, v173
	v_pk_fma_f32 v[48:49], v[48:49], s[2:3], v[172:173] op_sel_hi:[1,0,1]
	v_pk_fma_f32 v[46:47], v[46:47], s[2:3], v[170:171] op_sel_hi:[1,0,1]
	s_waitcnt vmcnt(9)
	v_lshlrev_b32_e32 v170, 16, v168
	v_and_b32_e32 v171, 0xffff0000, v168
	v_lshlrev_b32_e32 v168, 16, v169
	v_and_b32_e32 v169, 0xffff0000, v169
	v_lshlrev_b32_e32 v172, 16, v166
	v_and_b32_e32 v173, 0xffff0000, v166
	v_lshlrev_b32_e32 v166, 16, v167
	v_and_b32_e32 v167, 0xffff0000, v167
	v_mul_f32_e32 v166, s20, v166
	v_mul_f32_e32 v167, s20, v167
	v_mul_f32_e32 v168, s20, v168
	v_mul_f32_e32 v169, s20, v169
	v_pk_fma_f32 v[100:101], v[100:101], s[2:3], v[166:167] op_sel_hi:[1,0,1]
	v_mul_f32_e32 v166, s20, v170
	v_mul_f32_e32 v167, s20, v171
	v_pk_fma_f32 v[104:105], v[104:105], s[2:3], v[168:169] op_sel_hi:[1,0,1]
	s_waitcnt vmcnt(8)
	v_lshlrev_b32_e32 v168, 16, v162
	v_and_b32_e32 v169, 0xffff0000, v162
	v_lshlrev_b32_e32 v162, 16, v163
	v_and_b32_e32 v163, 0xffff0000, v163
	v_pk_fma_f32 v[102:103], v[102:103], s[2:3], v[166:167] op_sel_hi:[1,0,1]
	v_lshlrev_b32_e32 v166, 16, v164
	v_and_b32_e32 v167, 0xffff0000, v164
	v_lshlrev_b32_e32 v164, 16, v165
	v_and_b32_e32 v165, 0xffff0000, v165
	v_mul_f32_e32 v162, s20, v162
	v_mul_f32_e32 v163, s20, v163
	v_pk_fma_f32 v[36:37], v[36:37], s[2:3], v[162:163] op_sel_hi:[1,0,1]
	v_mul_f32_e32 v162, s20, v166
	v_mul_f32_e32 v163, s20, v167
	v_mul_f32_e32 v164, s20, v164
	v_mul_f32_e32 v165, s20, v165
	v_pk_fma_f32 v[40:41], v[40:41], s[2:3], v[164:165] op_sel_hi:[1,0,1]
	v_pk_fma_f32 v[38:39], v[38:39], s[2:3], v[162:163] op_sel_hi:[1,0,1]
	s_waitcnt vmcnt(7)
	v_lshlrev_b32_e32 v162, 16, v160
	v_and_b32_e32 v163, 0xffff0000, v160
	v_lshlrev_b32_e32 v160, 16, v161
	v_and_b32_e32 v161, 0xffff0000, v161
	v_lshlrev_b32_e32 v164, 16, v158
	v_and_b32_e32 v165, 0xffff0000, v158
	v_lshlrev_b32_e32 v158, 16, v159
	v_and_b32_e32 v159, 0xffff0000, v159
	v_mul_f32_e32 v158, s20, v158
	v_mul_f32_e32 v159, s20, v159
	v_mul_f32_e32 v160, s20, v160
	v_mul_f32_e32 v161, s20, v161
	v_pk_fma_f32 v[92:93], v[92:93], s[2:3], v[158:159] op_sel_hi:[1,0,1]
	v_mul_f32_e32 v158, s20, v162
	v_mul_f32_e32 v159, s20, v163
	v_pk_fma_f32 v[96:97], v[96:97], s[2:3], v[160:161] op_sel_hi:[1,0,1]
	s_waitcnt vmcnt(6)
	v_lshlrev_b32_e32 v160, 16, v154
	v_and_b32_e32 v161, 0xffff0000, v154
	v_lshlrev_b32_e32 v154, 16, v155
	v_and_b32_e32 v155, 0xffff0000, v155
	v_pk_fma_f32 v[94:95], v[94:95], s[2:3], v[158:159] op_sel_hi:[1,0,1]
	v_lshlrev_b32_e32 v158, 16, v156
	v_and_b32_e32 v159, 0xffff0000, v156
	v_lshlrev_b32_e32 v156, 16, v157
	v_and_b32_e32 v157, 0xffff0000, v157
	v_mul_f32_e32 v154, s20, v154
	v_mul_f32_e32 v155, s20, v155
	v_pk_fma_f32 v[28:29], v[28:29], s[2:3], v[154:155] op_sel_hi:[1,0,1]
	v_mul_f32_e32 v154, s20, v158
	v_mul_f32_e32 v155, s20, v159
	v_mul_f32_e32 v156, s20, v156
	v_mul_f32_e32 v157, s20, v157
	v_pk_fma_f32 v[32:33], v[32:33], s[2:3], v[156:157] op_sel_hi:[1,0,1]
	v_pk_fma_f32 v[30:31], v[30:31], s[2:3], v[154:155] op_sel_hi:[1,0,1]
	s_waitcnt vmcnt(5)
	v_lshlrev_b32_e32 v154, 16, v148
	v_and_b32_e32 v155, 0xffff0000, v148
	v_lshlrev_b32_e32 v148, 16, v149
	v_and_b32_e32 v149, 0xffff0000, v149
	v_lshlrev_b32_e32 v156, 16, v146
	v_and_b32_e32 v157, 0xffff0000, v146
	v_lshlrev_b32_e32 v146, 16, v147
	v_and_b32_e32 v147, 0xffff0000, v147
	v_mul_f32_e32 v146, s20, v146
	v_mul_f32_e32 v147, s20, v147
	v_mul_f32_e32 v148, s20, v148
	v_mul_f32_e32 v149, s20, v149
	v_pk_fma_f32 v[84:85], v[84:85], s[2:3], v[146:147] op_sel_hi:[1,0,1]
	v_mul_f32_e32 v146, s20, v154
	v_mul_f32_e32 v147, s20, v155
	v_pk_fma_f32 v[88:89], v[88:89], s[2:3], v[148:149] op_sel_hi:[1,0,1]
	s_waitcnt vmcnt(4)
	v_lshlrev_b32_e32 v148, 16, v138
	v_and_b32_e32 v149, 0xffff0000, v138
	v_lshlrev_b32_e32 v138, 16, v139
	v_and_b32_e32 v139, 0xffff0000, v139
	v_pk_fma_f32 v[86:87], v[86:87], s[2:3], v[146:147] op_sel_hi:[1,0,1]
	v_lshlrev_b32_e32 v146, 16, v140
	v_and_b32_e32 v147, 0xffff0000, v140
	v_lshlrev_b32_e32 v140, 16, v141
	v_and_b32_e32 v141, 0xffff0000, v141
	v_mul_f32_e32 v138, s20, v138
	v_mul_f32_e32 v139, s20, v139
	v_pk_fma_f32 v[20:21], v[20:21], s[2:3], v[138:139] op_sel_hi:[1,0,1]
	v_mul_f32_e32 v138, s20, v146
	v_mul_f32_e32 v139, s20, v147
	v_mul_f32_e32 v140, s20, v140
	v_mul_f32_e32 v141, s20, v141
	v_pk_fma_f32 v[24:25], v[24:25], s[2:3], v[140:141] op_sel_hi:[1,0,1]
	v_pk_fma_f32 v[22:23], v[22:23], s[2:3], v[138:139] op_sel_hi:[1,0,1]
	s_waitcnt vmcnt(3)
	v_lshlrev_b32_e32 v138, 16, v136
	v_and_b32_e32 v139, 0xffff0000, v136
	v_lshlrev_b32_e32 v136, 16, v137
	v_and_b32_e32 v137, 0xffff0000, v137
	v_lshlrev_b32_e32 v140, 16, v134
	v_and_b32_e32 v141, 0xffff0000, v134
	v_lshlrev_b32_e32 v134, 16, v135
	v_and_b32_e32 v135, 0xffff0000, v135
	v_mul_f32_e32 v134, s20, v134
	v_mul_f32_e32 v135, s20, v135
	v_mul_f32_e32 v136, s20, v136
	v_mul_f32_e32 v137, s20, v137
	v_pk_fma_f32 v[76:77], v[76:77], s[2:3], v[134:135] op_sel_hi:[1,0,1]
	v_mul_f32_e32 v134, s20, v138
	v_mul_f32_e32 v135, s20, v139
	v_pk_fma_f32 v[80:81], v[80:81], s[2:3], v[136:137] op_sel_hi:[1,0,1]
	s_waitcnt vmcnt(2)
	v_lshlrev_b32_e32 v136, 16, v130
	v_and_b32_e32 v137, 0xffff0000, v130
	v_lshlrev_b32_e32 v130, 16, v131
	v_and_b32_e32 v131, 0xffff0000, v131
	v_pk_fma_f32 v[78:79], v[78:79], s[2:3], v[134:135] op_sel_hi:[1,0,1]
	v_lshlrev_b32_e32 v134, 16, v132
	v_and_b32_e32 v135, 0xffff0000, v132
	v_mul_f32_e32 v130, s20, v130
	v_mul_f32_e32 v131, s20, v131
	v_lshlrev_b32_e32 v132, 16, v133
	v_and_b32_e32 v133, 0xffff0000, v133
	v_pk_fma_f32 v[12:13], v[12:13], s[2:3], v[130:131] op_sel_hi:[1,0,1]
	v_mul_f32_e32 v130, s20, v134
	v_mul_f32_e32 v131, s20, v135
	v_mul_f32_e32 v132, s20, v132
	v_mul_f32_e32 v133, s20, v133
	v_pk_fma_f32 v[14:15], v[14:15], s[2:3], v[130:131] op_sel_hi:[1,0,1]
	s_waitcnt vmcnt(1)
	v_lshlrev_b32_e32 v130, 16, v152
	v_and_b32_e32 v131, 0xffff0000, v152
	v_pk_fma_f32 v[16:17], v[16:17], s[2:3], v[132:133] op_sel_hi:[1,0,1]
	v_lshlrev_b32_e32 v132, 16, v153
	v_and_b32_e32 v133, 0xffff0000, v153
	v_mul_f32_e32 v130, s20, v130
	v_mul_f32_e32 v131, s20, v131
	v_mul_f32_e32 v240, s20, v240
	v_mul_f32_e32 v241, s20, v241
	v_mul_f32_e32 v192, s20, v192
	v_mul_f32_e32 v193, s20, v193
	v_mul_f32_e32 v132, s20, v132
	v_mul_f32_e32 v133, s20, v133
	v_pk_fma_f32 v[70:71], v[70:71], s[2:3], v[130:131] op_sel_hi:[1,0,1]
	s_waitcnt vmcnt(0)
	v_lshlrev_b32_e32 v130, 16, v144
	v_and_b32_e32 v131, 0xffff0000, v144
	v_pk_fma_f32 v[122:123], v[122:123], s[2:3], v[240:241] op_sel_hi:[1,0,1]
	v_pk_fma_f32 v[58:59], v[58:59], s[2:3], v[192:193] op_sel_hi:[1,0,1]
	v_pk_fma_f32 v[72:73], v[72:73], s[2:3], v[132:133] op_sel_hi:[1,0,1]
	v_lshlrev_b32_e32 v132, 16, v145
	v_and_b32_e32 v133, 0xffff0000, v145
	v_mul_f32_e32 v130, s20, v130
	v_mul_f32_e32 v131, s20, v131
	v_mul_f32_e32 v132, s20, v132
	v_mul_f32_e32 v133, s20, v133
	v_pk_fma_f32 v[6:7], v[6:7], s[2:3], v[130:131] op_sel_hi:[1,0,1]
	v_add_f32_e32 v130, v122, v123
	v_add_f32_e32 v131, v124, v125
	v_pk_fma_f32 v[8:9], v[8:9], s[2:3], v[132:133] op_sel_hi:[1,0,1]
	v_add_f32_e32 v130, v130, v131
	v_mul_f32_e32 v131, v123, v123
	v_mul_f32_e32 v132, v125, v125
	v_fmac_f32_e32 v131, v122, v122
	v_fmac_f32_e32 v132, v124, v124
	v_add_f32_e32 v131, v131, v132
	v_add_f32_e32 v132, v126, v127
	v_add_f32_e32 v133, v128, v129
	v_add_f32_e32 v130, 0, v130
	v_add_f32_e32 v132, v132, v133
	v_add_f32_e32 v130, v132, v130
	v_mul_f32_e32 v132, v127, v127
	v_mul_f32_e32 v133, v129, v129
	v_fmac_f32_e32 v132, v126, v126
	v_fmac_f32_e32 v133, v128, v128
	v_add_f32_e32 v132, v132, v133
	v_add_f32_e32 v131, v131, v132
	v_add_f32_e32 v132, v58, v59
	v_add_f32_e32 v133, v60, v61
	v_add_f32_e32 v132, v132, v133
	v_add_f32_e32 v130, v132, v130
	v_mul_f32_e32 v132, v59, v59
	v_mul_f32_e32 v133, v61, v61
	v_fmac_f32_e32 v132, v58, v58
	v_fmac_f32_e32 v133, v60, v60
	v_add_f32_e32 v132, v132, v133
	v_add_f32_e32 v131, v132, v131
	v_add_f32_e32 v132, v62, v63
	v_add_f32_e32 v133, v64, v65
	v_add_f32_e32 v132, v132, v133
	v_add_f32_e32 v130, v132, v130
	v_mul_f32_e32 v132, v63, v63
	v_mul_f32_e32 v133, v65, v65
	v_fmac_f32_e32 v132, v62, v62
	v_fmac_f32_e32 v133, v64, v64
	v_add_f32_e32 v132, v132, v133
	v_add_f32_e32 v132, v132, v131
	ds_swizzle_b32 v131, v130 offset:swizzle(SWAP,16)
	v_mul_f32_e32 v136, s20, v136
	v_mul_f32_e32 v137, s20, v137
	v_pk_fma_f32 v[10:11], v[10:11], s[2:3], v[136:137] op_sel_hi:[1,0,1]
	v_lshlrev_b32_e32 v134, 16, v150
	v_and_b32_e32 v135, 0xffff0000, v150
	v_lshlrev_b32_e32 v136, 16, v151
	v_and_b32_e32 v137, 0xffff0000, v151
	s_waitcnt lgkmcnt(0)
	v_add_f32_e32 v131, v130, v131
	ds_swizzle_b32 v130, v132 offset:swizzle(SWAP,16)
	v_mul_f32_e32 v134, s20, v134
	v_mul_f32_e32 v135, s20, v135
	v_mul_f32_e32 v136, s20, v136
	v_mul_f32_e32 v137, s20, v137
	v_pk_fma_f32 v[68:69], v[68:69], s[2:3], v[136:137] op_sel_hi:[1,0,1]
	v_pk_fma_f32 v[66:67], v[66:67], s[2:3], v[134:135] op_sel_hi:[1,0,1]
	v_lshlrev_b32_e32 v134, 16, v142
	v_and_b32_e32 v135, 0xffff0000, v142
	v_lshlrev_b32_e32 v136, 16, v143
	v_and_b32_e32 v137, 0xffff0000, v143
	v_mul_f32_e32 v188, s20, v188
	v_mul_f32_e32 v189, s20, v189
	v_mul_f32_e32 v184, s20, v184
	v_mul_f32_e32 v185, s20, v185
	v_mul_f32_e32 v180, s20, v180
	v_mul_f32_e32 v181, s20, v181
	v_mul_f32_e32 v176, s20, v176
	v_mul_f32_e32 v177, s20, v177
	v_mul_f32_e32 v172, s20, v172
	v_mul_f32_e32 v173, s20, v173
	v_mul_f32_e32 v168, s20, v168
	v_mul_f32_e32 v169, s20, v169
	v_mul_f32_e32 v164, s20, v164
	v_mul_f32_e32 v165, s20, v165
	v_mul_f32_e32 v160, s20, v160
	v_mul_f32_e32 v161, s20, v161
	v_mul_f32_e32 v156, s20, v156
	v_mul_f32_e32 v157, s20, v157
	v_mul_f32_e32 v148, s20, v148
	v_mul_f32_e32 v149, s20, v149
	v_mul_f32_e32 v140, s20, v140
	v_mul_f32_e32 v141, s20, v141
	v_mul_f32_e32 v134, s20, v134
	v_mul_f32_e32 v135, s20, v135
	v_mul_f32_e32 v136, s20, v136
	v_mul_f32_e32 v137, s20, v137
	v_pk_fma_f32 v[114:115], v[114:115], s[2:3], v[188:189] op_sel_hi:[1,0,1]
	v_pk_fma_f32 v[50:51], v[50:51], s[2:3], v[184:185] op_sel_hi:[1,0,1]
	v_pk_fma_f32 v[110:111], v[110:111], s[2:3], v[180:181] op_sel_hi:[1,0,1]
	v_pk_fma_f32 v[42:43], v[42:43], s[2:3], v[176:177] op_sel_hi:[1,0,1]
	v_pk_fma_f32 v[98:99], v[98:99], s[2:3], v[172:173] op_sel_hi:[1,0,1]
	v_pk_fma_f32 v[34:35], v[34:35], s[2:3], v[168:169] op_sel_hi:[1,0,1]
	v_pk_fma_f32 v[90:91], v[90:91], s[2:3], v[164:165] op_sel_hi:[1,0,1]
	v_pk_fma_f32 v[26:27], v[26:27], s[2:3], v[160:161] op_sel_hi:[1,0,1]
	v_pk_fma_f32 v[82:83], v[82:83], s[2:3], v[156:157] op_sel_hi:[1,0,1]
	v_pk_fma_f32 v[18:19], v[18:19], s[2:3], v[148:149] op_sel_hi:[1,0,1]
	v_pk_fma_f32 v[74:75], v[74:75], s[2:3], v[140:141] op_sel_hi:[1,0,1]
	v_pk_fma_f32 v[4:5], v[4:5], s[2:3], v[136:137] op_sel_hi:[1,0,1]
	v_pk_fma_f32 v[2:3], v[2:3], s[2:3], v[134:135] op_sel_hi:[1,0,1]
	s_nop 0
	s_waitcnt lgkmcnt(0)
	v_add_f32_e32 v130, v132, v130
	v_mov_b32_e32 v133, v131
	v_mov_b32_e32 v132, v130
	s_nop 0
	v_permlane32_swap_b32_e32 v131, v133
	v_permlane32_swap_b32_e32 v130, v132
	s_and_saveexec_b64 s[2:3], vcc
	s_mov_b64 s[52:53], 0x400
	s_cbranch_execz .LBB0_1805
	v_add_f32_e32 v130, v130, v132
	v_add_f32_e32 v131, v131, v133
	s_lshl_b32 s20, s28, 11
	v_mul_f32_e32 v132, 0x3c800000, v131
	v_fma_f32 v130, -v131, v132, v130
	s_add_i32 s20, s1, s20
	v_max_f32_e32 v133, 0, v130
	v_lshl_add_u32 v130, v0, 5, s20
	ds_write_b64 v130, v[132:133]
.LBB0_1805:
	s_or_b64 exec, exec, s[2:3]
	v_add_f32_e32 v130, v114, v115
	v_add_f32_e32 v131, v116, v117
	v_add_f32_e32 v130, v130, v131
	v_mul_f32_e32 v131, v115, v115
	v_mul_f32_e32 v132, v117, v117
	v_fmac_f32_e32 v131, v114, v114
	v_fmac_f32_e32 v132, v116, v116
	v_add_f32_e32 v131, v131, v132
	v_add_f32_e32 v132, v118, v119
	v_add_f32_e32 v133, v120, v121
	v_add_f32_e32 v130, 0, v130
	v_add_f32_e32 v132, v132, v133
	v_add_f32_e32 v130, v132, v130
	v_mul_f32_e32 v132, v119, v119
	v_mul_f32_e32 v133, v121, v121
	v_fmac_f32_e32 v132, v118, v118
	v_fmac_f32_e32 v133, v120, v120
	v_add_f32_e32 v132, v132, v133
	v_add_f32_e32 v131, v131, v132
	v_add_f32_e32 v132, v50, v51
	v_add_f32_e32 v133, v52, v53
	v_add_f32_e32 v132, v132, v133
	v_add_f32_e32 v130, v132, v130
	v_mul_f32_e32 v132, v51, v51
	v_mul_f32_e32 v133, v53, v53
	v_fmac_f32_e32 v132, v50, v50
	v_fmac_f32_e32 v133, v52, v52
	v_add_f32_e32 v132, v132, v133
	v_add_f32_e32 v131, v132, v131
	v_add_f32_e32 v132, v54, v55
	v_add_f32_e32 v133, v56, v57
	v_add_f32_e32 v132, v132, v133
	v_add_f32_e32 v130, v132, v130
	v_mul_f32_e32 v132, v55, v55
	v_mul_f32_e32 v133, v57, v57
	v_fmac_f32_e32 v132, v54, v54
	v_fmac_f32_e32 v133, v56, v56
	v_add_f32_e32 v132, v132, v133
	v_add_f32_e32 v132, v132, v131
	ds_swizzle_b32 v131, v130 offset:swizzle(SWAP,16)
	ds_swizzle_b32 v133, v132 offset:swizzle(SWAP,16)
	s_waitcnt lgkmcnt(1)
	v_add_f32_e32 v131, v130, v131
	s_waitcnt lgkmcnt(0)
	v_add_f32_e32 v130, v132, v133
	v_mov_b32_e32 v133, v131
	v_mov_b32_e32 v132, v130
	s_nop 0
	v_permlane32_swap_b32_e32 v131, v133
	v_permlane32_swap_b32_e32 v130, v132
	s_and_saveexec_b64 s[2:3], vcc
	s_cbranch_execz .LBB0_1807
	v_add_f32_e32 v130, v130, v132
	v_add_f32_e32 v131, v131, v133
	s_lshl_b32 s20, s28, 11
	v_mul_f32_e32 v132, 0x3c800000, v131
	v_fma_f32 v130, -v131, v132, v130
	s_add_i32 s20, s1, s20
	v_max_f32_e32 v133, 0, v130
	v_lshl_add_u32 v130, v0, 5, s20
	ds_write_b64 v130, v[132:133] offset:512
.LBB0_1807:
	s_or_b64 exec, exec, s[2:3]
	v_add_f32_e32 v130, v110, v111
	v_add_f32_e32 v131, v112, v113
	v_add_f32_e32 v130, v130, v131
	v_mul_f32_e32 v131, v111, v111
	v_mul_f32_e32 v132, v113, v113
	v_fmac_f32_e32 v131, v110, v110
	v_fmac_f32_e32 v132, v112, v112
	v_add_f32_e32 v131, v131, v132
	v_add_f32_e32 v132, v106, v107
	v_add_f32_e32 v133, v108, v109
	v_add_f32_e32 v130, 0, v130
	v_add_f32_e32 v132, v132, v133
	v_add_f32_e32 v130, v132, v130
	v_mul_f32_e32 v132, v107, v107
	v_mul_f32_e32 v133, v109, v109
	v_fmac_f32_e32 v132, v106, v106
	v_fmac_f32_e32 v133, v108, v108
	v_add_f32_e32 v132, v132, v133
	v_add_f32_e32 v131, v131, v132
	v_add_f32_e32 v132, v42, v43
	v_add_f32_e32 v133, v44, v45
	v_add_f32_e32 v132, v132, v133
	v_add_f32_e32 v130, v132, v130
	v_mul_f32_e32 v132, v43, v43
	v_mul_f32_e32 v133, v45, v45
	v_fmac_f32_e32 v132, v42, v42
	v_fmac_f32_e32 v133, v44, v44
	v_add_f32_e32 v132, v132, v133
	v_add_f32_e32 v131, v132, v131
	v_add_f32_e32 v132, v46, v47
	v_add_f32_e32 v133, v48, v49
	v_add_f32_e32 v132, v132, v133
	v_add_f32_e32 v130, v132, v130
	v_mul_f32_e32 v132, v47, v47
	v_mul_f32_e32 v133, v49, v49
	v_fmac_f32_e32 v132, v46, v46
	v_fmac_f32_e32 v133, v48, v48
	v_add_f32_e32 v132, v132, v133
	v_add_f32_e32 v132, v132, v131
	ds_swizzle_b32 v131, v130 offset:swizzle(SWAP,16)
	ds_swizzle_b32 v133, v132 offset:swizzle(SWAP,16)
	s_waitcnt lgkmcnt(1)
	v_add_f32_e32 v131, v130, v131
	s_waitcnt lgkmcnt(0)
	v_add_f32_e32 v130, v132, v133
	v_mov_b32_e32 v133, v131
	v_mov_b32_e32 v132, v130
	s_nop 0
	v_permlane32_swap_b32_e32 v131, v133
	v_permlane32_swap_b32_e32 v130, v132
	s_and_saveexec_b64 s[2:3], vcc
	s_cbranch_execz .LBB0_1809
	v_add_f32_e32 v130, v130, v132
	v_add_f32_e32 v131, v131, v133
	s_lshl_b32 s20, s28, 11
	v_mul_f32_e32 v132, 0x3c800000, v131
	v_fma_f32 v130, -v131, v132, v130
	s_add_i32 s20, s1, s20
	v_max_f32_e32 v133, 0, v130
	v_lshl_add_u32 v130, v0, 5, s20
	ds_write_b64 v130, v[132:133] offset:1024
.LBB0_1809:
	s_or_b64 exec, exec, s[2:3]
	v_add_f32_e32 v130, v98, v99
	v_add_f32_e32 v131, v100, v101
	v_add_f32_e32 v130, v130, v131
	v_mul_f32_e32 v131, v99, v99
	v_mul_f32_e32 v132, v101, v101
	v_fmac_f32_e32 v131, v98, v98
	v_fmac_f32_e32 v132, v100, v100
	v_add_f32_e32 v131, v131, v132
	v_add_f32_e32 v132, v102, v103
	v_add_f32_e32 v133, v104, v105
	v_add_f32_e32 v130, 0, v130
	v_add_f32_e32 v132, v132, v133
	v_add_f32_e32 v130, v132, v130
	v_mul_f32_e32 v132, v103, v103
	v_mul_f32_e32 v133, v105, v105
	v_fmac_f32_e32 v132, v102, v102
	v_fmac_f32_e32 v133, v104, v104
	v_add_f32_e32 v132, v132, v133
	v_add_f32_e32 v131, v131, v132
	v_add_f32_e32 v132, v34, v35
	v_add_f32_e32 v133, v36, v37
	v_add_f32_e32 v132, v132, v133
	v_add_f32_e32 v130, v132, v130
	v_mul_f32_e32 v132, v35, v35
	v_mul_f32_e32 v133, v37, v37
	v_fmac_f32_e32 v132, v34, v34
	v_fmac_f32_e32 v133, v36, v36
	v_add_f32_e32 v132, v132, v133
	v_add_f32_e32 v131, v132, v131
	v_add_f32_e32 v132, v38, v39
	v_add_f32_e32 v133, v40, v41
	v_add_f32_e32 v132, v132, v133
	v_add_f32_e32 v130, v132, v130
	v_mul_f32_e32 v132, v39, v39
	v_mul_f32_e32 v133, v41, v41
	v_fmac_f32_e32 v132, v38, v38
	v_fmac_f32_e32 v133, v40, v40
	v_add_f32_e32 v132, v132, v133
	v_add_f32_e32 v132, v132, v131
	ds_swizzle_b32 v131, v130 offset:swizzle(SWAP,16)
	ds_swizzle_b32 v133, v132 offset:swizzle(SWAP,16)
	s_waitcnt lgkmcnt(1)
	v_add_f32_e32 v131, v130, v131
	s_waitcnt lgkmcnt(0)
	v_add_f32_e32 v130, v132, v133
	v_mov_b32_e32 v133, v131
	v_mov_b32_e32 v132, v130
	s_nop 0
	v_permlane32_swap_b32_e32 v131, v133
	v_permlane32_swap_b32_e32 v130, v132
	s_and_saveexec_b64 s[2:3], vcc
	s_cbranch_execz .LBB0_1811
	v_add_f32_e32 v130, v130, v132
	v_add_f32_e32 v131, v131, v133
	s_lshl_b32 s20, s28, 11
	v_mul_f32_e32 v132, 0x3c800000, v131
	v_fma_f32 v130, -v131, v132, v130
	s_add_i32 s20, s1, s20
	v_max_f32_e32 v133, 0, v130
	v_lshl_add_u32 v130, v0, 5, s20
	ds_write_b64 v130, v[132:133] offset:1536
.LBB0_1811:
	s_or_b64 exec, exec, s[2:3]
	v_add_f32_e32 v130, v90, v91
	v_add_f32_e32 v131, v92, v93
	v_add_f32_e32 v130, v130, v131
	v_mul_f32_e32 v131, v91, v91
	v_mul_f32_e32 v132, v93, v93
	v_fmac_f32_e32 v131, v90, v90
	v_fmac_f32_e32 v132, v92, v92
	v_add_f32_e32 v131, v131, v132
	v_add_f32_e32 v132, v94, v95
	v_add_f32_e32 v133, v96, v97
	v_add_f32_e32 v130, 0, v130
	v_add_f32_e32 v132, v132, v133
	v_add_f32_e32 v130, v132, v130
	v_mul_f32_e32 v132, v95, v95
	v_mul_f32_e32 v133, v97, v97
	v_fmac_f32_e32 v132, v94, v94
	v_fmac_f32_e32 v133, v96, v96
	v_add_f32_e32 v132, v132, v133
	v_add_f32_e32 v131, v131, v132
	v_add_f32_e32 v132, v26, v27
	v_add_f32_e32 v133, v28, v29
	v_add_f32_e32 v132, v132, v133
	v_add_f32_e32 v130, v132, v130
	v_mul_f32_e32 v132, v27, v27
	v_mul_f32_e32 v133, v29, v29
	v_fmac_f32_e32 v132, v26, v26
	v_fmac_f32_e32 v133, v28, v28
	v_add_f32_e32 v132, v132, v133
	v_add_f32_e32 v131, v132, v131
	v_add_f32_e32 v132, v30, v31
	v_add_f32_e32 v133, v32, v33
	v_add_f32_e32 v132, v132, v133
	v_add_f32_e32 v130, v132, v130
	v_mul_f32_e32 v132, v31, v31
	v_mul_f32_e32 v133, v33, v33
	v_fmac_f32_e32 v132, v30, v30
	v_fmac_f32_e32 v133, v32, v32
	v_add_f32_e32 v132, v132, v133
	v_add_f32_e32 v132, v132, v131
	ds_swizzle_b32 v131, v130 offset:swizzle(SWAP,16)
	ds_swizzle_b32 v133, v132 offset:swizzle(SWAP,16)
	s_waitcnt lgkmcnt(1)
	v_add_f32_e32 v131, v130, v131
	s_waitcnt lgkmcnt(0)
	v_add_f32_e32 v130, v132, v133
	v_mov_b32_e32 v133, v131
	v_mov_b32_e32 v132, v130
	s_nop 0
	v_permlane32_swap_b32_e32 v131, v133
	v_permlane32_swap_b32_e32 v130, v132
	s_and_saveexec_b64 s[2:3], vcc
	s_cbranch_execz .LBB0_1813
	v_add_f32_e32 v130, v130, v132
	v_add_f32_e32 v131, v131, v133
	s_lshl_b32 s20, s28, 11
	v_mul_f32_e32 v132, 0x3c800000, v131
	v_fma_f32 v130, -v131, v132, v130
	s_add_i32 s20, s1, s20
	v_max_f32_e32 v133, 0, v130
	v_lshl_add_u32 v130, v0, 5, s20
	ds_write_b64 v130, v[132:133] offset:4096
.LBB0_1813:
	s_or_b64 exec, exec, s[2:3]
	v_add_f32_e32 v130, v82, v83
	v_add_f32_e32 v131, v84, v85
	v_add_f32_e32 v130, v130, v131
	v_mul_f32_e32 v131, v83, v83
	v_mul_f32_e32 v132, v85, v85
	v_fmac_f32_e32 v131, v82, v82
	v_fmac_f32_e32 v132, v84, v84
	v_add_f32_e32 v131, v131, v132
	v_add_f32_e32 v132, v86, v87
	v_add_f32_e32 v133, v88, v89
	v_add_f32_e32 v130, 0, v130
	v_add_f32_e32 v132, v132, v133
	v_add_f32_e32 v130, v132, v130
	v_mul_f32_e32 v132, v87, v87
	v_mul_f32_e32 v133, v89, v89
	v_fmac_f32_e32 v132, v86, v86
	v_fmac_f32_e32 v133, v88, v88
	v_add_f32_e32 v132, v132, v133
	v_add_f32_e32 v131, v131, v132
	v_add_f32_e32 v132, v18, v19
	v_add_f32_e32 v133, v20, v21
	v_add_f32_e32 v132, v132, v133
	v_add_f32_e32 v130, v132, v130
	v_mul_f32_e32 v132, v19, v19
	v_mul_f32_e32 v133, v21, v21
	v_fmac_f32_e32 v132, v18, v18
	v_fmac_f32_e32 v133, v20, v20
	v_add_f32_e32 v132, v132, v133
	v_add_f32_e32 v131, v132, v131
	v_add_f32_e32 v132, v22, v23
	v_add_f32_e32 v133, v24, v25
	v_add_f32_e32 v132, v132, v133
	v_add_f32_e32 v130, v132, v130
	v_mul_f32_e32 v132, v23, v23
	v_mul_f32_e32 v133, v25, v25
	v_fmac_f32_e32 v132, v22, v22
	v_fmac_f32_e32 v133, v24, v24
	v_add_f32_e32 v132, v132, v133
	v_add_f32_e32 v132, v132, v131
	ds_swizzle_b32 v131, v130 offset:swizzle(SWAP,16)
	ds_swizzle_b32 v133, v132 offset:swizzle(SWAP,16)
	s_waitcnt lgkmcnt(1)
	v_add_f32_e32 v131, v130, v131
	s_waitcnt lgkmcnt(0)
	v_add_f32_e32 v130, v132, v133
	v_mov_b32_e32 v133, v131
	v_mov_b32_e32 v132, v130
	s_nop 0
	v_permlane32_swap_b32_e32 v131, v133
	v_permlane32_swap_b32_e32 v130, v132
	s_and_saveexec_b64 s[2:3], vcc
	s_cbranch_execz .LBB0_1815
	v_add_f32_e32 v130, v130, v132
	v_add_f32_e32 v131, v131, v133
	s_lshl_b32 s20, s28, 11
	v_mul_f32_e32 v132, 0x3c800000, v131
	v_fma_f32 v130, -v131, v132, v130
	s_add_i32 s20, s1, s20
	v_max_f32_e32 v133, 0, v130
	v_lshl_add_u32 v130, v0, 5, s20
	ds_write_b64 v130, v[132:133] offset:4608
.LBB0_1815:
	s_or_b64 exec, exec, s[2:3]
	v_add_f32_e32 v130, v74, v75
	v_add_f32_e32 v131, v76, v77
	v_add_f32_e32 v130, v130, v131
	v_mul_f32_e32 v131, v75, v75
	v_mul_f32_e32 v132, v77, v77
	v_fmac_f32_e32 v131, v74, v74
	v_fmac_f32_e32 v132, v76, v76
	v_add_f32_e32 v131, v131, v132
	v_add_f32_e32 v132, v78, v79
	v_add_f32_e32 v133, v80, v81
	v_add_f32_e32 v130, 0, v130
	v_add_f32_e32 v132, v132, v133
	v_add_f32_e32 v130, v132, v130
	v_mul_f32_e32 v132, v79, v79
	v_mul_f32_e32 v133, v81, v81
	v_fmac_f32_e32 v132, v78, v78
	v_fmac_f32_e32 v133, v80, v80
	v_add_f32_e32 v132, v132, v133
	v_add_f32_e32 v131, v131, v132
	v_add_f32_e32 v132, v10, v11
	v_add_f32_e32 v133, v12, v13
	v_add_f32_e32 v132, v132, v133
	v_add_f32_e32 v130, v132, v130
	v_mul_f32_e32 v132, v11, v11
	v_mul_f32_e32 v133, v13, v13
	v_fmac_f32_e32 v132, v10, v10
	v_fmac_f32_e32 v133, v12, v12
	v_add_f32_e32 v132, v132, v133
	v_add_f32_e32 v131, v132, v131
	v_add_f32_e32 v132, v14, v15
	v_add_f32_e32 v133, v16, v17
	v_add_f32_e32 v132, v132, v133
	v_add_f32_e32 v130, v132, v130
	v_mul_f32_e32 v132, v15, v15
	v_mul_f32_e32 v133, v17, v17
	v_fmac_f32_e32 v132, v14, v14
	v_fmac_f32_e32 v133, v16, v16
	v_add_f32_e32 v132, v132, v133
	v_add_f32_e32 v132, v132, v131
	ds_swizzle_b32 v131, v130 offset:swizzle(SWAP,16)
	ds_swizzle_b32 v133, v132 offset:swizzle(SWAP,16)
	s_waitcnt lgkmcnt(1)
	v_add_f32_e32 v131, v130, v131
	s_waitcnt lgkmcnt(0)
	v_add_f32_e32 v130, v132, v133
	v_mov_b32_e32 v133, v131
	v_mov_b32_e32 v132, v130
	s_nop 0
	v_permlane32_swap_b32_e32 v131, v133
	v_permlane32_swap_b32_e32 v130, v132
	s_and_saveexec_b64 s[2:3], vcc
	s_cbranch_execz .LBB0_1817
	v_add_f32_e32 v130, v130, v132
	v_add_f32_e32 v131, v131, v133
	s_lshl_b32 s20, s28, 11
	v_mul_f32_e32 v132, 0x3c800000, v131
	v_fma_f32 v130, -v131, v132, v130
	s_add_i32 s20, s1, s20
	v_max_f32_e32 v133, 0, v130
	v_lshl_add_u32 v130, v0, 5, s20
	ds_write_b64 v130, v[132:133] offset:5120
.LBB0_1817:
	s_or_b64 exec, exec, s[2:3]
	v_add_f32_e32 v130, v66, v67
	v_add_f32_e32 v131, v68, v69
	v_add_f32_e32 v130, v130, v131
	v_mul_f32_e32 v131, v67, v67
	v_mul_f32_e32 v132, v69, v69
	v_fmac_f32_e32 v131, v66, v66
	v_fmac_f32_e32 v132, v68, v68
	v_add_f32_e32 v131, v131, v132
	v_add_f32_e32 v132, v70, v71
	v_add_f32_e32 v133, v72, v73
	v_add_f32_e32 v130, 0, v130
	v_add_f32_e32 v132, v132, v133
	v_add_f32_e32 v130, v132, v130
	v_mul_f32_e32 v132, v71, v71
	v_mul_f32_e32 v133, v73, v73
	v_fmac_f32_e32 v132, v70, v70
	v_fmac_f32_e32 v133, v72, v72
	v_add_f32_e32 v132, v132, v133
	v_add_f32_e32 v131, v131, v132
	v_add_f32_e32 v132, v2, v3
	v_add_f32_e32 v133, v4, v5
	v_add_f32_e32 v132, v132, v133
	v_add_f32_e32 v130, v132, v130
	v_mul_f32_e32 v132, v3, v3
	v_mul_f32_e32 v133, v5, v5
	v_fmac_f32_e32 v132, v2, v2
	v_fmac_f32_e32 v133, v4, v4
	v_add_f32_e32 v132, v132, v133
	v_add_f32_e32 v131, v132, v131
	v_add_f32_e32 v132, v6, v7
	v_add_f32_e32 v133, v8, v9
	v_add_f32_e32 v132, v132, v133
	v_add_f32_e32 v130, v132, v130
	v_mul_f32_e32 v132, v7, v7
	v_mul_f32_e32 v133, v9, v9
	v_fmac_f32_e32 v132, v6, v6
	v_fmac_f32_e32 v133, v8, v8
	v_add_f32_e32 v132, v132, v133
	v_add_f32_e32 v132, v132, v131
	ds_swizzle_b32 v131, v130 offset:swizzle(SWAP,16)
	ds_swizzle_b32 v133, v132 offset:swizzle(SWAP,16)
	s_waitcnt lgkmcnt(1)
	v_add_f32_e32 v131, v130, v131
	s_waitcnt lgkmcnt(0)
	v_add_f32_e32 v130, v132, v133
	v_mov_b32_e32 v133, v131
	v_mov_b32_e32 v132, v130
	s_nop 0
	v_permlane32_swap_b32_e32 v131, v133
	v_permlane32_swap_b32_e32 v130, v132
	s_and_saveexec_b64 s[2:3], vcc
	s_cbranch_execz .LBB0_1819
	v_add_f32_e32 v130, v130, v132
	v_add_f32_e32 v131, v131, v133
	s_lshl_b32 s20, s28, 11
	v_mul_f32_e32 v132, 0x3c800000, v131
	v_fma_f32 v130, -v131, v132, v130
	s_add_i32 s1, s1, s20
	v_max_f32_e32 v133, 0, v130
	v_lshl_add_u32 v0, v0, 5, s1
	ds_write_b64 v0, v[132:133] offset:5632
.LBB0_1819:
	s_or_b64 exec, exec, s[2:3]
	v_or_b32_e32 v0, s19, v231
	v_cmp_eq_u32_e32 vcc, 0, v0
	s_and_saveexec_b64 s[2:3], vcc
	ds_write_b32 v1, v1 offset:10240
	s_or_b64 exec, exec, s[2:3]
	s_waitcnt lgkmcnt(0)
	s_barrier
	v_cmp_gt_i32_e32 vcc, 32, v231
	s_and_saveexec_b64 s[2:3], vcc
	s_cbranch_execz .LBB0_1832
	s_lshl_b32 s1, s19, 5
	v_and_or_b32 v130, v231, 31, s1
	v_lshl_add_u32 v0, v130, 5, 0
	ds_read_b128 v[132:135], v0
	ds_read_b128 v[136:139], v0 offset:16
	s_ashr_i32 s19, s18, 31
	s_lshl_b64 s[18:19], s[18:19], 14
	s_add_u32 s18, s26, s18
	s_waitcnt lgkmcnt(1)
	v_add_f32_e32 v131, v132, v134
	s_waitcnt lgkmcnt(0)
	v_add_f32_e32 v131, v131, v136
	v_add_f32_e32 v131, v131, v138
	v_fmamk_f32 v132, v131, 0xbe800000, v132
	v_fmac_f32_e32 v134, 0xbe800000, v131
	v_fmamk_f32 v136, v131, 0xbe800000, v136
	v_fmac_f32_e32 v138, 0xbe800000, v131
	v_mul_f32_e32 v143, v132, v132
	v_mul_f32_e32 v145, v134, v134
	v_mul_f32_e32 v147, v136, v136
	v_mul_f32_e32 v149, v138, v138
	v_mov_b32_e32 v142, v133
	v_mov_b32_e32 v144, v135
	v_mov_b32_e32 v146, v137
	v_mov_b32_e32 v148, v139
	v_add_f32_e32 v132, v142, v144
	v_add_f32_e32 v133, v143, v145
	v_add_f32_e32 v134, v146, v148
	v_add_f32_e32 v135, v147, v149
	v_mul_f32_e32 v140, 0x3e800000, v131
	v_add_f32_e32 v132, v132, v134
	v_add_f32_e32 v133, v133, v135
	s_addc_u32 s19, s27, s19
	v_fmac_f32_e32 v132, 0x42800000, v133
	v_ashrrev_i32_e32 v131, 31, v130
	v_lshl_add_u64 v[136:137], v[130:131], 3, s[18:19]
	s_ashr_i32 s1, s0, 31
	v_and_b32_e32 v131, 0xffffffe0, v132
	v_lshl_add_u64 v[134:135], s[0:1], 3, v[136:137]
	v_or_b32_e32 v141, s25, v131
	s_mov_b64 s[0:1], 0x1000
	global_store_dwordx2 v[134:135], v[140:141], off sc1
	v_lshl_add_u64 v[140:141], v[136:137], 0, s[0:1]
	s_mov_b64 s[0:1], 0x1800
	s_memrealtime s[20:21]
	v_lshl_add_u64 v[142:143], v[136:137], 0, s[0:1]
	s_mov_b64 s[0:1], 0x2000
	v_lshl_add_u64 v[146:147], v[136:137], 0, s[0:1]
	s_mov_b64 s[0:1], 0x2800
	v_lshl_add_u64 v[148:149], v[136:137], 0, s[0:1]
	s_mov_b64 s[0:1], 0x3000
	v_lshl_add_u64 v[150:151], v[136:137], 0, s[0:1]
	s_mov_b64 s[0:1], 0x3800
	v_lshl_add_u64 v[152:153], v[136:137], 0, s[0:1]
	s_mov_b64 s[18:19], 0
	s_branch .LBB0_1825

.LBB0_1848:
	v_and_b32_e32 v250, 63, v130
	v_bfe_u32 v251, v130, 4, 2
	s_lshl_b32 s5, s23, 5
	s_lshl_b32 s4, s29, 8
	s_barrier
	s_or_b32 s5, s4, s5
	v_add_u32_e32 v238, s42, v0
	v_lshl_add_u32 v198, v251, 3, s5
	v_lshl_add_u32 v232, s0, 8, v238
	v_ashrrev_i32_e32 v199, 31, v198
	v_ashrrev_i32_e32 v233, 31, v232
	v_lshl_add_u64 v[134:135], v[198:199], 1, s[12:13]
	v_lshlrev_b64 v[2:3], 12, v[232:233]
	v_add_u32_e32 v228, 16, v232
	s_mov_b32 s5, 1.0
	s_mov_b32 s6, 0x3fd744fd
	s_mov_b32 s20, s18
	v_lshl_add_u64 v[230:231], v[134:135], 0, v[2:3]
	v_ashrrev_i32_e32 v229, 31, v228
	global_load_dwordx4 v[130:133], v[230:231], off
	global_load_dwordx4 v[194:197], v[230:231], off offset:256
	v_lshlrev_b64 v[2:3], 12, v[228:229]
	v_add_u32_e32 v224, 32, v232
	v_lshl_add_u64 v[226:227], v[134:135], 0, v[2:3]
	v_ashrrev_i32_e32 v225, 31, v224
	global_load_dwordx4 v[190:193], v[226:227], off
	global_load_dwordx4 v[186:189], v[226:227], off offset:256
	v_lshlrev_b64 v[2:3], 12, v[224:225]
	v_add_u32_e32 v220, 48, v232
	v_lshl_add_u64 v[222:223], v[134:135], 0, v[2:3]
	v_ashrrev_i32_e32 v221, 31, v220
	global_load_dwordx4 v[182:185], v[222:223], off
	global_load_dwordx4 v[178:181], v[222:223], off offset:256
	v_lshlrev_b64 v[2:3], 12, v[220:221]
	v_add_u32_e32 v216, 0x80, v232
	v_lshl_add_u64 v[218:219], v[134:135], 0, v[2:3]
	v_ashrrev_i32_e32 v217, 31, v216
	global_load_dwordx4 v[30:33], v[218:219], off
	global_load_dwordx4 v[26:29], v[218:219], off offset:256
	v_lshlrev_b64 v[2:3], 12, v[216:217]
	v_add_u32_e32 v212, 0x90, v232
	v_lshl_add_u64 v[214:215], v[134:135], 0, v[2:3]
	v_ashrrev_i32_e32 v213, 31, v212
	global_load_dwordx4 v[22:25], v[214:215], off
	global_load_dwordx4 v[18:21], v[214:215], off offset:256
	v_lshlrev_b64 v[2:3], 12, v[212:213]
	v_add_u32_e32 v208, 0xa0, v232
	v_lshl_add_u64 v[210:211], v[134:135], 0, v[2:3]
	v_ashrrev_i32_e32 v209, 31, v208
	global_load_dwordx4 v[14:17], v[210:211], off
	global_load_dwordx4 v[10:13], v[210:211], off offset:256
	v_lshlrev_b64 v[2:3], 12, v[208:209]
	v_add_u32_e32 v200, 0xb0, v232
	v_lshl_add_u64 v[206:207], v[134:135], 0, v[2:3]
	v_ashrrev_i32_e32 v201, 31, v200
	global_load_dwordx4 v[6:9], v[206:207], off
	global_load_dwordx4 v[2:5], v[206:207], off offset:256
	v_lshlrev_b64 v[136:137], 12, v[200:201]
	v_lshl_add_u64 v[204:205], v[134:135], 0, v[136:137]
	global_load_dwordx4 v[174:177], v[204:205], off
	global_load_dwordx4 v[170:173], v[204:205], off offset:256
	s_lshl_b32 s5, s23, 3
	v_cmp_eq_u32_e32 vcc, 0, v251
	s_add_i32 s5, s5, 0
	s_waitcnt vmcnt(15)
	v_lshlrev_b32_e32 v240, 16, v132
	v_and_b32_e32 v241, 0xffff0000, v132
	v_lshlrev_b32_e32 v132, 16, v133
	v_and_b32_e32 v133, 0xffff0000, v133
	v_lshlrev_b32_e32 v134, 16, v130
	v_and_b32_e32 v135, 0xffff0000, v130
	v_lshlrev_b32_e32 v130, 16, v131
	v_and_b32_e32 v131, 0xffff0000, v131
	v_pk_fma_f32 v[136:137], s[6:7], v[130:131], v[64:65] op_sel_hi:[0,1,1]
	v_pk_fma_f32 v[132:133], s[6:7], v[132:133], v[120:121] op_sel_hi:[0,1,1]
	s_waitcnt vmcnt(14)
	v_lshlrev_b32_e32 v120, 16, v197
	v_and_b32_e32 v121, 0xffff0000, v197
	v_lshlrev_b32_e32 v64, 16, v195
	v_and_b32_e32 v65, 0xffff0000, v195
	v_pk_fma_f32 v[134:135], s[6:7], v[134:135], v[62:63] op_sel_hi:[0,1,1]
	v_pk_fma_f32 v[130:131], s[6:7], v[240:241], v[118:119] op_sel_hi:[0,1,1]
	v_lshlrev_b32_e32 v118, 16, v196
	v_and_b32_e32 v119, 0xffff0000, v196
	v_lshlrev_b32_e32 v62, 16, v194
	v_and_b32_e32 v63, 0xffff0000, v194
	v_pk_fma_f32 v[64:65], s[6:7], v[64:65], v[60:61] op_sel_hi:[0,1,1]
	v_pk_fma_f32 v[60:61], s[6:7], v[120:121], v[116:117] op_sel_hi:[0,1,1]
	s_waitcnt vmcnt(13)
	v_lshlrev_b32_e32 v120, 16, v193
	v_and_b32_e32 v121, 0xffff0000, v193
	v_pk_fma_f32 v[62:63], s[6:7], v[62:63], v[58:59] op_sel_hi:[0,1,1]
	v_pk_fma_f32 v[58:59], s[6:7], v[118:119], v[114:115] op_sel_hi:[0,1,1]
	v_lshlrev_b32_e32 v118, 16, v192
	v_and_b32_e32 v119, 0xffff0000, v192
	v_pk_fma_f32 v[120:121], s[6:7], v[120:121], v[52:53] op_sel_hi:[0,1,1]
	s_waitcnt vmcnt(12)
	v_lshlrev_b32_e32 v52, 16, v187
	v_and_b32_e32 v53, 0xffff0000, v187
	v_pk_fma_f32 v[118:119], s[6:7], v[118:119], v[50:51] op_sel_hi:[0,1,1]
	v_lshlrev_b32_e32 v50, 16, v186
	v_and_b32_e32 v51, 0xffff0000, v186
	v_pk_fma_f32 v[52:53], s[6:7], v[52:53], v[112:113] op_sel_hi:[0,1,1]
	s_waitcnt vmcnt(11)
	v_lshlrev_b32_e32 v112, 16, v183
	v_and_b32_e32 v113, 0xffff0000, v183
	v_pk_fma_f32 v[50:51], s[6:7], v[50:51], v[110:111] op_sel_hi:[0,1,1]
	v_lshlrev_b32_e32 v110, 16, v182
	v_and_b32_e32 v111, 0xffff0000, v182
	v_pk_fma_f32 v[112:113], s[6:7], v[112:113], v[48:49] op_sel_hi:[0,1,1]
	s_waitcnt vmcnt(10)
	v_lshlrev_b32_e32 v48, 16, v181
	v_and_b32_e32 v49, 0xffff0000, v181
	v_pk_fma_f32 v[110:111], s[6:7], v[110:111], v[46:47] op_sel_hi:[0,1,1]
	v_lshlrev_b32_e32 v46, 16, v180
	v_and_b32_e32 v47, 0xffff0000, v180
	v_pk_fma_f32 v[48:49], s[6:7], v[48:49], v[104:105] op_sel_hi:[0,1,1]
	s_waitcnt vmcnt(9)
	v_lshlrev_b32_e32 v104, 16, v30
	v_and_b32_e32 v105, 0xffff0000, v30
	v_lshlrev_b32_e32 v30, 16, v31
	v_and_b32_e32 v31, 0xffff0000, v31
	v_pk_fma_f32 v[46:47], s[6:7], v[46:47], v[102:103] op_sel_hi:[0,1,1]
	v_lshlrev_b32_e32 v102, 16, v32
	v_and_b32_e32 v103, 0xffff0000, v32
	v_lshlrev_b32_e32 v32, 16, v33
	v_and_b32_e32 v33, 0xffff0000, v33
	v_pk_fma_f32 v[100:101], s[6:7], v[30:31], v[100:101] op_sel_hi:[0,1,1]
	s_waitcnt vmcnt(8)
	v_lshlrev_b32_e32 v30, 16, v28
	v_and_b32_e32 v31, 0xffff0000, v28
	v_lshlrev_b32_e32 v28, 16, v29
	v_and_b32_e32 v29, 0xffff0000, v29
	v_pk_fma_f32 v[98:99], s[6:7], v[104:105], v[98:99] op_sel_hi:[0,1,1]
	v_pk_fma_f32 v[104:105], s[6:7], v[32:33], v[36:37] op_sel_hi:[0,1,1]
	v_lshlrev_b32_e32 v32, 16, v26
	v_and_b32_e32 v33, 0xffff0000, v26
	v_lshlrev_b32_e32 v26, 16, v27
	v_and_b32_e32 v27, 0xffff0000, v27
	v_pk_fma_f32 v[40:41], s[6:7], v[28:29], v[40:41] op_sel_hi:[0,1,1]
	s_waitcnt vmcnt(7)
	v_lshlrev_b32_e32 v28, 16, v22
	v_and_b32_e32 v29, 0xffff0000, v22
	v_lshlrev_b32_e32 v22, 16, v23
	v_and_b32_e32 v23, 0xffff0000, v23
	v_pk_fma_f32 v[36:37], s[6:7], v[26:27], v[160:161] op_sel_hi:[0,1,1]
	v_lshlrev_b32_e32 v26, 16, v24
	v_and_b32_e32 v27, 0xffff0000, v24
	v_lshlrev_b32_e32 v24, 16, v25
	v_and_b32_e32 v25, 0xffff0000, v25
	v_pk_fma_f32 v[92:93], s[6:7], v[22:23], v[92:93] op_sel_hi:[0,1,1]
	s_waitcnt vmcnt(6)
	v_lshlrev_b32_e32 v22, 16, v20
	v_and_b32_e32 v23, 0xffff0000, v20
	v_lshlrev_b32_e32 v20, 16, v21
	v_and_b32_e32 v21, 0xffff0000, v21
	v_pk_fma_f32 v[102:103], s[6:7], v[102:103], v[34:35] op_sel_hi:[0,1,1]
	v_pk_fma_f32 v[34:35], s[6:7], v[32:33], v[158:159] op_sel_hi:[0,1,1]
	v_pk_fma_f32 v[96:97], s[6:7], v[24:25], v[96:97] op_sel_hi:[0,1,1]
	v_lshlrev_b32_e32 v24, 16, v18
	v_and_b32_e32 v25, 0xffff0000, v18
	v_lshlrev_b32_e32 v18, 16, v19
	v_and_b32_e32 v19, 0xffff0000, v19
	v_pk_fma_f32 v[32:33], s[6:7], v[20:21], v[156:157] op_sel_hi:[0,1,1]
	s_waitcnt vmcnt(5)
	v_lshlrev_b32_e32 v20, 16, v14
	v_and_b32_e32 v21, 0xffff0000, v14
	v_lshlrev_b32_e32 v14, 16, v15
	v_and_b32_e32 v15, 0xffff0000, v15
	v_pk_fma_f32 v[90:91], s[6:7], v[28:29], v[90:91] op_sel_hi:[0,1,1]
	v_pk_fma_f32 v[28:29], s[6:7], v[18:19], v[164:165] op_sel_hi:[0,1,1]
	v_lshlrev_b32_e32 v18, 16, v16
	v_and_b32_e32 v19, 0xffff0000, v16
	v_lshlrev_b32_e32 v16, 16, v17
	v_and_b32_e32 v17, 0xffff0000, v17
	v_pk_fma_f32 v[84:85], s[6:7], v[14:15], v[84:85] op_sel_hi:[0,1,1]
	s_waitcnt vmcnt(4)
	v_lshlrev_b32_e32 v14, 16, v12
	v_and_b32_e32 v15, 0xffff0000, v12
	v_lshlrev_b32_e32 v12, 16, v13
	v_and_b32_e32 v13, 0xffff0000, v13
	v_pk_fma_f32 v[94:95], s[6:7], v[26:27], v[94:95] op_sel_hi:[0,1,1]
	v_pk_fma_f32 v[26:27], s[6:7], v[24:25], v[162:163] op_sel_hi:[0,1,1]
	v_pk_fma_f32 v[88:89], s[6:7], v[16:17], v[88:89] op_sel_hi:[0,1,1]
	v_lshlrev_b32_e32 v16, 16, v10
	v_and_b32_e32 v17, 0xffff0000, v10
	v_lshlrev_b32_e32 v10, 16, v11
	v_and_b32_e32 v11, 0xffff0000, v11
	v_pk_fma_f32 v[24:25], s[6:7], v[12:13], v[148:149] op_sel_hi:[0,1,1]
	s_waitcnt vmcnt(3)
	v_lshlrev_b32_e32 v12, 16, v6
	v_and_b32_e32 v13, 0xffff0000, v6
	v_lshlrev_b32_e32 v6, 16, v7
	v_and_b32_e32 v7, 0xffff0000, v7
	v_pk_fma_f32 v[82:83], s[6:7], v[20:21], v[82:83] op_sel_hi:[0,1,1]
	v_pk_fma_f32 v[20:21], s[6:7], v[10:11], v[152:153] op_sel_hi:[0,1,1]
	v_lshlrev_b32_e32 v10, 16, v8
	v_and_b32_e32 v11, 0xffff0000, v8
	v_lshlrev_b32_e32 v8, 16, v9
	v_and_b32_e32 v9, 0xffff0000, v9
	v_pk_fma_f32 v[76:77], s[6:7], v[6:7], v[76:77] op_sel_hi:[0,1,1]
	s_waitcnt vmcnt(2)
	v_lshlrev_b32_e32 v6, 16, v4
	v_and_b32_e32 v7, 0xffff0000, v4
	v_pk_fma_f32 v[38:39], s[6:7], v[30:31], v[38:39] op_sel_hi:[0,1,1]
	v_pk_fma_f32 v[30:31], s[6:7], v[22:23], v[154:155] op_sel_hi:[0,1,1]
	v_pk_fma_f32 v[22:23], s[6:7], v[14:15], v[146:147] op_sel_hi:[0,1,1]
	v_pk_fma_f32 v[80:81], s[6:7], v[8:9], v[80:81] op_sel_hi:[0,1,1]
	v_lshlrev_b32_e32 v8, 16, v2
	v_and_b32_e32 v9, 0xffff0000, v2
	v_pk_fma_f32 v[14:15], s[6:7], v[6:7], v[138:139] op_sel_hi:[0,1,1]
	s_waitcnt vmcnt(1)
	v_lshlrev_b32_e32 v6, 16, v174
	v_and_b32_e32 v7, 0xffff0000, v174
	v_pk_fma_f32 v[78:79], s[6:7], v[10:11], v[78:79] op_sel_hi:[0,1,1]
	v_pk_fma_f32 v[10:11], s[6:7], v[8:9], v[142:143] op_sel_hi:[0,1,1]
	v_lshlrev_b32_e32 v8, 16, v175
	v_and_b32_e32 v9, 0xffff0000, v175
	v_pk_fma_f32 v[66:67], s[6:7], v[6:7], v[66:67] op_sel_hi:[0,1,1]
	s_waitcnt vmcnt(0)
	v_lshlrev_b32_e32 v6, 16, v172
	v_and_b32_e32 v7, 0xffff0000, v172
	v_pk_fma_f32 v[68:69], s[6:7], v[8:9], v[68:69] op_sel_hi:[0,1,1]
	v_lshlrev_b32_e32 v8, 16, v173
	v_and_b32_e32 v9, 0xffff0000, v173
	v_pk_fma_f32 v[6:7], s[6:7], v[6:7], v[122:123] op_sel_hi:[0,1,1]
	v_add_f32_e32 v122, v134, v135
	v_add_f32_e32 v123, v136, v137
	v_pk_fma_f32 v[8:9], s[6:7], v[8:9], v[124:125] op_sel_hi:[0,1,1]
	v_add_f32_e32 v122, v122, v123
	v_mul_f32_e32 v123, v135, v135
	v_mul_f32_e32 v124, v137, v137
	v_fmac_f32_e32 v123, v134, v134
	v_fmac_f32_e32 v124, v136, v136
	v_add_f32_e32 v123, v123, v124
	v_add_f32_e32 v124, v130, v131
	v_add_f32_e32 v125, v132, v133
	v_add_f32_e32 v122, 0, v122
	v_add_f32_e32 v124, v124, v125
	v_add_f32_e32 v122, v124, v122
	v_mul_f32_e32 v124, v131, v131
	v_mul_f32_e32 v125, v133, v133
	v_fmac_f32_e32 v124, v130, v130
	v_fmac_f32_e32 v125, v132, v132
	v_add_f32_e32 v124, v124, v125
	v_add_f32_e32 v123, v123, v124
	v_add_f32_e32 v124, v62, v63
	v_add_f32_e32 v125, v64, v65
	v_add_f32_e32 v124, v124, v125
	v_add_f32_e32 v122, v124, v122
	v_mul_f32_e32 v124, v63, v63
	v_mul_f32_e32 v125, v65, v65
	v_fmac_f32_e32 v124, v62, v62
	v_fmac_f32_e32 v125, v64, v64
	v_add_f32_e32 v124, v124, v125
	v_add_f32_e32 v123, v124, v123
	v_add_f32_e32 v124, v58, v59
	v_add_f32_e32 v125, v60, v61
	v_add_f32_e32 v124, v124, v125
	v_add_f32_e32 v122, v124, v122
	v_mul_f32_e32 v124, v59, v59
	v_mul_f32_e32 v125, v61, v61
	v_fmac_f32_e32 v124, v58, v58
	v_fmac_f32_e32 v125, v60, v60
	v_add_f32_e32 v124, v124, v125
	v_add_f32_e32 v124, v124, v123
	ds_swizzle_b32 v123, v122 offset:swizzle(SWAP,16)
	v_lshlrev_b32_e32 v114, 16, v190
	v_and_b32_e32 v115, 0xffff0000, v190
	v_lshlrev_b32_e32 v116, 16, v191
	v_and_b32_e32 v117, 0xffff0000, v191
	s_waitcnt lgkmcnt(0)
	v_add_f32_e32 v123, v122, v123
	ds_swizzle_b32 v122, v124 offset:swizzle(SWAP,16)
	v_pk_fma_f32 v[116:117], s[6:7], v[116:117], v[56:57] op_sel_hi:[0,1,1]
	v_pk_fma_f32 v[114:115], s[6:7], v[114:115], v[54:55] op_sel_hi:[0,1,1]
	v_lshlrev_b32_e32 v54, 16, v188
	v_and_b32_e32 v55, 0xffff0000, v188
	v_lshlrev_b32_e32 v56, 16, v189
	v_and_b32_e32 v57, 0xffff0000, v189
	v_lshlrev_b32_e32 v4, 16, v5
	v_and_b32_e32 v5, 0xffff0000, v5
	v_lshlrev_b32_e32 v2, 16, v3
	v_and_b32_e32 v3, 0xffff0000, v3
	v_pk_fma_f32 v[56:57], s[6:7], v[56:57], v[108:109] op_sel_hi:[0,1,1]
	v_pk_fma_f32 v[54:55], s[6:7], v[54:55], v[106:107] op_sel_hi:[0,1,1]
	v_lshlrev_b32_e32 v106, 16, v184
	v_and_b32_e32 v107, 0xffff0000, v184
	v_lshlrev_b32_e32 v108, 16, v185
	v_and_b32_e32 v109, 0xffff0000, v185
	v_pk_fma_f32 v[86:87], s[6:7], v[18:19], v[86:87] op_sel_hi:[0,1,1]
	v_pk_fma_f32 v[18:19], s[6:7], v[16:17], v[150:151] op_sel_hi:[0,1,1]
	v_pk_fma_f32 v[74:75], s[6:7], v[12:13], v[74:75] op_sel_hi:[0,1,1]
	v_pk_fma_f32 v[12:13], s[6:7], v[2:3], v[144:145] op_sel_hi:[0,1,1]
	v_pk_fma_f32 v[16:17], s[6:7], v[4:5], v[140:141] op_sel_hi:[0,1,1]
	v_lshlrev_b32_e32 v2, 16, v176
	v_and_b32_e32 v3, 0xffff0000, v176
	v_lshlrev_b32_e32 v4, 16, v177
	v_and_b32_e32 v5, 0xffff0000, v177
	v_pk_fma_f32 v[108:109], s[6:7], v[108:109], v[44:45] op_sel_hi:[0,1,1]
	v_pk_fma_f32 v[106:107], s[6:7], v[106:107], v[42:43] op_sel_hi:[0,1,1]
	v_lshlrev_b32_e32 v42, 16, v178
	v_and_b32_e32 v43, 0xffff0000, v178
	v_lshlrev_b32_e32 v44, 16, v179
	v_and_b32_e32 v45, 0xffff0000, v179
	v_pk_fma_f32 v[72:73], s[6:7], v[4:5], v[72:73] op_sel_hi:[0,1,1]
	v_pk_fma_f32 v[70:71], s[6:7], v[2:3], v[70:71] op_sel_hi:[0,1,1]
	v_lshlrev_b32_e32 v2, 16, v170
	v_and_b32_e32 v3, 0xffff0000, v170
	v_lshlrev_b32_e32 v4, 16, v171
	v_and_b32_e32 v5, 0xffff0000, v171
	v_pk_fma_f32 v[44:45], s[6:7], v[44:45], v[168:169] op_sel_hi:[0,1,1]
	v_pk_fma_f32 v[42:43], s[6:7], v[42:43], v[166:167] op_sel_hi:[0,1,1]
	v_pk_fma_f32 v[4:5], s[6:7], v[4:5], v[128:129] op_sel_hi:[0,1,1]
	v_pk_fma_f32 v[2:3], s[6:7], v[2:3], v[126:127] op_sel_hi:[0,1,1]
	s_waitcnt lgkmcnt(0)
	v_add_f32_e32 v122, v124, v122
	v_mov_b32_e32 v125, v123
	v_mov_b32_e32 v124, v122
	s_nop 0
	v_permlane32_swap_b32_e32 v123, v125
	v_permlane32_swap_b32_e32 v122, v124
	s_and_saveexec_b64 s[6:7], vcc
	s_mov_b64 s[52:53], 0x400
	s_cbranch_execz .LBB0_1850
	v_add_f32_e32 v122, v122, v124
	v_add_f32_e32 v123, v123, v125
	s_lshl_b32 s18, s22, 11
	v_mul_f32_e32 v124, 0x3c800000, v123
	v_fma_f32 v122, -v123, v124, v122
	s_add_i32 s18, s5, s18
	v_max_f32_e32 v125, 0, v122
	v_lshl_add_u32 v122, v0, 5, s18
	ds_write_b64 v122, v[124:125]
.LBB0_1850:
	s_or_b64 exec, exec, s[6:7]
	v_add_f32_e32 v122, v114, v115
	v_add_f32_e32 v123, v116, v117
	v_add_f32_e32 v122, v122, v123
	v_mul_f32_e32 v123, v115, v115
	v_mul_f32_e32 v124, v117, v117
	v_fmac_f32_e32 v123, v114, v114
	v_fmac_f32_e32 v124, v116, v116
	v_add_f32_e32 v123, v123, v124
	v_add_f32_e32 v124, v118, v119
	v_add_f32_e32 v125, v120, v121
	v_add_f32_e32 v122, 0, v122
	v_add_f32_e32 v124, v124, v125
	v_add_f32_e32 v122, v124, v122
	v_mul_f32_e32 v124, v119, v119
	v_mul_f32_e32 v125, v121, v121
	v_fmac_f32_e32 v124, v118, v118
	v_fmac_f32_e32 v125, v120, v120
	v_add_f32_e32 v124, v124, v125
	v_add_f32_e32 v123, v123, v124
	v_add_f32_e32 v124, v50, v51
	v_add_f32_e32 v125, v52, v53
	v_add_f32_e32 v124, v124, v125
	v_add_f32_e32 v122, v124, v122
	v_mul_f32_e32 v124, v51, v51
	v_mul_f32_e32 v125, v53, v53
	v_fmac_f32_e32 v124, v50, v50
	v_fmac_f32_e32 v125, v52, v52
	v_add_f32_e32 v124, v124, v125
	v_add_f32_e32 v123, v124, v123
	v_add_f32_e32 v124, v54, v55
	v_add_f32_e32 v125, v56, v57
	v_add_f32_e32 v124, v124, v125
	v_add_f32_e32 v122, v124, v122
	v_mul_f32_e32 v124, v55, v55
	v_mul_f32_e32 v125, v57, v57
	v_fmac_f32_e32 v124, v54, v54
	v_fmac_f32_e32 v125, v56, v56
	v_add_f32_e32 v124, v124, v125
	v_add_f32_e32 v124, v124, v123
	ds_swizzle_b32 v123, v122 offset:swizzle(SWAP,16)
	ds_swizzle_b32 v125, v124 offset:swizzle(SWAP,16)
	s_waitcnt lgkmcnt(1)
	v_add_f32_e32 v123, v122, v123
	s_waitcnt lgkmcnt(0)
	v_add_f32_e32 v122, v124, v125
	v_mov_b32_e32 v125, v123
	v_mov_b32_e32 v124, v122
	s_nop 0
	v_permlane32_swap_b32_e32 v123, v125
	v_permlane32_swap_b32_e32 v122, v124
	s_and_saveexec_b64 s[6:7], vcc
	s_cbranch_execz .LBB0_1852
	v_add_f32_e32 v122, v122, v124
	v_add_f32_e32 v123, v123, v125
	s_lshl_b32 s18, s22, 11
	v_mul_f32_e32 v124, 0x3c800000, v123
	v_fma_f32 v122, -v123, v124, v122
	s_add_i32 s18, s5, s18
	v_max_f32_e32 v125, 0, v122
	v_lshl_add_u32 v122, v0, 5, s18
	ds_write_b64 v122, v[124:125] offset:512
.LBB0_1852:
	s_or_b64 exec, exec, s[6:7]
	v_add_f32_e32 v122, v110, v111
	v_add_f32_e32 v123, v112, v113
	v_add_f32_e32 v122, v122, v123
	v_mul_f32_e32 v123, v111, v111
	v_mul_f32_e32 v124, v113, v113
	v_fmac_f32_e32 v123, v110, v110
	v_fmac_f32_e32 v124, v112, v112
	v_add_f32_e32 v123, v123, v124
	v_add_f32_e32 v124, v106, v107
	v_add_f32_e32 v125, v108, v109
	v_add_f32_e32 v122, 0, v122
	v_add_f32_e32 v124, v124, v125
	v_add_f32_e32 v122, v124, v122
	v_mul_f32_e32 v124, v107, v107
	v_mul_f32_e32 v125, v109, v109
	v_fmac_f32_e32 v124, v106, v106
	v_fmac_f32_e32 v125, v108, v108
	v_add_f32_e32 v124, v124, v125
	v_add_f32_e32 v123, v123, v124
	v_add_f32_e32 v124, v42, v43
	v_add_f32_e32 v125, v44, v45
	v_add_f32_e32 v124, v124, v125
	v_add_f32_e32 v122, v124, v122
	v_mul_f32_e32 v124, v43, v43
	v_mul_f32_e32 v125, v45, v45
	v_fmac_f32_e32 v124, v42, v42
	v_fmac_f32_e32 v125, v44, v44
	v_add_f32_e32 v124, v124, v125
	v_add_f32_e32 v123, v124, v123
	v_add_f32_e32 v124, v46, v47
	v_add_f32_e32 v125, v48, v49
	v_add_f32_e32 v124, v124, v125
	v_add_f32_e32 v122, v124, v122
	v_mul_f32_e32 v124, v47, v47
	v_mul_f32_e32 v125, v49, v49
	v_fmac_f32_e32 v124, v46, v46
	v_fmac_f32_e32 v125, v48, v48
	v_add_f32_e32 v124, v124, v125
	v_add_f32_e32 v124, v124, v123
	ds_swizzle_b32 v123, v122 offset:swizzle(SWAP,16)
	ds_swizzle_b32 v125, v124 offset:swizzle(SWAP,16)
	s_waitcnt lgkmcnt(1)
	v_add_f32_e32 v123, v122, v123
	s_waitcnt lgkmcnt(0)
	v_add_f32_e32 v122, v124, v125
	v_mov_b32_e32 v125, v123
	v_mov_b32_e32 v124, v122
	s_nop 0
	v_permlane32_swap_b32_e32 v123, v125
	v_permlane32_swap_b32_e32 v122, v124
	s_and_saveexec_b64 s[6:7], vcc
	s_cbranch_execz .LBB0_1854
	v_add_f32_e32 v122, v122, v124
	v_add_f32_e32 v123, v123, v125
	s_lshl_b32 s18, s22, 11
	v_mul_f32_e32 v124, 0x3c800000, v123
	v_fma_f32 v122, -v123, v124, v122
	s_add_i32 s18, s5, s18
	v_max_f32_e32 v125, 0, v122
	v_lshl_add_u32 v122, v0, 5, s18
	ds_write_b64 v122, v[124:125] offset:1024
.LBB0_1854:
	s_or_b64 exec, exec, s[6:7]
	v_add_f32_e32 v122, v98, v99
	v_add_f32_e32 v123, v100, v101
	v_add_f32_e32 v122, v122, v123
	v_mul_f32_e32 v123, v99, v99
	v_mul_f32_e32 v124, v101, v101
	v_fmac_f32_e32 v123, v98, v98
	v_fmac_f32_e32 v124, v100, v100
	v_add_f32_e32 v123, v123, v124
	v_add_f32_e32 v124, v102, v103
	v_add_f32_e32 v125, v104, v105
	v_add_f32_e32 v122, 0, v122
	v_add_f32_e32 v124, v124, v125
	v_add_f32_e32 v122, v124, v122
	v_mul_f32_e32 v124, v103, v103
	v_mul_f32_e32 v125, v105, v105
	v_fmac_f32_e32 v124, v102, v102
	v_fmac_f32_e32 v125, v104, v104
	v_add_f32_e32 v124, v124, v125
	v_add_f32_e32 v123, v123, v124
	v_add_f32_e32 v124, v34, v35
	v_add_f32_e32 v125, v36, v37
	v_add_f32_e32 v124, v124, v125
	v_add_f32_e32 v122, v124, v122
	v_mul_f32_e32 v124, v35, v35
	v_mul_f32_e32 v125, v37, v37
	v_fmac_f32_e32 v124, v34, v34
	v_fmac_f32_e32 v125, v36, v36
	v_add_f32_e32 v124, v124, v125
	v_add_f32_e32 v123, v124, v123
	v_add_f32_e32 v124, v38, v39
	v_add_f32_e32 v125, v40, v41
	v_add_f32_e32 v124, v124, v125
	v_add_f32_e32 v122, v124, v122
	v_mul_f32_e32 v124, v39, v39
	v_mul_f32_e32 v125, v41, v41
	v_fmac_f32_e32 v124, v38, v38
	v_fmac_f32_e32 v125, v40, v40
	v_add_f32_e32 v124, v124, v125
	v_add_f32_e32 v124, v124, v123
	ds_swizzle_b32 v123, v122 offset:swizzle(SWAP,16)
	ds_swizzle_b32 v125, v124 offset:swizzle(SWAP,16)
	s_waitcnt lgkmcnt(1)
	v_add_f32_e32 v123, v122, v123
	s_waitcnt lgkmcnt(0)
	v_add_f32_e32 v122, v124, v125
	v_mov_b32_e32 v125, v123
	v_mov_b32_e32 v124, v122
	s_nop 0
	v_permlane32_swap_b32_e32 v123, v125
	v_permlane32_swap_b32_e32 v122, v124
	s_and_saveexec_b64 s[6:7], vcc
	s_cbranch_execz .LBB0_1856
	v_add_f32_e32 v122, v122, v124
	v_add_f32_e32 v123, v123, v125
	s_lshl_b32 s18, s22, 11
	v_mul_f32_e32 v124, 0x3c800000, v123
	v_fma_f32 v122, -v123, v124, v122
	s_add_i32 s18, s5, s18
	v_max_f32_e32 v125, 0, v122
	v_lshl_add_u32 v122, v0, 5, s18
	ds_write_b64 v122, v[124:125] offset:1536
.LBB0_1856:
	s_or_b64 exec, exec, s[6:7]
	v_add_f32_e32 v122, v90, v91
	v_add_f32_e32 v123, v92, v93
	v_add_f32_e32 v122, v122, v123
	v_mul_f32_e32 v123, v91, v91
	v_mul_f32_e32 v124, v93, v93
	v_fmac_f32_e32 v123, v90, v90
	v_fmac_f32_e32 v124, v92, v92
	v_add_f32_e32 v123, v123, v124
	v_add_f32_e32 v124, v94, v95
	v_add_f32_e32 v125, v96, v97
	v_add_f32_e32 v122, 0, v122
	v_add_f32_e32 v124, v124, v125
	v_add_f32_e32 v122, v124, v122
	v_mul_f32_e32 v124, v95, v95
	v_mul_f32_e32 v125, v97, v97
	v_fmac_f32_e32 v124, v94, v94
	v_fmac_f32_e32 v125, v96, v96
	v_add_f32_e32 v124, v124, v125
	v_add_f32_e32 v123, v123, v124
	v_add_f32_e32 v124, v26, v27
	v_add_f32_e32 v125, v28, v29
	v_add_f32_e32 v124, v124, v125
	v_add_f32_e32 v122, v124, v122
	v_mul_f32_e32 v124, v27, v27
	v_mul_f32_e32 v125, v29, v29
	v_fmac_f32_e32 v124, v26, v26
	v_fmac_f32_e32 v125, v28, v28
	v_add_f32_e32 v124, v124, v125
	v_add_f32_e32 v123, v124, v123
	v_add_f32_e32 v124, v30, v31
	v_add_f32_e32 v125, v32, v33
	v_add_f32_e32 v124, v124, v125
	v_add_f32_e32 v122, v124, v122
	v_mul_f32_e32 v124, v31, v31
	v_mul_f32_e32 v125, v33, v33
	v_fmac_f32_e32 v124, v30, v30
	v_fmac_f32_e32 v125, v32, v32
	v_add_f32_e32 v124, v124, v125
	v_add_f32_e32 v124, v124, v123
	ds_swizzle_b32 v123, v122 offset:swizzle(SWAP,16)
	ds_swizzle_b32 v125, v124 offset:swizzle(SWAP,16)
	s_waitcnt lgkmcnt(1)
	v_add_f32_e32 v123, v122, v123
	s_waitcnt lgkmcnt(0)
	v_add_f32_e32 v122, v124, v125
	v_mov_b32_e32 v125, v123
	v_mov_b32_e32 v124, v122
	s_nop 0
	v_permlane32_swap_b32_e32 v123, v125
	v_permlane32_swap_b32_e32 v122, v124
	s_and_saveexec_b64 s[6:7], vcc
	s_cbranch_execz .LBB0_1858
	v_add_f32_e32 v122, v122, v124
	v_add_f32_e32 v123, v123, v125
	s_lshl_b32 s18, s22, 11
	v_mul_f32_e32 v124, 0x3c800000, v123
	v_fma_f32 v122, -v123, v124, v122
	s_add_i32 s18, s5, s18
	v_max_f32_e32 v125, 0, v122
	v_lshl_add_u32 v122, v0, 5, s18
	ds_write_b64 v122, v[124:125] offset:4096
.LBB0_1858:
	s_or_b64 exec, exec, s[6:7]
	v_add_f32_e32 v122, v82, v83
	v_add_f32_e32 v123, v84, v85
	v_add_f32_e32 v122, v122, v123
	v_mul_f32_e32 v123, v83, v83
	v_mul_f32_e32 v124, v85, v85
	v_fmac_f32_e32 v123, v82, v82
	v_fmac_f32_e32 v124, v84, v84
	v_add_f32_e32 v123, v123, v124
	v_add_f32_e32 v124, v86, v87
	v_add_f32_e32 v125, v88, v89
	v_add_f32_e32 v122, 0, v122
	v_add_f32_e32 v124, v124, v125
	v_add_f32_e32 v122, v124, v122
	v_mul_f32_e32 v124, v87, v87
	v_mul_f32_e32 v125, v89, v89
	v_fmac_f32_e32 v124, v86, v86
	v_fmac_f32_e32 v125, v88, v88
	v_add_f32_e32 v124, v124, v125
	v_add_f32_e32 v123, v123, v124
	v_add_f32_e32 v124, v18, v19
	v_add_f32_e32 v125, v20, v21
	v_add_f32_e32 v124, v124, v125
	v_add_f32_e32 v122, v124, v122
	v_mul_f32_e32 v124, v19, v19
	v_mul_f32_e32 v125, v21, v21
	v_fmac_f32_e32 v124, v18, v18
	v_fmac_f32_e32 v125, v20, v20
	v_add_f32_e32 v124, v124, v125
	v_add_f32_e32 v123, v124, v123
	v_add_f32_e32 v124, v22, v23
	v_add_f32_e32 v125, v24, v25
	v_add_f32_e32 v124, v124, v125
	v_add_f32_e32 v122, v124, v122
	v_mul_f32_e32 v124, v23, v23
	v_mul_f32_e32 v125, v25, v25
	v_fmac_f32_e32 v124, v22, v22
	v_fmac_f32_e32 v125, v24, v24
	v_add_f32_e32 v124, v124, v125
	v_add_f32_e32 v124, v124, v123
	ds_swizzle_b32 v123, v122 offset:swizzle(SWAP,16)
	ds_swizzle_b32 v125, v124 offset:swizzle(SWAP,16)
	s_waitcnt lgkmcnt(1)
	v_add_f32_e32 v123, v122, v123
	s_waitcnt lgkmcnt(0)
	v_add_f32_e32 v122, v124, v125
	v_mov_b32_e32 v125, v123
	v_mov_b32_e32 v124, v122
	s_nop 0
	v_permlane32_swap_b32_e32 v123, v125
	v_permlane32_swap_b32_e32 v122, v124
	s_and_saveexec_b64 s[6:7], vcc
	s_cbranch_execz .LBB0_1860
	v_add_f32_e32 v122, v122, v124
	v_add_f32_e32 v123, v123, v125
	s_lshl_b32 s18, s22, 11
	v_mul_f32_e32 v124, 0x3c800000, v123
	v_fma_f32 v122, -v123, v124, v122
	s_add_i32 s18, s5, s18
	v_max_f32_e32 v125, 0, v122
	v_lshl_add_u32 v122, v0, 5, s18
	ds_write_b64 v122, v[124:125] offset:4608
.LBB0_1860:
	s_or_b64 exec, exec, s[6:7]
	v_add_f32_e32 v122, v74, v75
	v_add_f32_e32 v123, v76, v77
	v_add_f32_e32 v122, v122, v123
	v_mul_f32_e32 v123, v75, v75
	v_mul_f32_e32 v124, v77, v77
	v_fmac_f32_e32 v123, v74, v74
	v_fmac_f32_e32 v124, v76, v76
	v_add_f32_e32 v123, v123, v124
	v_add_f32_e32 v124, v78, v79
	v_add_f32_e32 v125, v80, v81
	v_add_f32_e32 v122, 0, v122
	v_add_f32_e32 v124, v124, v125
	v_add_f32_e32 v122, v124, v122
	v_mul_f32_e32 v124, v79, v79
	v_mul_f32_e32 v125, v81, v81
	v_fmac_f32_e32 v124, v78, v78
	v_fmac_f32_e32 v125, v80, v80
	v_add_f32_e32 v124, v124, v125
	v_add_f32_e32 v123, v123, v124
	v_add_f32_e32 v124, v10, v11
	v_add_f32_e32 v125, v12, v13
	v_add_f32_e32 v124, v124, v125
	v_add_f32_e32 v122, v124, v122
	v_mul_f32_e32 v124, v11, v11
	v_mul_f32_e32 v125, v13, v13
	v_fmac_f32_e32 v124, v10, v10
	v_fmac_f32_e32 v125, v12, v12
	v_add_f32_e32 v124, v124, v125
	v_add_f32_e32 v123, v124, v123
	v_add_f32_e32 v124, v14, v15
	v_add_f32_e32 v125, v16, v17
	v_add_f32_e32 v124, v124, v125
	v_add_f32_e32 v122, v124, v122
	v_mul_f32_e32 v124, v15, v15
	v_mul_f32_e32 v125, v17, v17
	v_fmac_f32_e32 v124, v14, v14
	v_fmac_f32_e32 v125, v16, v16
	v_add_f32_e32 v124, v124, v125
	v_add_f32_e32 v124, v124, v123
	ds_swizzle_b32 v123, v122 offset:swizzle(SWAP,16)
	ds_swizzle_b32 v125, v124 offset:swizzle(SWAP,16)
	s_waitcnt lgkmcnt(1)
	v_add_f32_e32 v123, v122, v123
	s_waitcnt lgkmcnt(0)
	v_add_f32_e32 v122, v124, v125
	v_mov_b32_e32 v125, v123
	v_mov_b32_e32 v124, v122
	s_nop 0
	v_permlane32_swap_b32_e32 v123, v125
	v_permlane32_swap_b32_e32 v122, v124
	s_and_saveexec_b64 s[6:7], vcc
	s_cbranch_execz .LBB0_1862
	v_add_f32_e32 v122, v122, v124
	v_add_f32_e32 v123, v123, v125
	s_lshl_b32 s18, s22, 11
	v_mul_f32_e32 v124, 0x3c800000, v123
	v_fma_f32 v122, -v123, v124, v122
	s_add_i32 s18, s5, s18
	v_max_f32_e32 v125, 0, v122
	v_lshl_add_u32 v122, v0, 5, s18
	ds_write_b64 v122, v[124:125] offset:5120
.LBB0_1862:
	s_or_b64 exec, exec, s[6:7]
	v_add_f32_e32 v122, v66, v67
	v_add_f32_e32 v123, v68, v69
	v_add_f32_e32 v122, v122, v123
	v_mul_f32_e32 v123, v67, v67
	v_mul_f32_e32 v124, v69, v69
	v_fmac_f32_e32 v123, v66, v66
	v_fmac_f32_e32 v124, v68, v68
	v_add_f32_e32 v123, v123, v124
	v_add_f32_e32 v124, v70, v71
	v_add_f32_e32 v125, v72, v73
	v_add_f32_e32 v122, 0, v122
	v_add_f32_e32 v124, v124, v125
	v_add_f32_e32 v122, v124, v122
	v_mul_f32_e32 v124, v71, v71
	v_mul_f32_e32 v125, v73, v73
	v_fmac_f32_e32 v124, v70, v70
	v_fmac_f32_e32 v125, v72, v72
	v_add_f32_e32 v124, v124, v125
	v_add_f32_e32 v123, v123, v124
	v_add_f32_e32 v124, v2, v3
	v_add_f32_e32 v125, v4, v5
	v_add_f32_e32 v124, v124, v125
	v_add_f32_e32 v122, v124, v122
	v_mul_f32_e32 v124, v3, v3
	v_mul_f32_e32 v125, v5, v5
	v_fmac_f32_e32 v124, v2, v2
	v_fmac_f32_e32 v125, v4, v4
	v_add_f32_e32 v124, v124, v125
	v_add_f32_e32 v123, v124, v123
	v_add_f32_e32 v124, v6, v7
	v_add_f32_e32 v125, v8, v9
	v_add_f32_e32 v124, v124, v125
	v_add_f32_e32 v122, v124, v122
	v_mul_f32_e32 v124, v7, v7
	v_mul_f32_e32 v125, v9, v9
	v_fmac_f32_e32 v124, v6, v6
	v_fmac_f32_e32 v125, v8, v8
	v_add_f32_e32 v124, v124, v125
	v_add_f32_e32 v124, v124, v123
	ds_swizzle_b32 v123, v122 offset:swizzle(SWAP,16)
	ds_swizzle_b32 v125, v124 offset:swizzle(SWAP,16)
	s_waitcnt lgkmcnt(1)
	v_add_f32_e32 v123, v122, v123
	s_waitcnt lgkmcnt(0)
	v_add_f32_e32 v122, v124, v125
	v_mov_b32_e32 v125, v123
	v_mov_b32_e32 v124, v122
	s_nop 0
	v_permlane32_swap_b32_e32 v123, v125
	v_permlane32_swap_b32_e32 v122, v124
	s_and_saveexec_b64 s[6:7], vcc
	s_cbranch_execz .LBB0_1864
	v_add_f32_e32 v122, v122, v124
	v_add_f32_e32 v123, v123, v125
	s_lshl_b32 s18, s22, 11
	v_mul_f32_e32 v124, 0x3c800000, v123
	v_fma_f32 v122, -v123, v124, v122
	s_add_i32 s5, s5, s18
	v_max_f32_e32 v125, 0, v122
	v_lshl_add_u32 v0, v0, 5, s5
	ds_write_b64 v0, v[124:125] offset:5632
.LBB0_1864:
	s_or_b64 exec, exec, s[6:7]
	v_or_b32_e32 v0, s1, v250
	v_cmp_eq_u32_e32 vcc, 0, v0
	s_and_saveexec_b64 s[6:7], vcc
	ds_write_b32 v1, v1 offset:10240
	s_or_b64 exec, exec, s[6:7]
	s_waitcnt lgkmcnt(0)
	s_barrier
	v_cmp_gt_i32_e32 vcc, 32, v250
	s_and_saveexec_b64 s[6:7], vcc
	s_cbranch_execz .LBB0_1877
	s_lshl_b32 s1, s1, 5
	v_and_or_b32 v122, v250, 31, s1
	v_lshl_add_u32 v0, v122, 5, 0
	ds_read_b128 v[124:127], v0
	ds_read_b128 v[138:141], v0 offset:16
	s_ashr_i32 s1, s0, 31
	s_lshl_b64 s[0:1], s[0:1], 14
	s_add_u32 s0, s26, s0
	s_waitcnt lgkmcnt(1)
	v_add_f32_e32 v123, v124, v126
	s_waitcnt lgkmcnt(0)
	v_add_f32_e32 v123, v123, v138
	v_add_f32_e32 v123, v123, v140
	v_fmamk_f32 v124, v123, 0xbe800000, v124
	v_fmac_f32_e32 v126, 0xbe800000, v123
	v_fmamk_f32 v128, v123, 0xbe800000, v138
	v_fmac_f32_e32 v140, 0xbe800000, v123
	v_mul_f32_e32 v129, v124, v124
	v_mul_f32_e32 v145, v126, v126
	v_mul_f32_e32 v147, v128, v128
	v_mul_f32_e32 v149, v140, v140
	v_mov_b32_e32 v128, v125
	v_mov_b32_e32 v144, v127
	v_mov_b32_e32 v146, v139
	v_mov_b32_e32 v148, v141
	v_add_f32_e32 v124, v128, v144
	v_add_f32_e32 v125, v129, v145
	v_add_f32_e32 v126, v146, v148
	v_add_f32_e32 v127, v147, v149
	v_mul_f32_e32 v142, 0x3e800000, v123
	v_add_f32_e32 v124, v124, v126
	v_add_f32_e32 v125, v125, v127
	s_addc_u32 s1, s27, s1
	v_fmac_f32_e32 v124, 0x42800000, v125
	v_ashrrev_i32_e32 v123, 31, v122
	v_lshl_add_u64 v[128:129], v[122:123], 3, s[0:1]
	s_ashr_i32 s5, s4, 31
	v_and_b32_e32 v123, 0xffffffe0, v124
	s_mov_b64 s[0:1], 0x1000
	v_lshl_add_u64 v[126:127], s[4:5], 3, v[128:129]
	v_or_b32_e32 v143, s25, v123
	v_lshl_add_u64 v[140:141], v[128:129], 0, s[0:1]
	s_mov_b64 s[0:1], 0x1800
	global_store_dwordx2 v[126:127], v[142:143], off sc1
	s_memrealtime s[18:19]
	v_lshl_add_u64 v[142:143], v[128:129], 0, s[0:1]
	s_mov_b64 s[0:1], 0x2000
	v_lshl_add_u64 v[146:147], v[128:129], 0, s[0:1]
	s_mov_b64 s[0:1], 0x2800
	v_lshl_add_u64 v[148:149], v[128:129], 0, s[0:1]
	s_mov_b64 s[0:1], 0x3000
	v_lshl_add_u64 v[150:151], v[128:129], 0, s[0:1]
	s_mov_b64 s[0:1], 0x3800
	v_lshl_add_u64 v[152:153], v[128:129], 0, s[0:1]
	s_mov_b64 s[4:5], 0
	s_branch .LBB0_1870
